# GEMM unit loops (five of six sites): first K-loop trip peeled with srcC=0 on each accumulator's first MFMA, so the 157-instruction per-unit accumulator zeroing ladder is deleted
# baseline (speedup 1.0000x reference)
; #define ZERO4() ((f32x4){opaque0(), 0.f, 0.f, 0.f} * 0.f)
; template <class Epi, class Sched, bool GATHER = false>
; __device__ __forceinline__ void gemm_phase(LAS unsigned char* lds, const Gemm g, const Sched& S, const Epi& E, const int tid) {
;     ...
;     f32x4 acc[2][2][4][2];
; #pragma unroll
;     for (int a = 0; a < 2; ++a)
; #pragma unroll
;         for (int b = 0; b < 2; ++b)
; #pragma unroll
;             for (int m = 0; m < 4; ++m)
; #pragma unroll
;                 for (int n = 0; n < 2; ++n) acc[a][b][m][n] = ZERO4();
.LBB0_242:
	v_mov_b32_e32 v4, v3
	v_mov_b32_e32 v5, v3
	v_mul_f32_e32 v2, 0, v2
	s_mov_b64 s[4:5], 0

; #define LAS __attribute__((address_space(3)))
;     __device__ __forceinline__ bool next(int i, Unit& u) const { if (i >= per * reps) return false; return StaticOrder::next(i % per, u); }
; #define PG8_STAGE_A(bufoff, base_, nx_, kb_, h_) do { if (GATHER) { if (nx_) PG8_STAGE_G(bufoff, kb_, goN, h_); else PG8_STAGE_G(bufoff, kb_, goC, h_); } \
;         else PG8_STAGE(bufoff, (base_) + (kb_) + (h_) * hstep, voffA); } while (0)
; #define PG8_STAGE(bufoff, gbase, voff) do { _Pragma("unroll") for (int _i = 0; _i < 2; ++_i) \
;         __builtin_amdgcn_global_load_lds((const unsigned*)((const char*)(gbase) + (voff)[_i]), (LAS unsigned*)(lds + (bufoff) + ldsw + _i * 8192), 16, 0, 0); } while (0)
; #define PG8_WAIT_V(n) asm volatile("s_waitcnt vmcnt(" #n ")" ::: "memory")
; #define PG8_WAIT_L(n) asm volatile("s_waitcnt lgkmcnt(" #n ")" ::: "memory")
; template <class Epi, class Sched, bool GATHER = false>
; __device__ __forceinline__ void gemm_phase(LAS unsigned char* lds, const Gemm g, const Sched& S, const Epi& E, const int tid) {
;     ...
;         const bool has_next = S.next(ui + 1, nxt);
;         const char* nA = has_next ? (const char*)g.A + (size_t)nxt.pm * tstep : cA; const char* nB = has_next ? (const char*)g.Bt + (size_t)nxt.pb * tstep : cB;
;         if (GATHER && has_next && wid < 4) __builtin_amdgcn_global_load_lds((const unsigned*)(g.rowmap + nxt.rb + tid), (LAS unsigned*)(lds + STAGE_BYTES + ((ui + 1) & 1) * 1024 + wid * 256), 4, 0, 0);
;         for (int t = 0; t < nt; t += 2) {
;             const bool last = (t == nt - 2);
;             const char* a1 = cA + (size_t)(t + 1) * kstep;
;             const char* a2 = last ? nA : cA + (size_t)(t + 2) * kstep; const char* b2 = last ? nB : cB + (size_t)(t + 2) * kstep;
;             const char* a3 = a2 + kstep; const char* b3 = b2 + kstep;
;     ...
;             const size_t kb1 = (size_t)(t + 1) * kstep, kb2 = last ? (size_t)0 : (size_t)(t + 2) * kstep, kb3 = kb2 + kstep;
;             PG8_LDB(B0, 0, 0); PG8_LDB(B1, 0, 1); PG8_SCHED; PG8_LDA(At, 0, 0); PG8_STAGE_A(PG8_SA(1, 1), cA, false, kb1, 1);
;             PG8_WAIT_V(8); PG8_WAIT_L(0); PG8_BAR; PG8_MMA(0, 0, At, B0); PG8_MMA(0, 1, At, B1); PG8_BAR; PG8_SCHED;
;             PG8_LDA(At, 0, 1); PG8_STAGE(PG8_SB(0, 0), b2, voffB); PG8_STAGE(PG8_SB(0, 1), b2 + hstep, voffB); PG8_STAGE_A(PG8_SA(0, 0), (last ? nA : cA), last, kb2, 0);
.LBB0_246:
	s_ashr_i32 s15, s14, 31
	s_lshl_b64 s[18:19], s[14:15], 20
	s_add_u32 s18, s31, s18
	s_addc_u32 s19, s33, s19
	s_ashr_i32 s13, s12, 31
	s_lshl_b64 s[20:21], s[12:13], 20
	s_add_u32 s20, s36, s20
	s_addc_u32 s21, s37, s21
	s_and_b64 s[24:25], s[4:5], exec
	s_cselect_b32 s13, s21, s23
	s_cselect_b32 s15, s20, s22
	s_add_u32 s49, s22, 0x100
	s_addc_u32 s50, s23, 0
	s_add_u32 s22, s16, 0x80080
	s_addc_u32 s23, s17, 0
	v_lshl_add_u64 v[4:5], s[22:23], 0, v[142:143]
	v_lshl_add_u64 v[146:147], s[22:23], 0, v[144:145]
	s_mov_b32 s51, -2
	s_mov_b64 s[28:29], 0
	s_add_u32 s22, s28, 0x100
	s_addc_u32 s23, s29, 0
	s_add_u32 s54, s49, s28
	s_addc_u32 s55, s50, s29
	s_add_i32 s24, 0, 0x10000
	s_add_i32 s56, 0, 0x14000
	v_add_u32_e32 v2, s24, v1
	ds_read_b128 v[152:155], v2
	ds_read_b128 v[156:159], v2 offset:1024
	ds_read_b128 v[160:163], v2 offset:2048
	ds_read_b128 v[164:167], v2 offset:3072
	v_add_u32_e32 v2, s56, v1
	ds_read_b128 v[168:171], v2
	ds_read_b128 v[172:175], v2 offset:1024
	ds_read_b128 v[176:179], v2 offset:2048
	ds_read_b128 v[180:183], v2 offset:3072
	s_add_i32 s58, s24, s38
	s_add_i32 m0, s11, 0xc000
	s_add_i32 s57, s11, 0xe000
	s_add_i32 s59, s58, 0x2000
	s_cmp_eq_u32 s51, 28
	s_cselect_b64 s[52:53], -1, 0
	s_and_b64 s[24:25], s[52:53], exec
	s_cselect_b32 s25, s13, s55
	s_cselect_b32 s24, s15, s54
	v_lshl_add_u64 v[218:219], v[4:5], 0, s[28:29]
	ds_read_b128 v[184:187], v150
	ds_read_b128 v[188:191], v150 offset:1024
	ds_read_b128 v[192:195], v150 offset:2048
	ds_read_b128 v[196:199], v150 offset:3072
	ds_read_b128 v[202:205], v150 offset:4096
	ds_read_b128 v[206:209], v150 offset:5120
	ds_read_b128 v[210:213], v150 offset:6144
	ds_read_b128 v[214:217], v150 offset:7168
	global_load_lds_dwordx4 v[218:219], off
	v_lshl_add_u64 v[218:219], v[146:147], 0, s[28:29]
	s_mov_b32 m0, s57
	s_nop 0
	global_load_lds_dwordx4 v[218:219], off
	s_waitcnt vmcnt(8)
	s_waitcnt lgkmcnt(0)
	s_barrier
	s_waitcnt lgkmcnt(0)
	v_mfma_f32_16x16x32_bf16 v[14:17], v[152:155], v[184:187], 0
	v_mfma_f32_16x16x32_bf16 v[10:13], v[160:163], v[184:187], 0
	v_mfma_f32_16x16x32_bf16 v[6:9], v[152:155], v[192:195], 0
	v_mfma_f32_16x16x32_bf16 v[18:21], v[160:163], v[192:195], 0
	v_mfma_f32_16x16x32_bf16 v[22:25], v[152:155], v[202:205], 0
	v_mfma_f32_16x16x32_bf16 v[34:37], v[160:163], v[202:205], 0
	v_mfma_f32_16x16x32_bf16 v[26:29], v[152:155], v[210:213], 0
	v_mfma_f32_16x16x32_bf16 v[30:33], v[160:163], v[210:213], 0
	v_mfma_f32_16x16x32_bf16 v[14:17], v[156:159], v[188:191], v[14:17]
	v_mfma_f32_16x16x32_bf16 v[10:13], v[164:167], v[188:191], v[10:13]
	v_mfma_f32_16x16x32_bf16 v[6:9], v[156:159], v[196:199], v[6:9]
	v_mfma_f32_16x16x32_bf16 v[18:21], v[164:167], v[196:199], v[18:21]
	v_mfma_f32_16x16x32_bf16 v[22:25], v[156:159], v[206:209], v[22:25]
	v_mfma_f32_16x16x32_bf16 v[34:37], v[164:167], v[206:209], v[34:37]
	v_mfma_f32_16x16x32_bf16 v[26:29], v[156:159], v[214:217], v[26:29]
	v_mfma_f32_16x16x32_bf16 v[30:33], v[164:167], v[214:217], v[30:33]
	v_mfma_f32_16x16x32_bf16 v[66:69], v[168:171], v[184:187], 0
	v_mfma_f32_16x16x32_bf16 v[98:101], v[176:179], v[184:187], 0
	v_mfma_f32_16x16x32_bf16 v[62:65], v[168:171], v[192:195], 0
	v_mfma_f32_16x16x32_bf16 v[94:97], v[176:179], v[192:195], 0
	v_mfma_f32_16x16x32_bf16 v[58:61], v[168:171], v[202:205], 0
	v_mfma_f32_16x16x32_bf16 v[90:93], v[176:179], v[202:205], 0
	v_mfma_f32_16x16x32_bf16 v[54:57], v[168:171], v[210:213], 0
	v_mfma_f32_16x16x32_bf16 v[86:89], v[176:179], v[210:213], 0
	v_mfma_f32_16x16x32_bf16 v[66:69], v[172:175], v[188:191], v[66:69]
	v_mfma_f32_16x16x32_bf16 v[98:101], v[180:183], v[188:191], v[98:101]
	v_mfma_f32_16x16x32_bf16 v[62:65], v[172:175], v[196:199], v[62:65]
	v_mfma_f32_16x16x32_bf16 v[94:97], v[180:183], v[196:199], v[94:97]
	v_mfma_f32_16x16x32_bf16 v[58:61], v[172:175], v[206:209], v[58:61]
	v_mfma_f32_16x16x32_bf16 v[90:93], v[180:183], v[206:209], v[90:93]
	v_mfma_f32_16x16x32_bf16 v[54:57], v[172:175], v[214:217], v[54:57]
	v_mfma_f32_16x16x32_bf16 v[86:89], v[180:183], v[214:217], v[86:89]
	s_barrier
	s_mov_b32 m0, s58
	v_lshl_add_u64 v[218:219], s[24:25], 0, v[138:139]
	s_cselect_b32 s54, 0, s23
	s_cselect_b32 s55, 0, s22
	s_add_u32 s28, s24, 0x80000
	ds_read_b128 v[184:187], v150 offset:16384
	ds_read_b128 v[188:191], v150 offset:17408
	ds_read_b128 v[192:195], v150 offset:18432
	ds_read_b128 v[196:199], v150 offset:19456
	ds_read_b128 v[202:205], v150 offset:20480
	ds_read_b128 v[206:209], v150 offset:21504
	ds_read_b128 v[210:213], v150 offset:22528
	ds_read_b128 v[214:217], v150 offset:23552
	global_load_lds_dwordx4 v[218:219], off
	v_lshl_add_u64 v[220:221], s[24:25], 0, v[134:135]
	s_mov_b32 m0, s59
	s_addc_u32 s29, s25, 0
	s_add_i32 s56, s56, s38
	global_load_lds_dwordx4 v[220:221], off
	v_lshl_add_u64 v[222:223], s[28:29], 0, v[138:139]
	s_mov_b32 m0, s56
	s_nop 0
	global_load_lds_dwordx4 v[222:223], off
	v_lshl_add_u64 v[222:223], s[28:29], 0, v[134:135]
	s_add_i32 m0, s56, 0x2000
	s_and_b64 s[28:29], s[52:53], s[4:5]
	s_and_b64 s[28:29], s[28:29], exec
	s_cselect_b32 s28, s18, s16
	s_cselect_b32 s29, s19, s17
	s_add_u32 s28, s28, s55
	s_addc_u32 s29, s29, s54
	global_load_lds_dwordx4 v[222:223], off
	v_lshl_add_u64 v[222:223], s[28:29], 0, v[140:141]
	s_mov_b32 m0, s11
	v_lshl_add_u64 v[224:225], s[28:29], 0, v[136:137]
	global_load_lds_dwordx4 v[222:223], off
	s_mov_b32 m0, s40
	s_nop 0
	global_load_lds_dwordx4 v[224:225], off
	s_waitcnt vmcnt(8)
	s_waitcnt lgkmcnt(0)
	s_barrier
; #define PG8_STAGE_A(bufoff, base_, nx_, kb_, h_) do { if (GATHER) { if (nx_) PG8_STAGE_G(bufoff, kb_, goN, h_); else PG8_STAGE_G(bufoff, kb_, goC, h_); } \
;         else PG8_STAGE(bufoff, (base_) + (kb_) + (h_) * hstep, voffA); } while (0)
; #define PG8_LDA(dst, b, h) do { _Pragma("unroll") for (int m = 0; m < 4; ++m) _Pragma("unroll") for (int k = 0; k < 2; ++k) dst[m][k] = *(const LAS bf16x8*)(lds + PG8_SA(b, h) + aoff + m * 2048 + k * 1024); } while (0)
; #define PG8_LDB(dst, b, h) do { _Pragma("unroll") for (int n = 0; n < 2; ++n) _Pragma("unroll") for (int k = 0; k < 2; ++k) dst[n][k] = *(const LAS bf16x8*)(lds + PG8_SB(b, h) + boff + n * 2048 + k * 1024); } while (0)
; #define PG8_MMA(ai, bj, At, Bt) do { __builtin_amdgcn_s_setprio(1); _Pragma("unroll") for (int m = 0; m < 4; ++m) _Pragma("unroll") for (int n = 0; n < 2; ++n) _Pragma("unroll") for (int k = 0; k < 2; ++k) \
;         acc[ai][bj][m][n] = __builtin_amdgcn_mfma_f32_16x16x32_bf16(Bt[n][k], At[m][k], acc[ai][bj][m][n], 0, 0, 0); __builtin_amdgcn_s_setprio(0); } while (0)
; #define PG8_WAIT_V(n) asm volatile("s_waitcnt vmcnt(" #n ")" ::: "memory")
; #define PG8_WAIT_L(n) asm volatile("s_waitcnt lgkmcnt(" #n ")" ::: "memory")
; #define PG8_BAR __builtin_amdgcn_s_barrier()
; #define PG8_SCHED __builtin_amdgcn_sched_barrier(0)
; template <class Epi, class Sched, bool GATHER = false>
; __device__ __forceinline__ void gemm_phase(LAS unsigned char* lds, const Gemm g, const Sched& S, const Epi& E, const int tid) {
;     ...
;             PG8_WAIT_V(8); PG8_WAIT_L(0); PG8_BAR; PG8_MMA(1, 0, At, B0); PG8_MMA(1, 1, At, B1); PG8_BAR; PG8_SCHED;
;             PG8_LDB(B0, 1, 0); PG8_LDB(B1, 1, 1); PG8_SCHED; PG8_LDA(At, 1, 0); PG8_STAGE_A(PG8_SA(0, 1), (last ? nA : cA), last, kb2, 1);
;             PG8_WAIT_V(8); PG8_WAIT_L(0); PG8_BAR; PG8_MMA(0, 0, At, B0); PG8_MMA(0, 1, At, B1); PG8_BAR; PG8_SCHED;
	s_waitcnt lgkmcnt(0)
	v_mfma_f32_16x16x32_bf16 v[50:53], v[152:155], v[184:187], 0
	v_mfma_f32_16x16x32_bf16 v[82:85], v[160:163], v[184:187], 0
	v_mfma_f32_16x16x32_bf16 v[46:49], v[152:155], v[192:195], 0
	v_mfma_f32_16x16x32_bf16 v[78:81], v[160:163], v[192:195], 0
	v_mfma_f32_16x16x32_bf16 v[42:45], v[152:155], v[202:205], 0
	v_mfma_f32_16x16x32_bf16 v[74:77], v[160:163], v[202:205], 0
	v_mfma_f32_16x16x32_bf16 v[38:41], v[152:155], v[210:213], 0
	v_mfma_f32_16x16x32_bf16 v[70:73], v[160:163], v[210:213], 0
	v_mfma_f32_16x16x32_bf16 v[50:53], v[156:159], v[188:191], v[50:53]
	v_mfma_f32_16x16x32_bf16 v[82:85], v[164:167], v[188:191], v[82:85]
	v_mfma_f32_16x16x32_bf16 v[46:49], v[156:159], v[196:199], v[46:49]
	v_mfma_f32_16x16x32_bf16 v[78:81], v[164:167], v[196:199], v[78:81]
	v_mfma_f32_16x16x32_bf16 v[42:45], v[156:159], v[206:209], v[42:45]
	v_mfma_f32_16x16x32_bf16 v[74:77], v[164:167], v[206:209], v[74:77]
	v_mfma_f32_16x16x32_bf16 v[38:41], v[156:159], v[214:217], v[38:41]
	v_mfma_f32_16x16x32_bf16 v[70:73], v[164:167], v[214:217], v[70:73]
	v_mfma_f32_16x16x32_bf16 v[114:117], v[168:171], v[184:187], 0
	v_mfma_f32_16x16x32_bf16 v[130:133], v[176:179], v[184:187], 0
	v_mfma_f32_16x16x32_bf16 v[110:113], v[168:171], v[192:195], 0
	v_mfma_f32_16x16x32_bf16 v[126:129], v[176:179], v[192:195], 0
	v_mfma_f32_16x16x32_bf16 v[106:109], v[168:171], v[202:205], 0
	v_mfma_f32_16x16x32_bf16 v[122:125], v[176:179], v[202:205], 0
	v_mfma_f32_16x16x32_bf16 v[102:105], v[168:171], v[210:213], 0
	v_mfma_f32_16x16x32_bf16 v[118:121], v[176:179], v[210:213], 0
	v_mfma_f32_16x16x32_bf16 v[114:117], v[172:175], v[188:191], v[114:117]
	v_mfma_f32_16x16x32_bf16 v[130:133], v[180:183], v[188:191], v[130:133]
	v_mfma_f32_16x16x32_bf16 v[110:113], v[172:175], v[196:199], v[110:113]
	v_mfma_f32_16x16x32_bf16 v[126:129], v[180:183], v[196:199], v[126:129]
	v_mfma_f32_16x16x32_bf16 v[106:109], v[172:175], v[206:209], v[106:109]
	v_mfma_f32_16x16x32_bf16 v[122:125], v[180:183], v[206:209], v[122:125]
	v_mfma_f32_16x16x32_bf16 v[102:105], v[172:175], v[214:217], v[102:105]
	v_mfma_f32_16x16x32_bf16 v[118:121], v[180:183], v[214:217], v[118:121]
	s_barrier
	s_add_i32 s52, 0, 0x18000
	v_add_u32_e32 v2, s52, v1
	s_add_i32 s53, 0, 0x1c000
	ds_read_b128 v[152:155], v2
	ds_read_b128 v[156:159], v2 offset:1024
	ds_read_b128 v[160:163], v2 offset:2048
	ds_read_b128 v[164:167], v2 offset:3072
	v_add_u32_e32 v2, s53, v1
	ds_read_b128 v[168:171], v2
	ds_read_b128 v[172:175], v2 offset:1024
	ds_read_b128 v[176:179], v2 offset:2048
	ds_read_b128 v[180:183], v2 offset:3072
	s_add_u32 s28, s28, 0x80000
	s_addc_u32 s29, s29, 0
	s_mov_b32 m0, s41
	v_lshl_add_u64 v[226:227], s[28:29], 0, v[140:141]
	ds_read_b128 v[184:187], v150 offset:32768
	ds_read_b128 v[188:191], v150 offset:33792
	ds_read_b128 v[192:195], v150 offset:34816
	ds_read_b128 v[196:199], v150 offset:35840
	ds_read_b128 v[202:205], v150 offset:36864
	ds_read_b128 v[206:209], v150 offset:37888
	ds_read_b128 v[210:213], v150 offset:38912
	ds_read_b128 v[214:217], v150 offset:39936
	global_load_lds_dwordx4 v[226:227], off
	v_lshl_add_u64 v[226:227], s[28:29], 0, v[136:137]
	s_mov_b32 m0, s42
	s_nop 0
	global_load_lds_dwordx4 v[226:227], off
	s_waitcnt vmcnt(8)
	s_waitcnt lgkmcnt(0)
	s_barrier
	s_waitcnt lgkmcnt(0)
	v_mfma_f32_16x16x32_bf16 v[14:17], v[152:155], v[184:187], v[14:17]
	v_mfma_f32_16x16x32_bf16 v[10:13], v[160:163], v[184:187], v[10:13]
	v_mfma_f32_16x16x32_bf16 v[6:9], v[152:155], v[192:195], v[6:9]
	v_mfma_f32_16x16x32_bf16 v[18:21], v[160:163], v[192:195], v[18:21]
	v_mfma_f32_16x16x32_bf16 v[22:25], v[152:155], v[202:205], v[22:25]
	v_mfma_f32_16x16x32_bf16 v[34:37], v[160:163], v[202:205], v[34:37]
	v_mfma_f32_16x16x32_bf16 v[26:29], v[152:155], v[210:213], v[26:29]
	v_mfma_f32_16x16x32_bf16 v[30:33], v[160:163], v[210:213], v[30:33]
	v_mfma_f32_16x16x32_bf16 v[14:17], v[156:159], v[188:191], v[14:17]
	v_mfma_f32_16x16x32_bf16 v[10:13], v[164:167], v[188:191], v[10:13]
	v_mfma_f32_16x16x32_bf16 v[6:9], v[156:159], v[196:199], v[6:9]
	v_mfma_f32_16x16x32_bf16 v[18:21], v[164:167], v[196:199], v[18:21]
	v_mfma_f32_16x16x32_bf16 v[22:25], v[156:159], v[206:209], v[22:25]
	v_mfma_f32_16x16x32_bf16 v[34:37], v[164:167], v[206:209], v[34:37]
	v_mfma_f32_16x16x32_bf16 v[26:29], v[156:159], v[214:217], v[26:29]
	v_mfma_f32_16x16x32_bf16 v[30:33], v[164:167], v[214:217], v[30:33]
	v_mfma_f32_16x16x32_bf16 v[66:69], v[168:171], v[184:187], v[66:69]
	v_mfma_f32_16x16x32_bf16 v[98:101], v[176:179], v[184:187], v[98:101]
	v_mfma_f32_16x16x32_bf16 v[62:65], v[168:171], v[192:195], v[62:65]
	v_mfma_f32_16x16x32_bf16 v[94:97], v[176:179], v[192:195], v[94:97]
	v_mfma_f32_16x16x32_bf16 v[58:61], v[168:171], v[202:205], v[58:61]
	v_mfma_f32_16x16x32_bf16 v[90:93], v[176:179], v[202:205], v[90:93]
	v_mfma_f32_16x16x32_bf16 v[54:57], v[168:171], v[210:213], v[54:57]
	v_mfma_f32_16x16x32_bf16 v[86:89], v[176:179], v[210:213], v[86:89]
	v_mfma_f32_16x16x32_bf16 v[66:69], v[172:175], v[188:191], v[66:69]
	v_mfma_f32_16x16x32_bf16 v[98:101], v[180:183], v[188:191], v[98:101]
	v_mfma_f32_16x16x32_bf16 v[62:65], v[172:175], v[196:199], v[62:65]
	v_mfma_f32_16x16x32_bf16 v[94:97], v[180:183], v[196:199], v[94:97]
	v_mfma_f32_16x16x32_bf16 v[58:61], v[172:175], v[206:209], v[58:61]
	v_mfma_f32_16x16x32_bf16 v[90:93], v[180:183], v[206:209], v[90:93]
	v_mfma_f32_16x16x32_bf16 v[54:57], v[172:175], v[214:217], v[54:57]
	v_mfma_f32_16x16x32_bf16 v[86:89], v[180:183], v[214:217], v[86:89]
	s_barrier
; #define PG8_STAGE_A(bufoff, base_, nx_, kb_, h_) do { if (GATHER) { if (nx_) PG8_STAGE_G(bufoff, kb_, goN, h_); else PG8_STAGE_G(bufoff, kb_, goC, h_); } \
;         else PG8_STAGE(bufoff, (base_) + (kb_) + (h_) * hstep, voffA); } while (0)
; #define PG8_STAGE(bufoff, gbase, voff) do { _Pragma("unroll") for (int _i = 0; _i < 2; ++_i) \
;         __builtin_amdgcn_global_load_lds((const unsigned*)((const char*)(gbase) + (voff)[_i]), (LAS unsigned*)(lds + (bufoff) + ldsw + _i * 8192), 16, 0, 0); } while (0)
; #define PG8_LDA(dst, b, h) do { _Pragma("unroll") for (int m = 0; m < 4; ++m) _Pragma("unroll") for (int k = 0; k < 2; ++k) dst[m][k] = *(const LAS bf16x8*)(lds + PG8_SA(b, h) + aoff + m * 2048 + k * 1024); } while (0)
; #define PG8_LDB(dst, b, h) do { _Pragma("unroll") for (int n = 0; n < 2; ++n) _Pragma("unroll") for (int k = 0; k < 2; ++k) dst[n][k] = *(const LAS bf16x8*)(lds + PG8_SB(b, h) + boff + n * 2048 + k * 1024); } while (0)
; #define PG8_MMA(ai, bj, At, Bt) do { __builtin_amdgcn_s_setprio(1); _Pragma("unroll") for (int m = 0; m < 4; ++m) _Pragma("unroll") for (int n = 0; n < 2; ++n) _Pragma("unroll") for (int k = 0; k < 2; ++k) \
;         acc[ai][bj][m][n] = __builtin_amdgcn_mfma_f32_16x16x32_bf16(Bt[n][k], At[m][k], acc[ai][bj][m][n], 0, 0, 0); __builtin_amdgcn_s_setprio(0); } while (0)
; #define PG8_WAIT_V(n) asm volatile("s_waitcnt vmcnt(" #n ")" ::: "memory")
; #define PG8_WAIT_L(n) asm volatile("s_waitcnt lgkmcnt(" #n ")" ::: "memory")
; #define PG8_BAR __builtin_amdgcn_s_barrier()
; #define PG8_SCHED __builtin_amdgcn_sched_barrier(0)
; template <class Epi, class Sched, bool GATHER = false>
; __device__ __forceinline__ void gemm_phase(LAS unsigned char* lds, const Gemm g, const Sched& S, const Epi& E, const int tid) {
;     ...
;             PG8_LDB(B0, 0, 0); PG8_LDB(B1, 0, 1); PG8_SCHED; PG8_LDA(At, 0, 0); PG8_STAGE_A(PG8_SA(1, 1), cA, false, kb1, 1);
;             PG8_WAIT_V(8); PG8_WAIT_L(0); PG8_BAR; PG8_MMA(0, 0, At, B0); PG8_MMA(0, 1, At, B1); PG8_BAR; PG8_SCHED;
;     ...
;             PG8_LDA(At, 1, 1); PG8_STAGE(PG8_SB(1, 0), b3, voffB); PG8_STAGE(PG8_SB(1, 1), b3 + hstep, voffB); PG8_STAGE_A(PG8_SA(1, 0), (last ? nA : cA), last, kb3, 0);
;             PG8_WAIT_V(8); PG8_WAIT_L(0); PG8_BAR; PG8_MMA(1, 0, At, B0); PG8_MMA(1, 1, At, B1); PG8_BAR; PG8_SCHED;
;     ...
;         }
	s_add_i32 s28, s52, s38
	v_lshl_add_u64 v[218:219], v[218:219], 0, s[0:1]
	s_mov_b32 m0, s28
	ds_read_b128 v[184:187], v150 offset:49152
	ds_read_b128 v[188:191], v150 offset:50176
	ds_read_b128 v[192:195], v150 offset:51200
	ds_read_b128 v[196:199], v150 offset:52224
	ds_read_b128 v[202:205], v150 offset:53248
	ds_read_b128 v[206:209], v150 offset:54272
	ds_read_b128 v[210:213], v150 offset:55296
	ds_read_b128 v[214:217], v150 offset:56320
	global_load_lds_dwordx4 v[218:219], off
	s_add_i32 m0, s28, 0x2000
	s_add_u32 s24, s24, 0x80080
	v_lshl_add_u64 v[218:219], v[220:221], 0, s[0:1]
	s_addc_u32 s25, s25, 0
	s_add_i32 s28, s53, s38
	global_load_lds_dwordx4 v[218:219], off
	v_lshl_add_u64 v[218:219], s[24:25], 0, v[138:139]
	s_mov_b32 m0, s28
	s_nop 0
	global_load_lds_dwordx4 v[218:219], off
	v_lshl_add_u64 v[218:219], s[24:25], 0, v[134:135]
	s_add_i32 m0, s28, 0x2000
	s_nop 0
	global_load_lds_dwordx4 v[218:219], off
	v_lshl_add_u64 v[218:219], v[222:223], 0, s[0:1]
	s_mov_b32 m0, s44
	s_nop 0
	global_load_lds_dwordx4 v[218:219], off
	v_lshl_add_u64 v[218:219], v[224:225], 0, s[0:1]
	s_mov_b32 m0, s45
	s_nop 0
	global_load_lds_dwordx4 v[218:219], off
	s_waitcnt vmcnt(8)
	s_waitcnt lgkmcnt(0)
	s_barrier
	s_waitcnt lgkmcnt(0)
	v_mfma_f32_16x16x32_bf16 v[50:53], v[152:155], v[184:187], v[50:53]
	v_mfma_f32_16x16x32_bf16 v[82:85], v[160:163], v[184:187], v[82:85]
	v_mfma_f32_16x16x32_bf16 v[46:49], v[152:155], v[192:195], v[46:49]
	v_mfma_f32_16x16x32_bf16 v[78:81], v[160:163], v[192:195], v[78:81]
	v_mfma_f32_16x16x32_bf16 v[42:45], v[152:155], v[202:205], v[42:45]
	v_mfma_f32_16x16x32_bf16 v[74:77], v[160:163], v[202:205], v[74:77]
	v_mfma_f32_16x16x32_bf16 v[38:41], v[152:155], v[210:213], v[38:41]
	v_mfma_f32_16x16x32_bf16 v[70:73], v[160:163], v[210:213], v[70:73]
	v_mfma_f32_16x16x32_bf16 v[50:53], v[156:159], v[188:191], v[50:53]
	v_mfma_f32_16x16x32_bf16 v[82:85], v[164:167], v[188:191], v[82:85]
	v_mfma_f32_16x16x32_bf16 v[46:49], v[156:159], v[196:199], v[46:49]
	v_mfma_f32_16x16x32_bf16 v[78:81], v[164:167], v[196:199], v[78:81]
	v_mfma_f32_16x16x32_bf16 v[42:45], v[156:159], v[206:209], v[42:45]
	v_mfma_f32_16x16x32_bf16 v[74:77], v[164:167], v[206:209], v[74:77]
	v_mfma_f32_16x16x32_bf16 v[38:41], v[156:159], v[214:217], v[38:41]
	v_mfma_f32_16x16x32_bf16 v[70:73], v[164:167], v[214:217], v[70:73]
	v_mfma_f32_16x16x32_bf16 v[114:117], v[168:171], v[184:187], v[114:117]
	v_mfma_f32_16x16x32_bf16 v[130:133], v[176:179], v[184:187], v[130:133]
	v_mfma_f32_16x16x32_bf16 v[110:113], v[168:171], v[192:195], v[110:113]
	v_mfma_f32_16x16x32_bf16 v[126:129], v[176:179], v[192:195], v[126:129]
	v_mfma_f32_16x16x32_bf16 v[106:109], v[168:171], v[202:205], v[106:109]
	v_mfma_f32_16x16x32_bf16 v[122:125], v[176:179], v[202:205], v[122:125]
	v_mfma_f32_16x16x32_bf16 v[102:105], v[168:171], v[210:213], v[102:105]
	v_mfma_f32_16x16x32_bf16 v[118:121], v[176:179], v[210:213], v[118:121]
	v_mfma_f32_16x16x32_bf16 v[114:117], v[172:175], v[188:191], v[114:117]
	v_mfma_f32_16x16x32_bf16 v[130:133], v[180:183], v[188:191], v[130:133]
	v_mfma_f32_16x16x32_bf16 v[110:113], v[172:175], v[196:199], v[110:113]
	v_mfma_f32_16x16x32_bf16 v[126:129], v[180:183], v[196:199], v[126:129]
	v_mfma_f32_16x16x32_bf16 v[106:109], v[172:175], v[206:209], v[106:109]
	v_mfma_f32_16x16x32_bf16 v[122:125], v[180:183], v[206:209], v[122:125]
	v_mfma_f32_16x16x32_bf16 v[102:105], v[172:175], v[214:217], v[102:105]
	v_mfma_f32_16x16x32_bf16 v[118:121], v[180:183], v[214:217], v[118:121]
	s_barrier
	s_add_i32 s51, s51, 2
	s_cmp_gt_u32 s51, 29
	s_mov_b64 s[28:29], s[22:23]
	s_cbranch_scc1 .Lpeel0_exit
.LBB0_247:
	s_add_u32 s22, s28, 0x100
	s_addc_u32 s23, s29, 0
	s_add_u32 s54, s49, s28
	s_addc_u32 s55, s50, s29
	s_add_i32 s24, 0, 0x10000
	s_add_i32 s56, 0, 0x14000
	v_add_u32_e32 v2, s24, v1
	ds_read_b128 v[152:155], v2
	ds_read_b128 v[156:159], v2 offset:1024
	ds_read_b128 v[160:163], v2 offset:2048
	ds_read_b128 v[164:167], v2 offset:3072
	v_add_u32_e32 v2, s56, v1
	ds_read_b128 v[168:171], v2
	ds_read_b128 v[172:175], v2 offset:1024
	ds_read_b128 v[176:179], v2 offset:2048
	ds_read_b128 v[180:183], v2 offset:3072
	s_add_i32 s58, s24, s38
	s_add_i32 m0, s11, 0xc000
	s_add_i32 s57, s11, 0xe000
	s_add_i32 s59, s58, 0x2000
	s_cmp_eq_u32 s51, 28
	s_cselect_b64 s[52:53], -1, 0
	s_and_b64 s[24:25], s[52:53], exec
	s_cselect_b32 s25, s13, s55
	s_cselect_b32 s24, s15, s54
	v_lshl_add_u64 v[218:219], v[4:5], 0, s[28:29]
	ds_read_b128 v[184:187], v150
	ds_read_b128 v[188:191], v150 offset:1024
	ds_read_b128 v[192:195], v150 offset:2048
	ds_read_b128 v[196:199], v150 offset:3072
	ds_read_b128 v[202:205], v150 offset:4096
	ds_read_b128 v[206:209], v150 offset:5120
	ds_read_b128 v[210:213], v150 offset:6144
	ds_read_b128 v[214:217], v150 offset:7168
	global_load_lds_dwordx4 v[218:219], off
	v_lshl_add_u64 v[218:219], v[146:147], 0, s[28:29]
	s_mov_b32 m0, s57
	s_nop 0
	global_load_lds_dwordx4 v[218:219], off
	s_waitcnt vmcnt(8)
	s_waitcnt lgkmcnt(0)
	s_barrier
; #define PG8_STAGE_A(bufoff, base_, nx_, kb_, h_) do { if (GATHER) { if (nx_) PG8_STAGE_G(bufoff, kb_, goN, h_); else PG8_STAGE_G(bufoff, kb_, goC, h_); } \
;         else PG8_STAGE(bufoff, (base_) + (kb_) + (h_) * hstep, voffA); } while (0)
; #define PG8_STAGE(bufoff, gbase, voff) do { _Pragma("unroll") for (int _i = 0; _i < 2; ++_i) \
;         __builtin_amdgcn_global_load_lds((const unsigned*)((const char*)(gbase) + (voff)[_i]), (LAS unsigned*)(lds + (bufoff) + ldsw + _i * 8192), 16, 0, 0); } while (0)
; #define PG8_LDA(dst, b, h) do { _Pragma("unroll") for (int m = 0; m < 4; ++m) _Pragma("unroll") for (int k = 0; k < 2; ++k) dst[m][k] = *(const LAS bf16x8*)(lds + PG8_SA(b, h) + aoff + m * 2048 + k * 1024); } while (0)
; #define PG8_LDB(dst, b, h) do { _Pragma("unroll") for (int n = 0; n < 2; ++n) _Pragma("unroll") for (int k = 0; k < 2; ++k) dst[n][k] = *(const LAS bf16x8*)(lds + PG8_SB(b, h) + boff + n * 2048 + k * 1024); } while (0)
; #define PG8_MMA(ai, bj, At, Bt) do { __builtin_amdgcn_s_setprio(1); _Pragma("unroll") for (int m = 0; m < 4; ++m) _Pragma("unroll") for (int n = 0; n < 2; ++n) _Pragma("unroll") for (int k = 0; k < 2; ++k) \
;         acc[ai][bj][m][n] = __builtin_amdgcn_mfma_f32_16x16x32_bf16(Bt[n][k], At[m][k], acc[ai][bj][m][n], 0, 0, 0); __builtin_amdgcn_s_setprio(0); } while (0)
; #define PG8_WAIT_V(n) asm volatile("s_waitcnt vmcnt(" #n ")" ::: "memory")
; #define PG8_WAIT_L(n) asm volatile("s_waitcnt lgkmcnt(" #n ")" ::: "memory")
; #define PG8_BAR __builtin_amdgcn_s_barrier()
; template <class Epi, class Sched, bool GATHER = false>
; __device__ __forceinline__ void gemm_phase(LAS unsigned char* lds, const Gemm g, const Sched& S, const Epi& E, const int tid) {
;     ...
;             PG8_WAIT_V(8); PG8_WAIT_L(0); PG8_BAR; PG8_MMA(0, 0, At, B0); PG8_MMA(0, 1, At, B1); PG8_BAR; PG8_SCHED;
;             PG8_LDA(At, 0, 1); PG8_STAGE(PG8_SB(0, 0), b2, voffB); PG8_STAGE(PG8_SB(0, 1), b2 + hstep, voffB); PG8_STAGE_A(PG8_SA(0, 0), (last ? nA : cA), last, kb2, 0);
;             PG8_WAIT_V(8); PG8_WAIT_L(0); PG8_BAR; PG8_MMA(1, 0, At, B0); PG8_MMA(1, 1, At, B1); PG8_BAR; PG8_SCHED;
;             PG8_LDB(B0, 1, 0); PG8_LDB(B1, 1, 1); PG8_SCHED; PG8_LDA(At, 1, 0); PG8_STAGE_A(PG8_SA(0, 1), (last ? nA : cA), last, kb2, 1);
;             PG8_WAIT_V(8); PG8_WAIT_L(0); PG8_BAR; PG8_MMA(0, 0, At, B0); PG8_MMA(0, 1, At, B1); PG8_BAR; PG8_SCHED;
	s_waitcnt lgkmcnt(0)
	v_mfma_f32_16x16x32_bf16 v[14:17], v[152:155], v[184:187], v[14:17]
	v_mfma_f32_16x16x32_bf16 v[10:13], v[160:163], v[184:187], v[10:13]
	v_mfma_f32_16x16x32_bf16 v[6:9], v[152:155], v[192:195], v[6:9]
	v_mfma_f32_16x16x32_bf16 v[18:21], v[160:163], v[192:195], v[18:21]
	v_mfma_f32_16x16x32_bf16 v[22:25], v[152:155], v[202:205], v[22:25]
	v_mfma_f32_16x16x32_bf16 v[34:37], v[160:163], v[202:205], v[34:37]
	v_mfma_f32_16x16x32_bf16 v[26:29], v[152:155], v[210:213], v[26:29]
	v_mfma_f32_16x16x32_bf16 v[30:33], v[160:163], v[210:213], v[30:33]
	v_mfma_f32_16x16x32_bf16 v[14:17], v[156:159], v[188:191], v[14:17]
	v_mfma_f32_16x16x32_bf16 v[10:13], v[164:167], v[188:191], v[10:13]
	v_mfma_f32_16x16x32_bf16 v[6:9], v[156:159], v[196:199], v[6:9]
	v_mfma_f32_16x16x32_bf16 v[18:21], v[164:167], v[196:199], v[18:21]
	v_mfma_f32_16x16x32_bf16 v[22:25], v[156:159], v[206:209], v[22:25]
	v_mfma_f32_16x16x32_bf16 v[34:37], v[164:167], v[206:209], v[34:37]
	v_mfma_f32_16x16x32_bf16 v[26:29], v[156:159], v[214:217], v[26:29]
	v_mfma_f32_16x16x32_bf16 v[30:33], v[164:167], v[214:217], v[30:33]
	v_mfma_f32_16x16x32_bf16 v[66:69], v[168:171], v[184:187], v[66:69]
	v_mfma_f32_16x16x32_bf16 v[98:101], v[176:179], v[184:187], v[98:101]
	v_mfma_f32_16x16x32_bf16 v[62:65], v[168:171], v[192:195], v[62:65]
	v_mfma_f32_16x16x32_bf16 v[94:97], v[176:179], v[192:195], v[94:97]
	v_mfma_f32_16x16x32_bf16 v[58:61], v[168:171], v[202:205], v[58:61]
	v_mfma_f32_16x16x32_bf16 v[90:93], v[176:179], v[202:205], v[90:93]
	v_mfma_f32_16x16x32_bf16 v[54:57], v[168:171], v[210:213], v[54:57]
	v_mfma_f32_16x16x32_bf16 v[86:89], v[176:179], v[210:213], v[86:89]
	v_mfma_f32_16x16x32_bf16 v[66:69], v[172:175], v[188:191], v[66:69]
	v_mfma_f32_16x16x32_bf16 v[98:101], v[180:183], v[188:191], v[98:101]
	v_mfma_f32_16x16x32_bf16 v[62:65], v[172:175], v[196:199], v[62:65]
	v_mfma_f32_16x16x32_bf16 v[94:97], v[180:183], v[196:199], v[94:97]
	v_mfma_f32_16x16x32_bf16 v[58:61], v[172:175], v[206:209], v[58:61]
	v_mfma_f32_16x16x32_bf16 v[90:93], v[180:183], v[206:209], v[90:93]
	v_mfma_f32_16x16x32_bf16 v[54:57], v[172:175], v[214:217], v[54:57]
	v_mfma_f32_16x16x32_bf16 v[86:89], v[180:183], v[214:217], v[86:89]
	s_barrier
	s_mov_b32 m0, s58
	v_lshl_add_u64 v[218:219], s[24:25], 0, v[138:139]
	s_cselect_b32 s54, 0, s23
	s_cselect_b32 s55, 0, s22
	s_add_u32 s28, s24, 0x80000
	ds_read_b128 v[184:187], v150 offset:16384
	ds_read_b128 v[188:191], v150 offset:17408
	ds_read_b128 v[192:195], v150 offset:18432
	ds_read_b128 v[196:199], v150 offset:19456
	ds_read_b128 v[202:205], v150 offset:20480
	ds_read_b128 v[206:209], v150 offset:21504
	ds_read_b128 v[210:213], v150 offset:22528
	ds_read_b128 v[214:217], v150 offset:23552
	global_load_lds_dwordx4 v[218:219], off
	v_lshl_add_u64 v[220:221], s[24:25], 0, v[134:135]
	s_mov_b32 m0, s59
	s_addc_u32 s29, s25, 0
	s_add_i32 s56, s56, s38
	global_load_lds_dwordx4 v[220:221], off
	v_lshl_add_u64 v[222:223], s[28:29], 0, v[138:139]
	s_mov_b32 m0, s56
	s_nop 0
	global_load_lds_dwordx4 v[222:223], off
	v_lshl_add_u64 v[222:223], s[28:29], 0, v[134:135]
	s_add_i32 m0, s56, 0x2000
	s_and_b64 s[28:29], s[52:53], s[4:5]
	s_and_b64 s[28:29], s[28:29], exec
	s_cselect_b32 s28, s18, s16
	s_cselect_b32 s29, s19, s17
	s_add_u32 s28, s28, s55
	s_addc_u32 s29, s29, s54
	global_load_lds_dwordx4 v[222:223], off
	v_lshl_add_u64 v[222:223], s[28:29], 0, v[140:141]
	s_mov_b32 m0, s11
	v_lshl_add_u64 v[224:225], s[28:29], 0, v[136:137]
	global_load_lds_dwordx4 v[222:223], off
	s_mov_b32 m0, s40
	s_nop 0
	global_load_lds_dwordx4 v[224:225], off
	s_waitcnt vmcnt(8)
	s_waitcnt lgkmcnt(0)
	s_barrier
	s_waitcnt lgkmcnt(0)
	v_mfma_f32_16x16x32_bf16 v[50:53], v[152:155], v[184:187], v[50:53]
	v_mfma_f32_16x16x32_bf16 v[82:85], v[160:163], v[184:187], v[82:85]
	v_mfma_f32_16x16x32_bf16 v[46:49], v[152:155], v[192:195], v[46:49]
	v_mfma_f32_16x16x32_bf16 v[78:81], v[160:163], v[192:195], v[78:81]
	v_mfma_f32_16x16x32_bf16 v[42:45], v[152:155], v[202:205], v[42:45]
	v_mfma_f32_16x16x32_bf16 v[74:77], v[160:163], v[202:205], v[74:77]
	v_mfma_f32_16x16x32_bf16 v[38:41], v[152:155], v[210:213], v[38:41]
	v_mfma_f32_16x16x32_bf16 v[70:73], v[160:163], v[210:213], v[70:73]
	v_mfma_f32_16x16x32_bf16 v[50:53], v[156:159], v[188:191], v[50:53]
	v_mfma_f32_16x16x32_bf16 v[82:85], v[164:167], v[188:191], v[82:85]
	v_mfma_f32_16x16x32_bf16 v[46:49], v[156:159], v[196:199], v[46:49]
	v_mfma_f32_16x16x32_bf16 v[78:81], v[164:167], v[196:199], v[78:81]
	v_mfma_f32_16x16x32_bf16 v[42:45], v[156:159], v[206:209], v[42:45]
	v_mfma_f32_16x16x32_bf16 v[74:77], v[164:167], v[206:209], v[74:77]
	v_mfma_f32_16x16x32_bf16 v[38:41], v[156:159], v[214:217], v[38:41]
	v_mfma_f32_16x16x32_bf16 v[70:73], v[164:167], v[214:217], v[70:73]
	v_mfma_f32_16x16x32_bf16 v[114:117], v[168:171], v[184:187], v[114:117]
	v_mfma_f32_16x16x32_bf16 v[130:133], v[176:179], v[184:187], v[130:133]
	v_mfma_f32_16x16x32_bf16 v[110:113], v[168:171], v[192:195], v[110:113]
	v_mfma_f32_16x16x32_bf16 v[126:129], v[176:179], v[192:195], v[126:129]
	v_mfma_f32_16x16x32_bf16 v[106:109], v[168:171], v[202:205], v[106:109]
	v_mfma_f32_16x16x32_bf16 v[122:125], v[176:179], v[202:205], v[122:125]
	v_mfma_f32_16x16x32_bf16 v[102:105], v[168:171], v[210:213], v[102:105]
	v_mfma_f32_16x16x32_bf16 v[118:121], v[176:179], v[210:213], v[118:121]
	v_mfma_f32_16x16x32_bf16 v[114:117], v[172:175], v[188:191], v[114:117]
	v_mfma_f32_16x16x32_bf16 v[130:133], v[180:183], v[188:191], v[130:133]
	v_mfma_f32_16x16x32_bf16 v[110:113], v[172:175], v[196:199], v[110:113]
	v_mfma_f32_16x16x32_bf16 v[126:129], v[180:183], v[196:199], v[126:129]
	v_mfma_f32_16x16x32_bf16 v[106:109], v[172:175], v[206:209], v[106:109]
	v_mfma_f32_16x16x32_bf16 v[122:125], v[180:183], v[206:209], v[122:125]
	v_mfma_f32_16x16x32_bf16 v[102:105], v[172:175], v[214:217], v[102:105]
	v_mfma_f32_16x16x32_bf16 v[118:121], v[180:183], v[214:217], v[118:121]
	s_barrier
; #define PG8_STAGE_A(bufoff, base_, nx_, kb_, h_) do { if (GATHER) { if (nx_) PG8_STAGE_G(bufoff, kb_, goN, h_); else PG8_STAGE_G(bufoff, kb_, goC, h_); } \
;         else PG8_STAGE(bufoff, (base_) + (kb_) + (h_) * hstep, voffA); } while (0)
; #define PG8_STAGE(bufoff, gbase, voff) do { _Pragma("unroll") for (int _i = 0; _i < 2; ++_i) \
;         __builtin_amdgcn_global_load_lds((const unsigned*)((const char*)(gbase) + (voff)[_i]), (LAS unsigned*)(lds + (bufoff) + ldsw + _i * 8192), 16, 0, 0); } while (0)
; #define PG8_LDA(dst, b, h) do { _Pragma("unroll") for (int m = 0; m < 4; ++m) _Pragma("unroll") for (int k = 0; k < 2; ++k) dst[m][k] = *(const LAS bf16x8*)(lds + PG8_SA(b, h) + aoff + m * 2048 + k * 1024); } while (0)
; #define PG8_LDB(dst, b, h) do { _Pragma("unroll") for (int n = 0; n < 2; ++n) _Pragma("unroll") for (int k = 0; k < 2; ++k) dst[n][k] = *(const LAS bf16x8*)(lds + PG8_SB(b, h) + boff + n * 2048 + k * 1024); } while (0)
; #define PG8_MMA(ai, bj, At, Bt) do { __builtin_amdgcn_s_setprio(1); _Pragma("unroll") for (int m = 0; m < 4; ++m) _Pragma("unroll") for (int n = 0; n < 2; ++n) _Pragma("unroll") for (int k = 0; k < 2; ++k) \
;         acc[ai][bj][m][n] = __builtin_amdgcn_mfma_f32_16x16x32_bf16(Bt[n][k], At[m][k], acc[ai][bj][m][n], 0, 0, 0); __builtin_amdgcn_s_setprio(0); } while (0)
; #define PG8_WAIT_V(n) asm volatile("s_waitcnt vmcnt(" #n ")" ::: "memory")
; #define PG8_WAIT_L(n) asm volatile("s_waitcnt lgkmcnt(" #n ")" ::: "memory")
; #define PG8_BAR __builtin_amdgcn_s_barrier()
; #define PG8_SCHED __builtin_amdgcn_sched_barrier(0)
; template <class Epi, class Sched, bool GATHER = false>
; __device__ __forceinline__ void gemm_phase(LAS unsigned char* lds, const Gemm g, const Sched& S, const Epi& E, const int tid) {
;     ...
;             PG8_LDB(B0, 1, 0); PG8_LDB(B1, 1, 1); PG8_SCHED; PG8_LDA(At, 1, 0); PG8_STAGE_A(PG8_SA(0, 1), (last ? nA : cA), last, kb2, 1);
;             PG8_WAIT_V(8); PG8_WAIT_L(0); PG8_BAR; PG8_MMA(0, 0, At, B0); PG8_MMA(0, 1, At, B1); PG8_BAR; PG8_SCHED;
;             PG8_LDA(At, 1, 1); PG8_STAGE(PG8_SB(1, 0), b3, voffB); PG8_STAGE(PG8_SB(1, 1), b3 + hstep, voffB); PG8_STAGE_A(PG8_SA(1, 0), (last ? nA : cA), last, kb3, 0);
;             PG8_WAIT_V(8); PG8_WAIT_L(0); PG8_BAR; PG8_MMA(1, 0, At, B0); PG8_MMA(1, 1, At, B1); PG8_BAR; PG8_SCHED;
;     ...
;         }
	s_add_i32 s52, 0, 0x18000
	v_add_u32_e32 v2, s52, v1
	s_add_i32 s53, 0, 0x1c000
	ds_read_b128 v[152:155], v2
	ds_read_b128 v[156:159], v2 offset:1024
	ds_read_b128 v[160:163], v2 offset:2048
	ds_read_b128 v[164:167], v2 offset:3072
	v_add_u32_e32 v2, s53, v1
	ds_read_b128 v[168:171], v2
	ds_read_b128 v[172:175], v2 offset:1024
	ds_read_b128 v[176:179], v2 offset:2048
	ds_read_b128 v[180:183], v2 offset:3072
	s_add_u32 s28, s28, 0x80000
	s_addc_u32 s29, s29, 0
	s_mov_b32 m0, s41
	v_lshl_add_u64 v[226:227], s[28:29], 0, v[140:141]
	ds_read_b128 v[184:187], v150 offset:32768
	ds_read_b128 v[188:191], v150 offset:33792
	ds_read_b128 v[192:195], v150 offset:34816
	ds_read_b128 v[196:199], v150 offset:35840
	ds_read_b128 v[202:205], v150 offset:36864
	ds_read_b128 v[206:209], v150 offset:37888
	ds_read_b128 v[210:213], v150 offset:38912
	ds_read_b128 v[214:217], v150 offset:39936
	global_load_lds_dwordx4 v[226:227], off
	v_lshl_add_u64 v[226:227], s[28:29], 0, v[136:137]
	s_mov_b32 m0, s42
	s_nop 0
	global_load_lds_dwordx4 v[226:227], off
	s_waitcnt vmcnt(8)
	s_waitcnt lgkmcnt(0)
	s_barrier
	s_waitcnt lgkmcnt(0)
	v_mfma_f32_16x16x32_bf16 v[14:17], v[152:155], v[184:187], v[14:17]
	v_mfma_f32_16x16x32_bf16 v[10:13], v[160:163], v[184:187], v[10:13]
	v_mfma_f32_16x16x32_bf16 v[6:9], v[152:155], v[192:195], v[6:9]
	v_mfma_f32_16x16x32_bf16 v[18:21], v[160:163], v[192:195], v[18:21]
	v_mfma_f32_16x16x32_bf16 v[22:25], v[152:155], v[202:205], v[22:25]
	v_mfma_f32_16x16x32_bf16 v[34:37], v[160:163], v[202:205], v[34:37]
	v_mfma_f32_16x16x32_bf16 v[26:29], v[152:155], v[210:213], v[26:29]
	v_mfma_f32_16x16x32_bf16 v[30:33], v[160:163], v[210:213], v[30:33]
	v_mfma_f32_16x16x32_bf16 v[14:17], v[156:159], v[188:191], v[14:17]
	v_mfma_f32_16x16x32_bf16 v[10:13], v[164:167], v[188:191], v[10:13]
	v_mfma_f32_16x16x32_bf16 v[6:9], v[156:159], v[196:199], v[6:9]
	v_mfma_f32_16x16x32_bf16 v[18:21], v[164:167], v[196:199], v[18:21]
	v_mfma_f32_16x16x32_bf16 v[22:25], v[156:159], v[206:209], v[22:25]
	v_mfma_f32_16x16x32_bf16 v[34:37], v[164:167], v[206:209], v[34:37]
	v_mfma_f32_16x16x32_bf16 v[26:29], v[156:159], v[214:217], v[26:29]
	v_mfma_f32_16x16x32_bf16 v[30:33], v[164:167], v[214:217], v[30:33]
	v_mfma_f32_16x16x32_bf16 v[66:69], v[168:171], v[184:187], v[66:69]
	v_mfma_f32_16x16x32_bf16 v[98:101], v[176:179], v[184:187], v[98:101]
	v_mfma_f32_16x16x32_bf16 v[62:65], v[168:171], v[192:195], v[62:65]
	v_mfma_f32_16x16x32_bf16 v[94:97], v[176:179], v[192:195], v[94:97]
	v_mfma_f32_16x16x32_bf16 v[58:61], v[168:171], v[202:205], v[58:61]
	v_mfma_f32_16x16x32_bf16 v[90:93], v[176:179], v[202:205], v[90:93]
	v_mfma_f32_16x16x32_bf16 v[54:57], v[168:171], v[210:213], v[54:57]
	v_mfma_f32_16x16x32_bf16 v[86:89], v[176:179], v[210:213], v[86:89]
	v_mfma_f32_16x16x32_bf16 v[66:69], v[172:175], v[188:191], v[66:69]
	v_mfma_f32_16x16x32_bf16 v[98:101], v[180:183], v[188:191], v[98:101]
	v_mfma_f32_16x16x32_bf16 v[62:65], v[172:175], v[196:199], v[62:65]
	v_mfma_f32_16x16x32_bf16 v[94:97], v[180:183], v[196:199], v[94:97]
	v_mfma_f32_16x16x32_bf16 v[58:61], v[172:175], v[206:209], v[58:61]
	v_mfma_f32_16x16x32_bf16 v[90:93], v[180:183], v[206:209], v[90:93]
	v_mfma_f32_16x16x32_bf16 v[54:57], v[172:175], v[214:217], v[54:57]
	v_mfma_f32_16x16x32_bf16 v[86:89], v[180:183], v[214:217], v[86:89]
	s_barrier
	s_add_i32 s28, s52, s38
	v_lshl_add_u64 v[218:219], v[218:219], 0, s[0:1]
	s_mov_b32 m0, s28
	ds_read_b128 v[184:187], v150 offset:49152
	ds_read_b128 v[188:191], v150 offset:50176
	ds_read_b128 v[192:195], v150 offset:51200
	ds_read_b128 v[196:199], v150 offset:52224
	ds_read_b128 v[202:205], v150 offset:53248
	ds_read_b128 v[206:209], v150 offset:54272
	ds_read_b128 v[210:213], v150 offset:55296
	ds_read_b128 v[214:217], v150 offset:56320
	global_load_lds_dwordx4 v[218:219], off
	s_add_i32 m0, s28, 0x2000
	s_add_u32 s24, s24, 0x80080
	v_lshl_add_u64 v[218:219], v[220:221], 0, s[0:1]
	s_addc_u32 s25, s25, 0
	s_add_i32 s28, s53, s38
	global_load_lds_dwordx4 v[218:219], off
	v_lshl_add_u64 v[218:219], s[24:25], 0, v[138:139]
	s_mov_b32 m0, s28
	s_nop 0
	global_load_lds_dwordx4 v[218:219], off
	v_lshl_add_u64 v[218:219], s[24:25], 0, v[134:135]
	s_add_i32 m0, s28, 0x2000
	s_nop 0
	global_load_lds_dwordx4 v[218:219], off
	v_lshl_add_u64 v[218:219], v[222:223], 0, s[0:1]
	s_mov_b32 m0, s44
	s_nop 0
	global_load_lds_dwordx4 v[218:219], off
	v_lshl_add_u64 v[218:219], v[224:225], 0, s[0:1]
	s_mov_b32 m0, s45
	s_nop 0
	global_load_lds_dwordx4 v[218:219], off
	s_waitcnt vmcnt(8)
	s_waitcnt lgkmcnt(0)
	s_barrier
	s_waitcnt lgkmcnt(0)
	v_mfma_f32_16x16x32_bf16 v[50:53], v[152:155], v[184:187], v[50:53]
	v_mfma_f32_16x16x32_bf16 v[82:85], v[160:163], v[184:187], v[82:85]
	v_mfma_f32_16x16x32_bf16 v[46:49], v[152:155], v[192:195], v[46:49]
	v_mfma_f32_16x16x32_bf16 v[78:81], v[160:163], v[192:195], v[78:81]
	v_mfma_f32_16x16x32_bf16 v[42:45], v[152:155], v[202:205], v[42:45]
	v_mfma_f32_16x16x32_bf16 v[74:77], v[160:163], v[202:205], v[74:77]
	v_mfma_f32_16x16x32_bf16 v[38:41], v[152:155], v[210:213], v[38:41]
	v_mfma_f32_16x16x32_bf16 v[70:73], v[160:163], v[210:213], v[70:73]
	v_mfma_f32_16x16x32_bf16 v[50:53], v[156:159], v[188:191], v[50:53]
	v_mfma_f32_16x16x32_bf16 v[82:85], v[164:167], v[188:191], v[82:85]
	v_mfma_f32_16x16x32_bf16 v[46:49], v[156:159], v[196:199], v[46:49]
	v_mfma_f32_16x16x32_bf16 v[78:81], v[164:167], v[196:199], v[78:81]
	v_mfma_f32_16x16x32_bf16 v[42:45], v[156:159], v[206:209], v[42:45]
	v_mfma_f32_16x16x32_bf16 v[74:77], v[164:167], v[206:209], v[74:77]
	v_mfma_f32_16x16x32_bf16 v[38:41], v[156:159], v[214:217], v[38:41]
	v_mfma_f32_16x16x32_bf16 v[70:73], v[164:167], v[214:217], v[70:73]
	v_mfma_f32_16x16x32_bf16 v[114:117], v[168:171], v[184:187], v[114:117]
	v_mfma_f32_16x16x32_bf16 v[130:133], v[176:179], v[184:187], v[130:133]
	v_mfma_f32_16x16x32_bf16 v[110:113], v[168:171], v[192:195], v[110:113]
	v_mfma_f32_16x16x32_bf16 v[126:129], v[176:179], v[192:195], v[126:129]
	v_mfma_f32_16x16x32_bf16 v[106:109], v[168:171], v[202:205], v[106:109]
	v_mfma_f32_16x16x32_bf16 v[122:125], v[176:179], v[202:205], v[122:125]
	v_mfma_f32_16x16x32_bf16 v[102:105], v[168:171], v[210:213], v[102:105]
	v_mfma_f32_16x16x32_bf16 v[118:121], v[176:179], v[210:213], v[118:121]
	v_mfma_f32_16x16x32_bf16 v[114:117], v[172:175], v[188:191], v[114:117]
	v_mfma_f32_16x16x32_bf16 v[130:133], v[180:183], v[188:191], v[130:133]
	v_mfma_f32_16x16x32_bf16 v[110:113], v[172:175], v[196:199], v[110:113]
	v_mfma_f32_16x16x32_bf16 v[126:129], v[180:183], v[196:199], v[126:129]
	v_mfma_f32_16x16x32_bf16 v[106:109], v[172:175], v[206:209], v[106:109]
	v_mfma_f32_16x16x32_bf16 v[122:125], v[180:183], v[206:209], v[122:125]
	v_mfma_f32_16x16x32_bf16 v[102:105], v[172:175], v[214:217], v[102:105]
	v_mfma_f32_16x16x32_bf16 v[118:121], v[180:183], v[214:217], v[118:121]
	s_barrier
	s_add_i32 s51, s51, 2
	s_cmp_gt_u32 s51, 29
	s_mov_b64 s[28:29], s[22:23]
	s_cbranch_scc0 .LBB0_247
; __device__ __forceinline__ unsigned cvt_pk_bf16(float lo, float hi) { const f32x2 v = {lo, hi}; const bf16x2_t b = __builtin_convertvector(v, bf16x2_t); return __builtin_bit_cast(unsigned, b); }
; #define ZERO4() ((f32x4){opaque0(), 0.f, 0.f, 0.f} * 0.f)
; #define PG8_BAR __builtin_amdgcn_s_barrier()
;     __device__ __forceinline__ void operator()(const f32x4 (&acc)[2][2][4][2], const Unit& u, int wr, int wc, int fr, int fq) const {
;         const int row0 = u.pm * BM + wr * 64 + fr, col0 = u.pn * BM + wc * 32 + 8 * fq;
; #pragma unroll
;         for (int ai = 0; ai < 2; ++ai)
; #pragma unroll
;             for (int m = 0; m < 4; ++m) { bf16_t* rowp = O + (size_t)(row0 + ai * HALF + m * 16) * ldc + col0;
; #pragma unroll
;                 for (int bj = 0; bj < 2; ++bj) { const f32x4 v0 = acc[ai][bj][m][0], v1 = acc[ai][bj][m][1];
;                     u32x4 w; w.x = cvt_pk_bf16(v0[0], v0[1]); w.y = cvt_pk_bf16(v0[2], v0[3]); w.z = cvt_pk_bf16(v1[0], v1[1]); w.w = cvt_pk_bf16(v1[2], v1[3]);
;                     *(u32x4*)(rowp + bj * HALF) = w; } }
; template <class Epi, class Sched, bool GATHER = false>
; __device__ __forceinline__ void gemm_phase(LAS unsigned char* lds, const Gemm g, const Sched& S, const Epi& E, const int tid) {
;     ...
;         if (wr == 0) PG8_BAR;
;         E(acc, cur, wr, wc, fr, fq);
;         if (!has_next) break;
; #pragma unroll
;         for (int a = 0; a < 2; ++a)
; #pragma unroll
;             for (int b = 0; b < 2; ++b)
; #pragma unroll
;                 for (int m = 0; m < 4; ++m)
; #pragma unroll
;                     for (int n = 0; n < 2; ++n) acc[a][b][m][n] = ZERO4();
;         cur = nxt; cA = nA; cB = nB; ++ui;
;         if (GATHER) {
; #pragma unroll
;             for (int h_ = 0; h_ < 2; ++h_) { goC[h_][0] = goN[h_][0]; goC[h_][1] = goN[h_][1]; } }
;         if (wr == 1) PG8_BAR;
.Lpeel0_exit:
	s_and_b64 vcc, exec, s[8:9]
	s_cbranch_vccz .LBB0_250
	s_barrier
.LBB0_250:
	v_lshl_or_b32 v4, s48, 8, v149
	v_lshl_add_u32 v2, s10, 8, v148
	v_ashrrev_i32_e32 v5, 31, v4
	v_mov_b64_e32 v[146:147], s[6:7]
	v_mad_i64_i32 v[152:153], s[16:17], v2, s97, v[146:147]
	v_lshlrev_b64 v[154:155], 1, v[4:5]
	v_lshl_add_u64 v[4:5], v[152:153], 0, v[154:155]
	v_cvt_pk_bf16_f32 v14, v14, v15
	v_cvt_pk_bf16_f32 v15, v16, v17
	v_cvt_pk_bf16_f32 v16, v10, v11
	v_cvt_pk_bf16_f32 v17, v12, v13
	v_cvt_pk_bf16_f32 v10, v66, v67
	v_cvt_pk_bf16_f32 v11, v68, v69
	v_cvt_pk_bf16_f32 v12, v98, v99
	v_cvt_pk_bf16_f32 v13, v100, v101
	global_store_dwordx4 v[4:5], v[14:17], off
	global_store_dwordx4 v[4:5], v[10:13], off offset:256
	v_or_b32_e32 v4, 16, v2
	v_mad_i64_i32 v[4:5], s[16:17], v4, s97, v[146:147]
	v_lshl_add_u64 v[10:11], v[4:5], 0, v[154:155]
	v_cvt_pk_bf16_f32 v4, v6, v7
	v_cvt_pk_bf16_f32 v5, v8, v9
	v_cvt_pk_bf16_f32 v6, v18, v19
	v_cvt_pk_bf16_f32 v7, v20, v21
	global_store_dwordx4 v[10:11], v[4:7], off
	s_andn2_b64 vcc, exec, s[4:5]
	s_mov_b64 s[4:5], -1
	v_cvt_pk_bf16_f32 v4, v62, v63
	v_cvt_pk_bf16_f32 v5, v64, v65
	v_cvt_pk_bf16_f32 v6, v94, v95
	v_cvt_pk_bf16_f32 v7, v96, v97
	global_store_dwordx4 v[10:11], v[4:7], off offset:256
	s_movk_i32 s50, 0xa0
	s_nop 0
	v_or_b32_e32 v4, 32, v2
	v_mad_i64_i32 v[4:5], s[16:17], v4, s97, v[146:147]
	v_lshl_add_u64 v[8:9], v[4:5], 0, v[154:155]
	v_cvt_pk_bf16_f32 v4, v22, v23
	v_cvt_pk_bf16_f32 v5, v24, v25
	v_cvt_pk_bf16_f32 v6, v34, v35
	v_cvt_pk_bf16_f32 v7, v36, v37
	global_store_dwordx4 v[8:9], v[4:7], off
	s_nop 1
	v_cvt_pk_bf16_f32 v4, v58, v59
	v_cvt_pk_bf16_f32 v5, v60, v61
	v_cvt_pk_bf16_f32 v6, v90, v91
	v_cvt_pk_bf16_f32 v7, v92, v93
	global_store_dwordx4 v[8:9], v[4:7], off offset:256
	s_nop 1
	v_or_b32_e32 v4, 48, v2
	v_mad_i64_i32 v[4:5], s[16:17], v4, s97, v[146:147]
	v_lshl_add_u64 v[8:9], v[4:5], 0, v[154:155]
	v_cvt_pk_bf16_f32 v4, v26, v27
	v_cvt_pk_bf16_f32 v5, v28, v29
	v_cvt_pk_bf16_f32 v6, v30, v31
	v_cvt_pk_bf16_f32 v7, v32, v33
	global_store_dwordx4 v[8:9], v[4:7], off
	s_nop 1
	v_cvt_pk_bf16_f32 v4, v54, v55
	v_cvt_pk_bf16_f32 v5, v56, v57
	v_cvt_pk_bf16_f32 v6, v86, v87
	v_cvt_pk_bf16_f32 v7, v88, v89
	global_store_dwordx4 v[8:9], v[4:7], off offset:256
	s_nop 1
	v_add_u32_e32 v4, 0x80, v2
	v_mad_i64_i32 v[4:5], s[16:17], v4, s97, v[146:147]
	v_lshl_add_u64 v[8:9], v[4:5], 0, v[154:155]
	v_cvt_pk_bf16_f32 v4, v50, v51
	v_cvt_pk_bf16_f32 v5, v52, v53
	v_cvt_pk_bf16_f32 v6, v82, v83
	v_cvt_pk_bf16_f32 v7, v84, v85
	global_store_dwordx4 v[8:9], v[4:7], off
	s_nop 1
	v_cvt_pk_bf16_f32 v4, v114, v115
	v_cvt_pk_bf16_f32 v5, v116, v117
	v_cvt_pk_bf16_f32 v6, v130, v131
	v_cvt_pk_bf16_f32 v7, v132, v133
	global_store_dwordx4 v[8:9], v[4:7], off offset:256
	s_nop 1
	v_add_u32_e32 v4, 0x90, v2
	v_mad_i64_i32 v[4:5], s[16:17], v4, s97, v[146:147]
	v_lshl_add_u64 v[8:9], v[4:5], 0, v[154:155]
	v_cvt_pk_bf16_f32 v4, v46, v47
	v_cvt_pk_bf16_f32 v5, v48, v49
	v_cvt_pk_bf16_f32 v6, v78, v79
	v_cvt_pk_bf16_f32 v7, v80, v81
	global_store_dwordx4 v[8:9], v[4:7], off
	s_nop 1
	v_cvt_pk_bf16_f32 v4, v110, v111
	v_cvt_pk_bf16_f32 v5, v112, v113
	v_cvt_pk_bf16_f32 v6, v126, v127
	v_cvt_pk_bf16_f32 v7, v128, v129
	global_store_dwordx4 v[8:9], v[4:7], off offset:256
	s_nop 1
	v_add_u32_e32 v4, 0xa0, v2
	v_mad_i64_i32 v[4:5], s[16:17], v4, s97, v[146:147]
	v_lshl_add_u64 v[8:9], v[4:5], 0, v[154:155]
	v_cvt_pk_bf16_f32 v4, v42, v43
	v_cvt_pk_bf16_f32 v5, v44, v45
	v_cvt_pk_bf16_f32 v6, v74, v75
	v_cvt_pk_bf16_f32 v7, v76, v77
	global_store_dwordx4 v[8:9], v[4:7], off
	v_add_u32_e32 v2, 0xb0, v2
	s_nop 0
	v_cvt_pk_bf16_f32 v4, v106, v107
	v_cvt_pk_bf16_f32 v5, v108, v109
	v_cvt_pk_bf16_f32 v6, v122, v123
	v_cvt_pk_bf16_f32 v7, v124, v125
	global_store_dwordx4 v[8:9], v[4:7], off offset:256
	s_nop 1
	v_mad_i64_i32 v[4:5], s[16:17], v2, s97, v[146:147]
	v_lshl_add_u64 v[8:9], v[4:5], 0, v[154:155]
	v_cvt_pk_bf16_f32 v4, v38, v39
	v_cvt_pk_bf16_f32 v5, v40, v41
	v_cvt_pk_bf16_f32 v6, v70, v71
	v_cvt_pk_bf16_f32 v7, v72, v73
	global_store_dwordx4 v[8:9], v[4:7], off
	s_nop 1
	v_cvt_pk_bf16_f32 v4, v102, v103
	v_cvt_pk_bf16_f32 v5, v104, v105
	v_cvt_pk_bf16_f32 v6, v118, v119
	v_cvt_pk_bf16_f32 v7, v120, v121
	global_store_dwordx4 v[8:9], v[4:7], off offset:256
	s_cbranch_vccnz .LBB0_243
	v_mov_b32_e32 v2, v3
	s_andn2_b64 vcc, exec, s[2:3]
	s_cbranch_vccnz .LBB0_242
	s_barrier
	s_branch .LBB0_242

; #define LAS __attribute__((address_space(3)))
;     __device__ __forceinline__ bool next(int i, Unit& u) const { if (i >= per * reps) return false; return StaticOrder::next(i % per, u); }
; #define PG8_STAGE_A(bufoff, base_, nx_, kb_, h_) do { if (GATHER) { if (nx_) PG8_STAGE_G(bufoff, kb_, goN, h_); else PG8_STAGE_G(bufoff, kb_, goC, h_); } \
;         else PG8_STAGE(bufoff, (base_) + (kb_) + (h_) * hstep, voffA); } while (0)
; #define PG8_STAGE(bufoff, gbase, voff) do { _Pragma("unroll") for (int _i = 0; _i < 2; ++_i) \
;         __builtin_amdgcn_global_load_lds((const unsigned*)((const char*)(gbase) + (voff)[_i]), (LAS unsigned*)(lds + (bufoff) + ldsw + _i * 8192), 16, 0, 0); } while (0)
; #define PG8_WAIT_V(n) asm volatile("s_waitcnt vmcnt(" #n ")" ::: "memory")
; #define PG8_WAIT_L(n) asm volatile("s_waitcnt lgkmcnt(" #n ")" ::: "memory")
; template <class Epi, class Sched, bool GATHER = false>
; __device__ __forceinline__ void gemm_phase(LAS unsigned char* lds, const Gemm g, const Sched& S, const Epi& E, const int tid) {
;     ...
;         const bool has_next = S.next(ui + 1, nxt);
;         const char* nA = has_next ? (const char*)g.A + (size_t)nxt.pm * tstep : cA; const char* nB = has_next ? (const char*)g.Bt + (size_t)nxt.pb * tstep : cB;
;         if (GATHER && has_next && wid < 4) __builtin_amdgcn_global_load_lds((const unsigned*)(g.rowmap + nxt.rb + tid), (LAS unsigned*)(lds + STAGE_BYTES + ((ui + 1) & 1) * 1024 + wid * 256), 4, 0, 0);
;         for (int t = 0; t < nt; t += 2) {
;             const bool last = (t == nt - 2);
;             const char* a1 = cA + (size_t)(t + 1) * kstep;
;             const char* a2 = last ? nA : cA + (size_t)(t + 2) * kstep; const char* b2 = last ? nB : cB + (size_t)(t + 2) * kstep;
;             const char* a3 = a2 + kstep; const char* b3 = b2 + kstep;
;     ...
;             const size_t kb1 = (size_t)(t + 1) * kstep, kb2 = last ? (size_t)0 : (size_t)(t + 2) * kstep, kb3 = kb2 + kstep;
;             PG8_LDB(B0, 0, 0); PG8_LDB(B1, 0, 1); PG8_SCHED; PG8_LDA(At, 0, 0); PG8_STAGE_A(PG8_SA(1, 1), cA, false, kb1, 1);
;             PG8_WAIT_V(8); PG8_WAIT_L(0); PG8_BAR; PG8_MMA(0, 0, At, B0); PG8_MMA(0, 1, At, B1); PG8_BAR; PG8_SCHED;
;             PG8_LDA(At, 0, 1); PG8_STAGE(PG8_SB(0, 0), b2, voffB); PG8_STAGE(PG8_SB(0, 1), b2 + hstep, voffB); PG8_STAGE_A(PG8_SA(0, 0), (last ? nA : cA), last, kb2, 0);
.LBB0_1127:
	s_ashr_i32 s17, s16, 31
	s_lshl_b64 s[18:19], s[16:17], 20
	s_add_u32 s18, s34, s18
	s_addc_u32 s19, s35, s19
	s_ashr_i32 s15, s14, 31
	s_lshl_b64 s[20:21], s[14:15], 20
	s_add_u32 s20, s36, s20
	s_addc_u32 s21, s37, s21
	s_and_b64 s[24:25], s[4:5], exec
	s_cselect_b32 s15, s21, s23
	s_cselect_b32 s17, s20, s22
	s_add_u32 s47, s22, 0x100
	s_addc_u32 s48, s23, 0
	s_add_u32 s22, s10, 0x80080
	s_addc_u32 s23, s11, 0
	v_lshl_add_u64 v[4:5], s[22:23], 0, v[142:143]
	v_lshl_add_u64 v[146:147], s[22:23], 0, v[144:145]
	s_mov_b32 s49, -2
	s_mov_b64 s[28:29], 0
	s_add_u32 s22, s28, 0x100
	s_addc_u32 s23, s29, 0
	s_add_u32 s52, s47, s28
	s_addc_u32 s53, s48, s29
	s_add_i32 s24, 0, 0x10000
	s_add_i32 s54, 0, 0x14000
	v_add_u32_e32 v2, s24, v148
	ds_read_b128 v[152:155], v2
	ds_read_b128 v[156:159], v2 offset:1024
	ds_read_b128 v[160:163], v2 offset:2048
	ds_read_b128 v[164:167], v2 offset:3072
	v_add_u32_e32 v2, s54, v148
	ds_read_b128 v[168:171], v2
	ds_read_b128 v[172:175], v2 offset:1024
	ds_read_b128 v[176:179], v2 offset:2048
	ds_read_b128 v[180:183], v2 offset:3072
	s_add_i32 s56, s24, s33
	s_add_i32 m0, s9, 0xc000
	s_add_i32 s55, s9, 0xe000
	s_add_i32 s57, s56, 0x2000
	s_cmp_eq_u32 s49, 28
	s_cselect_b64 s[50:51], -1, 0
	s_and_b64 s[24:25], s[50:51], exec
	s_cselect_b32 s25, s15, s53
	s_cselect_b32 s24, s17, s52
	v_lshl_add_u64 v[218:219], v[4:5], 0, s[28:29]
	ds_read_b128 v[184:187], v150
	ds_read_b128 v[188:191], v150 offset:1024
	ds_read_b128 v[192:195], v150 offset:2048
	ds_read_b128 v[196:199], v150 offset:3072
	ds_read_b128 v[202:205], v150 offset:4096
	ds_read_b128 v[206:209], v150 offset:5120
	ds_read_b128 v[210:213], v150 offset:6144
	ds_read_b128 v[214:217], v150 offset:7168
	global_load_lds_dwordx4 v[218:219], off
	v_lshl_add_u64 v[218:219], v[146:147], 0, s[28:29]
	s_mov_b32 m0, s55
	s_nop 0
	global_load_lds_dwordx4 v[218:219], off
	s_waitcnt vmcnt(8)
	s_waitcnt lgkmcnt(0)
	s_barrier
	s_waitcnt lgkmcnt(0)
	v_mfma_f32_16x16x32_bf16 v[86:89], v[152:155], v[184:187], 0
	v_mfma_f32_16x16x32_bf16 v[18:21], v[160:163], v[184:187], 0
	v_mfma_f32_16x16x32_bf16 v[6:9], v[152:155], v[192:195], 0
	v_mfma_f32_16x16x32_bf16 v[22:25], v[160:163], v[192:195], 0
	v_mfma_f32_16x16x32_bf16 v[10:13], v[152:155], v[202:205], 0
	v_mfma_f32_16x16x32_bf16 v[26:29], v[160:163], v[202:205], 0
	v_mfma_f32_16x16x32_bf16 v[14:17], v[152:155], v[210:213], 0
	v_mfma_f32_16x16x32_bf16 v[30:33], v[160:163], v[210:213], 0
	v_mfma_f32_16x16x32_bf16 v[86:89], v[156:159], v[188:191], v[86:89]
	v_mfma_f32_16x16x32_bf16 v[18:21], v[164:167], v[188:191], v[18:21]
	v_mfma_f32_16x16x32_bf16 v[6:9], v[156:159], v[196:199], v[6:9]
	v_mfma_f32_16x16x32_bf16 v[22:25], v[164:167], v[196:199], v[22:25]
	v_mfma_f32_16x16x32_bf16 v[10:13], v[156:159], v[206:209], v[10:13]
	v_mfma_f32_16x16x32_bf16 v[26:29], v[164:167], v[206:209], v[26:29]
	v_mfma_f32_16x16x32_bf16 v[14:17], v[156:159], v[214:217], v[14:17]
	v_mfma_f32_16x16x32_bf16 v[30:33], v[164:167], v[214:217], v[30:33]
	v_mfma_f32_16x16x32_bf16 v[34:37], v[168:171], v[184:187], 0
	v_mfma_f32_16x16x32_bf16 v[50:53], v[176:179], v[184:187], 0
	v_mfma_f32_16x16x32_bf16 v[38:41], v[168:171], v[192:195], 0
	v_mfma_f32_16x16x32_bf16 v[58:61], v[176:179], v[192:195], 0
	v_mfma_f32_16x16x32_bf16 v[42:45], v[168:171], v[202:205], 0
	v_mfma_f32_16x16x32_bf16 v[66:69], v[176:179], v[202:205], 0
	v_mfma_f32_16x16x32_bf16 v[46:49], v[168:171], v[210:213], 0
	v_mfma_f32_16x16x32_bf16 v[74:77], v[176:179], v[210:213], 0
	v_mfma_f32_16x16x32_bf16 v[34:37], v[172:175], v[188:191], v[34:37]
	v_mfma_f32_16x16x32_bf16 v[50:53], v[180:183], v[188:191], v[50:53]
	v_mfma_f32_16x16x32_bf16 v[38:41], v[172:175], v[196:199], v[38:41]
	v_mfma_f32_16x16x32_bf16 v[58:61], v[180:183], v[196:199], v[58:61]
	v_mfma_f32_16x16x32_bf16 v[42:45], v[172:175], v[206:209], v[42:45]
	v_mfma_f32_16x16x32_bf16 v[66:69], v[180:183], v[206:209], v[66:69]
	v_mfma_f32_16x16x32_bf16 v[46:49], v[172:175], v[214:217], v[46:49]
	v_mfma_f32_16x16x32_bf16 v[74:77], v[180:183], v[214:217], v[74:77]
	s_barrier
	s_mov_b32 m0, s56
	v_lshl_add_u64 v[218:219], s[24:25], 0, v[136:137]
	s_cselect_b32 s52, 0, s23
	s_cselect_b32 s53, 0, s22
	s_add_u32 s28, s24, 0x80000
	ds_read_b128 v[184:187], v150 offset:16384
	ds_read_b128 v[188:191], v150 offset:17408
	ds_read_b128 v[192:195], v150 offset:18432
	ds_read_b128 v[196:199], v150 offset:19456
	ds_read_b128 v[202:205], v150 offset:20480
	ds_read_b128 v[206:209], v150 offset:21504
	ds_read_b128 v[210:213], v150 offset:22528
	ds_read_b128 v[214:217], v150 offset:23552
	global_load_lds_dwordx4 v[218:219], off
	v_lshl_add_u64 v[220:221], s[24:25], 0, v[140:141]
	s_mov_b32 m0, s57
	s_addc_u32 s29, s25, 0
	s_add_i32 s54, s54, s33
	global_load_lds_dwordx4 v[220:221], off
	v_lshl_add_u64 v[222:223], s[28:29], 0, v[136:137]
	s_mov_b32 m0, s54
	s_nop 0
	global_load_lds_dwordx4 v[222:223], off
	v_lshl_add_u64 v[222:223], s[28:29], 0, v[140:141]
	s_add_i32 m0, s54, 0x2000
	s_and_b64 s[28:29], s[50:51], s[4:5]
	s_and_b64 s[28:29], s[28:29], exec
	s_cselect_b32 s28, s18, s10
	s_cselect_b32 s29, s19, s11
	s_add_u32 s28, s28, s53
	s_addc_u32 s29, s29, s52
	global_load_lds_dwordx4 v[222:223], off
	v_lshl_add_u64 v[222:223], s[28:29], 0, v[134:135]
	s_mov_b32 m0, s9
	v_lshl_add_u64 v[224:225], s[28:29], 0, v[138:139]
	global_load_lds_dwordx4 v[222:223], off
	s_mov_b32 m0, s38
	s_nop 0
	global_load_lds_dwordx4 v[224:225], off
	s_waitcnt vmcnt(8)
	s_waitcnt lgkmcnt(0)
	s_barrier
; #define PG8_STAGE_A(bufoff, base_, nx_, kb_, h_) do { if (GATHER) { if (nx_) PG8_STAGE_G(bufoff, kb_, goN, h_); else PG8_STAGE_G(bufoff, kb_, goC, h_); } \
;         else PG8_STAGE(bufoff, (base_) + (kb_) + (h_) * hstep, voffA); } while (0)
; #define PG8_LDA(dst, b, h) do { _Pragma("unroll") for (int m = 0; m < 4; ++m) _Pragma("unroll") for (int k = 0; k < 2; ++k) dst[m][k] = *(const LAS bf16x8*)(lds + PG8_SA(b, h) + aoff + m * 2048 + k * 1024); } while (0)
; #define PG8_LDB(dst, b, h) do { _Pragma("unroll") for (int n = 0; n < 2; ++n) _Pragma("unroll") for (int k = 0; k < 2; ++k) dst[n][k] = *(const LAS bf16x8*)(lds + PG8_SB(b, h) + boff + n * 2048 + k * 1024); } while (0)
; #define PG8_MMA(ai, bj, At, Bt) do { __builtin_amdgcn_s_setprio(1); _Pragma("unroll") for (int m = 0; m < 4; ++m) _Pragma("unroll") for (int n = 0; n < 2; ++n) _Pragma("unroll") for (int k = 0; k < 2; ++k) \
;         acc[ai][bj][m][n] = __builtin_amdgcn_mfma_f32_16x16x32_bf16(Bt[n][k], At[m][k], acc[ai][bj][m][n], 0, 0, 0); __builtin_amdgcn_s_setprio(0); } while (0)
; #define PG8_WAIT_V(n) asm volatile("s_waitcnt vmcnt(" #n ")" ::: "memory")
; #define PG8_WAIT_L(n) asm volatile("s_waitcnt lgkmcnt(" #n ")" ::: "memory")
; #define PG8_BAR __builtin_amdgcn_s_barrier()
; #define PG8_SCHED __builtin_amdgcn_sched_barrier(0)
; template <class Epi, class Sched, bool GATHER = false>
; __device__ __forceinline__ void gemm_phase(LAS unsigned char* lds, const Gemm g, const Sched& S, const Epi& E, const int tid) {
;     ...
;             PG8_WAIT_V(8); PG8_WAIT_L(0); PG8_BAR; PG8_MMA(1, 0, At, B0); PG8_MMA(1, 1, At, B1); PG8_BAR; PG8_SCHED;
;             PG8_LDB(B0, 1, 0); PG8_LDB(B1, 1, 1); PG8_SCHED; PG8_LDA(At, 1, 0); PG8_STAGE_A(PG8_SA(0, 1), (last ? nA : cA), last, kb2, 1);
;             PG8_WAIT_V(8); PG8_WAIT_L(0); PG8_BAR; PG8_MMA(0, 0, At, B0); PG8_MMA(0, 1, At, B1); PG8_BAR; PG8_SCHED;
	s_waitcnt lgkmcnt(0)
	v_mfma_f32_16x16x32_bf16 v[54:57], v[152:155], v[184:187], 0
	v_mfma_f32_16x16x32_bf16 v[78:81], v[160:163], v[184:187], 0
	v_mfma_f32_16x16x32_bf16 v[62:65], v[152:155], v[192:195], 0
	v_mfma_f32_16x16x32_bf16 v[82:85], v[160:163], v[192:195], 0
	v_mfma_f32_16x16x32_bf16 v[70:73], v[152:155], v[202:205], 0
	v_mfma_f32_16x16x32_bf16 v[98:101], v[160:163], v[202:205], 0
	v_mfma_f32_16x16x32_bf16 v[90:93], v[152:155], v[210:213], 0
	v_mfma_f32_16x16x32_bf16 v[94:97], v[160:163], v[210:213], 0
	v_mfma_f32_16x16x32_bf16 v[54:57], v[156:159], v[188:191], v[54:57]
	v_mfma_f32_16x16x32_bf16 v[78:81], v[164:167], v[188:191], v[78:81]
	v_mfma_f32_16x16x32_bf16 v[62:65], v[156:159], v[196:199], v[62:65]
	v_mfma_f32_16x16x32_bf16 v[82:85], v[164:167], v[196:199], v[82:85]
	v_mfma_f32_16x16x32_bf16 v[70:73], v[156:159], v[206:209], v[70:73]
	v_mfma_f32_16x16x32_bf16 v[98:101], v[164:167], v[206:209], v[98:101]
	v_mfma_f32_16x16x32_bf16 v[90:93], v[156:159], v[214:217], v[90:93]
	v_mfma_f32_16x16x32_bf16 v[94:97], v[164:167], v[214:217], v[94:97]
	v_mfma_f32_16x16x32_bf16 v[114:117], v[168:171], v[184:187], 0
	v_mfma_f32_16x16x32_bf16 v[130:133], v[176:179], v[184:187], 0
	v_mfma_f32_16x16x32_bf16 v[110:113], v[168:171], v[192:195], 0
	v_mfma_f32_16x16x32_bf16 v[126:129], v[176:179], v[192:195], 0
	v_mfma_f32_16x16x32_bf16 v[106:109], v[168:171], v[202:205], 0
	v_mfma_f32_16x16x32_bf16 v[122:125], v[176:179], v[202:205], 0
	v_mfma_f32_16x16x32_bf16 v[102:105], v[168:171], v[210:213], 0
	v_mfma_f32_16x16x32_bf16 v[118:121], v[176:179], v[210:213], 0
	v_mfma_f32_16x16x32_bf16 v[114:117], v[172:175], v[188:191], v[114:117]
	v_mfma_f32_16x16x32_bf16 v[130:133], v[180:183], v[188:191], v[130:133]
	v_mfma_f32_16x16x32_bf16 v[110:113], v[172:175], v[196:199], v[110:113]
	v_mfma_f32_16x16x32_bf16 v[126:129], v[180:183], v[196:199], v[126:129]
	v_mfma_f32_16x16x32_bf16 v[106:109], v[172:175], v[206:209], v[106:109]
	v_mfma_f32_16x16x32_bf16 v[122:125], v[180:183], v[206:209], v[122:125]
	v_mfma_f32_16x16x32_bf16 v[102:105], v[172:175], v[214:217], v[102:105]
	v_mfma_f32_16x16x32_bf16 v[118:121], v[180:183], v[214:217], v[118:121]
	s_barrier
	s_add_i32 s50, 0, 0x18000
	v_add_u32_e32 v2, s50, v148
	s_add_i32 s51, 0, 0x1c000
	ds_read_b128 v[152:155], v2
	ds_read_b128 v[156:159], v2 offset:1024
	ds_read_b128 v[160:163], v2 offset:2048
	ds_read_b128 v[164:167], v2 offset:3072
	v_add_u32_e32 v2, s51, v148
	ds_read_b128 v[168:171], v2
	ds_read_b128 v[172:175], v2 offset:1024
	ds_read_b128 v[176:179], v2 offset:2048
	ds_read_b128 v[180:183], v2 offset:3072
	s_add_u32 s28, s28, 0x80000
	s_addc_u32 s29, s29, 0
	s_mov_b32 m0, s39
	v_lshl_add_u64 v[226:227], s[28:29], 0, v[134:135]
	ds_read_b128 v[184:187], v150 offset:32768
	ds_read_b128 v[188:191], v150 offset:33792
	ds_read_b128 v[192:195], v150 offset:34816
	ds_read_b128 v[196:199], v150 offset:35840
	ds_read_b128 v[202:205], v150 offset:36864
	ds_read_b128 v[206:209], v150 offset:37888
	ds_read_b128 v[210:213], v150 offset:38912
	ds_read_b128 v[214:217], v150 offset:39936
	global_load_lds_dwordx4 v[226:227], off
	v_lshl_add_u64 v[226:227], s[28:29], 0, v[138:139]
	s_mov_b32 m0, s40
	s_nop 0
	global_load_lds_dwordx4 v[226:227], off
	s_waitcnt vmcnt(8)
	s_waitcnt lgkmcnt(0)
	s_barrier
	s_waitcnt lgkmcnt(0)
	v_mfma_f32_16x16x32_bf16 v[86:89], v[152:155], v[184:187], v[86:89]
	v_mfma_f32_16x16x32_bf16 v[18:21], v[160:163], v[184:187], v[18:21]
	v_mfma_f32_16x16x32_bf16 v[6:9], v[152:155], v[192:195], v[6:9]
	v_mfma_f32_16x16x32_bf16 v[22:25], v[160:163], v[192:195], v[22:25]
	v_mfma_f32_16x16x32_bf16 v[10:13], v[152:155], v[202:205], v[10:13]
	v_mfma_f32_16x16x32_bf16 v[26:29], v[160:163], v[202:205], v[26:29]
	v_mfma_f32_16x16x32_bf16 v[14:17], v[152:155], v[210:213], v[14:17]
	v_mfma_f32_16x16x32_bf16 v[30:33], v[160:163], v[210:213], v[30:33]
	v_mfma_f32_16x16x32_bf16 v[86:89], v[156:159], v[188:191], v[86:89]
	v_mfma_f32_16x16x32_bf16 v[18:21], v[164:167], v[188:191], v[18:21]
	v_mfma_f32_16x16x32_bf16 v[6:9], v[156:159], v[196:199], v[6:9]
	v_mfma_f32_16x16x32_bf16 v[22:25], v[164:167], v[196:199], v[22:25]
	v_mfma_f32_16x16x32_bf16 v[10:13], v[156:159], v[206:209], v[10:13]
	v_mfma_f32_16x16x32_bf16 v[26:29], v[164:167], v[206:209], v[26:29]
	v_mfma_f32_16x16x32_bf16 v[14:17], v[156:159], v[214:217], v[14:17]
	v_mfma_f32_16x16x32_bf16 v[30:33], v[164:167], v[214:217], v[30:33]
	v_mfma_f32_16x16x32_bf16 v[34:37], v[168:171], v[184:187], v[34:37]
	v_mfma_f32_16x16x32_bf16 v[50:53], v[176:179], v[184:187], v[50:53]
	v_mfma_f32_16x16x32_bf16 v[38:41], v[168:171], v[192:195], v[38:41]
	v_mfma_f32_16x16x32_bf16 v[58:61], v[176:179], v[192:195], v[58:61]
	v_mfma_f32_16x16x32_bf16 v[42:45], v[168:171], v[202:205], v[42:45]
	v_mfma_f32_16x16x32_bf16 v[66:69], v[176:179], v[202:205], v[66:69]
	v_mfma_f32_16x16x32_bf16 v[46:49], v[168:171], v[210:213], v[46:49]
	v_mfma_f32_16x16x32_bf16 v[74:77], v[176:179], v[210:213], v[74:77]
	v_mfma_f32_16x16x32_bf16 v[34:37], v[172:175], v[188:191], v[34:37]
	v_mfma_f32_16x16x32_bf16 v[50:53], v[180:183], v[188:191], v[50:53]
	v_mfma_f32_16x16x32_bf16 v[38:41], v[172:175], v[196:199], v[38:41]
	v_mfma_f32_16x16x32_bf16 v[58:61], v[180:183], v[196:199], v[58:61]
	v_mfma_f32_16x16x32_bf16 v[42:45], v[172:175], v[206:209], v[42:45]
	v_mfma_f32_16x16x32_bf16 v[66:69], v[180:183], v[206:209], v[66:69]
	v_mfma_f32_16x16x32_bf16 v[46:49], v[172:175], v[214:217], v[46:49]
	v_mfma_f32_16x16x32_bf16 v[74:77], v[180:183], v[214:217], v[74:77]
	s_barrier
; #define PG8_STAGE_A(bufoff, base_, nx_, kb_, h_) do { if (GATHER) { if (nx_) PG8_STAGE_G(bufoff, kb_, goN, h_); else PG8_STAGE_G(bufoff, kb_, goC, h_); } \
;         else PG8_STAGE(bufoff, (base_) + (kb_) + (h_) * hstep, voffA); } while (0)
; #define PG8_STAGE(bufoff, gbase, voff) do { _Pragma("unroll") for (int _i = 0; _i < 2; ++_i) \
;         __builtin_amdgcn_global_load_lds((const unsigned*)((const char*)(gbase) + (voff)[_i]), (LAS unsigned*)(lds + (bufoff) + ldsw + _i * 8192), 16, 0, 0); } while (0)
; #define PG8_LDA(dst, b, h) do { _Pragma("unroll") for (int m = 0; m < 4; ++m) _Pragma("unroll") for (int k = 0; k < 2; ++k) dst[m][k] = *(const LAS bf16x8*)(lds + PG8_SA(b, h) + aoff + m * 2048 + k * 1024); } while (0)
; #define PG8_LDB(dst, b, h) do { _Pragma("unroll") for (int n = 0; n < 2; ++n) _Pragma("unroll") for (int k = 0; k < 2; ++k) dst[n][k] = *(const LAS bf16x8*)(lds + PG8_SB(b, h) + boff + n * 2048 + k * 1024); } while (0)
; #define PG8_MMA(ai, bj, At, Bt) do { __builtin_amdgcn_s_setprio(1); _Pragma("unroll") for (int m = 0; m < 4; ++m) _Pragma("unroll") for (int n = 0; n < 2; ++n) _Pragma("unroll") for (int k = 0; k < 2; ++k) \
;         acc[ai][bj][m][n] = __builtin_amdgcn_mfma_f32_16x16x32_bf16(Bt[n][k], At[m][k], acc[ai][bj][m][n], 0, 0, 0); __builtin_amdgcn_s_setprio(0); } while (0)
; #define PG8_WAIT_V(n) asm volatile("s_waitcnt vmcnt(" #n ")" ::: "memory")
; #define PG8_WAIT_L(n) asm volatile("s_waitcnt lgkmcnt(" #n ")" ::: "memory")
; #define PG8_BAR __builtin_amdgcn_s_barrier()
; #define PG8_SCHED __builtin_amdgcn_sched_barrier(0)
; template <class Epi, class Sched, bool GATHER = false>
; __device__ __forceinline__ void gemm_phase(LAS unsigned char* lds, const Gemm g, const Sched& S, const Epi& E, const int tid) {
;     ...
;             PG8_LDB(B0, 0, 0); PG8_LDB(B1, 0, 1); PG8_SCHED; PG8_LDA(At, 0, 0); PG8_STAGE_A(PG8_SA(1, 1), cA, false, kb1, 1);
;             PG8_WAIT_V(8); PG8_WAIT_L(0); PG8_BAR; PG8_MMA(0, 0, At, B0); PG8_MMA(0, 1, At, B1); PG8_BAR; PG8_SCHED;
;     ...
;             PG8_LDA(At, 1, 1); PG8_STAGE(PG8_SB(1, 0), b3, voffB); PG8_STAGE(PG8_SB(1, 1), b3 + hstep, voffB); PG8_STAGE_A(PG8_SA(1, 0), (last ? nA : cA), last, kb3, 0);
;             PG8_WAIT_V(8); PG8_WAIT_L(0); PG8_BAR; PG8_MMA(1, 0, At, B0); PG8_MMA(1, 1, At, B1); PG8_BAR; PG8_SCHED;
;     ...
;         }
	s_add_i32 s28, s50, s33
	v_lshl_add_u64 v[218:219], v[218:219], 0, s[0:1]
	s_mov_b32 m0, s28
	ds_read_b128 v[184:187], v150 offset:49152
	ds_read_b128 v[188:191], v150 offset:50176
	ds_read_b128 v[192:195], v150 offset:51200
	ds_read_b128 v[196:199], v150 offset:52224
	ds_read_b128 v[202:205], v150 offset:53248
	ds_read_b128 v[206:209], v150 offset:54272
	ds_read_b128 v[210:213], v150 offset:55296
	ds_read_b128 v[214:217], v150 offset:56320
	global_load_lds_dwordx4 v[218:219], off
	s_add_i32 m0, s28, 0x2000
	s_add_u32 s24, s24, 0x80080
	v_lshl_add_u64 v[218:219], v[220:221], 0, s[0:1]
	s_addc_u32 s25, s25, 0
	s_add_i32 s28, s51, s33
	global_load_lds_dwordx4 v[218:219], off
	v_lshl_add_u64 v[218:219], s[24:25], 0, v[136:137]
	s_mov_b32 m0, s28
	s_nop 0
	global_load_lds_dwordx4 v[218:219], off
	v_lshl_add_u64 v[218:219], s[24:25], 0, v[140:141]
	s_add_i32 m0, s28, 0x2000
	s_nop 0
	global_load_lds_dwordx4 v[218:219], off
	v_lshl_add_u64 v[218:219], v[222:223], 0, s[0:1]
	s_mov_b32 m0, s42
	s_nop 0
	global_load_lds_dwordx4 v[218:219], off
	v_lshl_add_u64 v[218:219], v[224:225], 0, s[0:1]
	s_mov_b32 m0, s43
	s_nop 0
	global_load_lds_dwordx4 v[218:219], off
	s_waitcnt vmcnt(8)
	s_waitcnt lgkmcnt(0)
	s_barrier
	s_waitcnt lgkmcnt(0)
	v_mfma_f32_16x16x32_bf16 v[54:57], v[152:155], v[184:187], v[54:57]
	v_mfma_f32_16x16x32_bf16 v[78:81], v[160:163], v[184:187], v[78:81]
	v_mfma_f32_16x16x32_bf16 v[62:65], v[152:155], v[192:195], v[62:65]
	v_mfma_f32_16x16x32_bf16 v[82:85], v[160:163], v[192:195], v[82:85]
	v_mfma_f32_16x16x32_bf16 v[70:73], v[152:155], v[202:205], v[70:73]
	v_mfma_f32_16x16x32_bf16 v[98:101], v[160:163], v[202:205], v[98:101]
	v_mfma_f32_16x16x32_bf16 v[90:93], v[152:155], v[210:213], v[90:93]
	v_mfma_f32_16x16x32_bf16 v[94:97], v[160:163], v[210:213], v[94:97]
	v_mfma_f32_16x16x32_bf16 v[54:57], v[156:159], v[188:191], v[54:57]
	v_mfma_f32_16x16x32_bf16 v[78:81], v[164:167], v[188:191], v[78:81]
	v_mfma_f32_16x16x32_bf16 v[62:65], v[156:159], v[196:199], v[62:65]
	v_mfma_f32_16x16x32_bf16 v[82:85], v[164:167], v[196:199], v[82:85]
	v_mfma_f32_16x16x32_bf16 v[70:73], v[156:159], v[206:209], v[70:73]
	v_mfma_f32_16x16x32_bf16 v[98:101], v[164:167], v[206:209], v[98:101]
	v_mfma_f32_16x16x32_bf16 v[90:93], v[156:159], v[214:217], v[90:93]
	v_mfma_f32_16x16x32_bf16 v[94:97], v[164:167], v[214:217], v[94:97]
	v_mfma_f32_16x16x32_bf16 v[114:117], v[168:171], v[184:187], v[114:117]
	v_mfma_f32_16x16x32_bf16 v[130:133], v[176:179], v[184:187], v[130:133]
	v_mfma_f32_16x16x32_bf16 v[110:113], v[168:171], v[192:195], v[110:113]
	v_mfma_f32_16x16x32_bf16 v[126:129], v[176:179], v[192:195], v[126:129]
	v_mfma_f32_16x16x32_bf16 v[106:109], v[168:171], v[202:205], v[106:109]
	v_mfma_f32_16x16x32_bf16 v[122:125], v[176:179], v[202:205], v[122:125]
	v_mfma_f32_16x16x32_bf16 v[102:105], v[168:171], v[210:213], v[102:105]
	v_mfma_f32_16x16x32_bf16 v[118:121], v[176:179], v[210:213], v[118:121]
	v_mfma_f32_16x16x32_bf16 v[114:117], v[172:175], v[188:191], v[114:117]
	v_mfma_f32_16x16x32_bf16 v[130:133], v[180:183], v[188:191], v[130:133]
	v_mfma_f32_16x16x32_bf16 v[110:113], v[172:175], v[196:199], v[110:113]
	v_mfma_f32_16x16x32_bf16 v[126:129], v[180:183], v[196:199], v[126:129]
	v_mfma_f32_16x16x32_bf16 v[106:109], v[172:175], v[206:209], v[106:109]
	v_mfma_f32_16x16x32_bf16 v[122:125], v[180:183], v[206:209], v[122:125]
	v_mfma_f32_16x16x32_bf16 v[102:105], v[172:175], v[214:217], v[102:105]
	v_mfma_f32_16x16x32_bf16 v[118:121], v[180:183], v[214:217], v[118:121]
	s_barrier
	s_add_i32 s49, s49, 2
	s_cmp_gt_u32 s49, 29
	s_mov_b64 s[28:29], s[22:23]
	s_cbranch_scc1 .Lpeel1_exit
.LBB0_1128:
	s_add_u32 s22, s28, 0x100
	s_addc_u32 s23, s29, 0
	s_add_u32 s52, s47, s28
	s_addc_u32 s53, s48, s29
	s_add_i32 s24, 0, 0x10000
	s_add_i32 s54, 0, 0x14000
	v_add_u32_e32 v2, s24, v148
	ds_read_b128 v[152:155], v2
	ds_read_b128 v[156:159], v2 offset:1024
	ds_read_b128 v[160:163], v2 offset:2048
	ds_read_b128 v[164:167], v2 offset:3072
	v_add_u32_e32 v2, s54, v148
	ds_read_b128 v[168:171], v2
	ds_read_b128 v[172:175], v2 offset:1024
	ds_read_b128 v[176:179], v2 offset:2048
	ds_read_b128 v[180:183], v2 offset:3072
	s_add_i32 s56, s24, s33
	s_add_i32 m0, s9, 0xc000
	s_add_i32 s55, s9, 0xe000
	s_add_i32 s57, s56, 0x2000
	s_cmp_eq_u32 s49, 28
	s_cselect_b64 s[50:51], -1, 0
	s_and_b64 s[24:25], s[50:51], exec
	s_cselect_b32 s25, s15, s53
	s_cselect_b32 s24, s17, s52
	v_lshl_add_u64 v[218:219], v[4:5], 0, s[28:29]
	ds_read_b128 v[184:187], v150
	ds_read_b128 v[188:191], v150 offset:1024
	ds_read_b128 v[192:195], v150 offset:2048
	ds_read_b128 v[196:199], v150 offset:3072
	ds_read_b128 v[202:205], v150 offset:4096
	ds_read_b128 v[206:209], v150 offset:5120
	ds_read_b128 v[210:213], v150 offset:6144
	ds_read_b128 v[214:217], v150 offset:7168
	global_load_lds_dwordx4 v[218:219], off
	v_lshl_add_u64 v[218:219], v[146:147], 0, s[28:29]
	s_mov_b32 m0, s55
	s_nop 0
	global_load_lds_dwordx4 v[218:219], off
	s_waitcnt vmcnt(8)
	s_waitcnt lgkmcnt(0)
	s_barrier
; #define PG8_STAGE_A(bufoff, base_, nx_, kb_, h_) do { if (GATHER) { if (nx_) PG8_STAGE_G(bufoff, kb_, goN, h_); else PG8_STAGE_G(bufoff, kb_, goC, h_); } \
;         else PG8_STAGE(bufoff, (base_) + (kb_) + (h_) * hstep, voffA); } while (0)
; #define PG8_STAGE(bufoff, gbase, voff) do { _Pragma("unroll") for (int _i = 0; _i < 2; ++_i) \
;         __builtin_amdgcn_global_load_lds((const unsigned*)((const char*)(gbase) + (voff)[_i]), (LAS unsigned*)(lds + (bufoff) + ldsw + _i * 8192), 16, 0, 0); } while (0)
; #define PG8_LDA(dst, b, h) do { _Pragma("unroll") for (int m = 0; m < 4; ++m) _Pragma("unroll") for (int k = 0; k < 2; ++k) dst[m][k] = *(const LAS bf16x8*)(lds + PG8_SA(b, h) + aoff + m * 2048 + k * 1024); } while (0)
; #define PG8_LDB(dst, b, h) do { _Pragma("unroll") for (int n = 0; n < 2; ++n) _Pragma("unroll") for (int k = 0; k < 2; ++k) dst[n][k] = *(const LAS bf16x8*)(lds + PG8_SB(b, h) + boff + n * 2048 + k * 1024); } while (0)
; #define PG8_MMA(ai, bj, At, Bt) do { __builtin_amdgcn_s_setprio(1); _Pragma("unroll") for (int m = 0; m < 4; ++m) _Pragma("unroll") for (int n = 0; n < 2; ++n) _Pragma("unroll") for (int k = 0; k < 2; ++k) \
;         acc[ai][bj][m][n] = __builtin_amdgcn_mfma_f32_16x16x32_bf16(Bt[n][k], At[m][k], acc[ai][bj][m][n], 0, 0, 0); __builtin_amdgcn_s_setprio(0); } while (0)
; #define PG8_WAIT_V(n) asm volatile("s_waitcnt vmcnt(" #n ")" ::: "memory")
; #define PG8_WAIT_L(n) asm volatile("s_waitcnt lgkmcnt(" #n ")" ::: "memory")
; #define PG8_BAR __builtin_amdgcn_s_barrier()
; template <class Epi, class Sched, bool GATHER = false>
; __device__ __forceinline__ void gemm_phase(LAS unsigned char* lds, const Gemm g, const Sched& S, const Epi& E, const int tid) {
;     ...
;             PG8_WAIT_V(8); PG8_WAIT_L(0); PG8_BAR; PG8_MMA(0, 0, At, B0); PG8_MMA(0, 1, At, B1); PG8_BAR; PG8_SCHED;
;             PG8_LDA(At, 0, 1); PG8_STAGE(PG8_SB(0, 0), b2, voffB); PG8_STAGE(PG8_SB(0, 1), b2 + hstep, voffB); PG8_STAGE_A(PG8_SA(0, 0), (last ? nA : cA), last, kb2, 0);
;             PG8_WAIT_V(8); PG8_WAIT_L(0); PG8_BAR; PG8_MMA(1, 0, At, B0); PG8_MMA(1, 1, At, B1); PG8_BAR; PG8_SCHED;
;             PG8_LDB(B0, 1, 0); PG8_LDB(B1, 1, 1); PG8_SCHED; PG8_LDA(At, 1, 0); PG8_STAGE_A(PG8_SA(0, 1), (last ? nA : cA), last, kb2, 1);
;             PG8_WAIT_V(8); PG8_WAIT_L(0); PG8_BAR; PG8_MMA(0, 0, At, B0); PG8_MMA(0, 1, At, B1); PG8_BAR; PG8_SCHED;
	s_waitcnt lgkmcnt(0)
	v_mfma_f32_16x16x32_bf16 v[86:89], v[152:155], v[184:187], v[86:89]
	v_mfma_f32_16x16x32_bf16 v[18:21], v[160:163], v[184:187], v[18:21]
	v_mfma_f32_16x16x32_bf16 v[6:9], v[152:155], v[192:195], v[6:9]
	v_mfma_f32_16x16x32_bf16 v[22:25], v[160:163], v[192:195], v[22:25]
	v_mfma_f32_16x16x32_bf16 v[10:13], v[152:155], v[202:205], v[10:13]
	v_mfma_f32_16x16x32_bf16 v[26:29], v[160:163], v[202:205], v[26:29]
	v_mfma_f32_16x16x32_bf16 v[14:17], v[152:155], v[210:213], v[14:17]
	v_mfma_f32_16x16x32_bf16 v[30:33], v[160:163], v[210:213], v[30:33]
	v_mfma_f32_16x16x32_bf16 v[86:89], v[156:159], v[188:191], v[86:89]
	v_mfma_f32_16x16x32_bf16 v[18:21], v[164:167], v[188:191], v[18:21]
	v_mfma_f32_16x16x32_bf16 v[6:9], v[156:159], v[196:199], v[6:9]
	v_mfma_f32_16x16x32_bf16 v[22:25], v[164:167], v[196:199], v[22:25]
	v_mfma_f32_16x16x32_bf16 v[10:13], v[156:159], v[206:209], v[10:13]
	v_mfma_f32_16x16x32_bf16 v[26:29], v[164:167], v[206:209], v[26:29]
	v_mfma_f32_16x16x32_bf16 v[14:17], v[156:159], v[214:217], v[14:17]
	v_mfma_f32_16x16x32_bf16 v[30:33], v[164:167], v[214:217], v[30:33]
	v_mfma_f32_16x16x32_bf16 v[34:37], v[168:171], v[184:187], v[34:37]
	v_mfma_f32_16x16x32_bf16 v[50:53], v[176:179], v[184:187], v[50:53]
	v_mfma_f32_16x16x32_bf16 v[38:41], v[168:171], v[192:195], v[38:41]
	v_mfma_f32_16x16x32_bf16 v[58:61], v[176:179], v[192:195], v[58:61]
	v_mfma_f32_16x16x32_bf16 v[42:45], v[168:171], v[202:205], v[42:45]
	v_mfma_f32_16x16x32_bf16 v[66:69], v[176:179], v[202:205], v[66:69]
	v_mfma_f32_16x16x32_bf16 v[46:49], v[168:171], v[210:213], v[46:49]
	v_mfma_f32_16x16x32_bf16 v[74:77], v[176:179], v[210:213], v[74:77]
	v_mfma_f32_16x16x32_bf16 v[34:37], v[172:175], v[188:191], v[34:37]
	v_mfma_f32_16x16x32_bf16 v[50:53], v[180:183], v[188:191], v[50:53]
	v_mfma_f32_16x16x32_bf16 v[38:41], v[172:175], v[196:199], v[38:41]
	v_mfma_f32_16x16x32_bf16 v[58:61], v[180:183], v[196:199], v[58:61]
	v_mfma_f32_16x16x32_bf16 v[42:45], v[172:175], v[206:209], v[42:45]
	v_mfma_f32_16x16x32_bf16 v[66:69], v[180:183], v[206:209], v[66:69]
	v_mfma_f32_16x16x32_bf16 v[46:49], v[172:175], v[214:217], v[46:49]
	v_mfma_f32_16x16x32_bf16 v[74:77], v[180:183], v[214:217], v[74:77]
	s_barrier
	s_mov_b32 m0, s56
	v_lshl_add_u64 v[218:219], s[24:25], 0, v[136:137]
	s_cselect_b32 s52, 0, s23
	s_cselect_b32 s53, 0, s22
	s_add_u32 s28, s24, 0x80000
	ds_read_b128 v[184:187], v150 offset:16384
	ds_read_b128 v[188:191], v150 offset:17408
	ds_read_b128 v[192:195], v150 offset:18432
	ds_read_b128 v[196:199], v150 offset:19456
	ds_read_b128 v[202:205], v150 offset:20480
	ds_read_b128 v[206:209], v150 offset:21504
	ds_read_b128 v[210:213], v150 offset:22528
	ds_read_b128 v[214:217], v150 offset:23552
	global_load_lds_dwordx4 v[218:219], off
	v_lshl_add_u64 v[220:221], s[24:25], 0, v[140:141]
	s_mov_b32 m0, s57
	s_addc_u32 s29, s25, 0
	s_add_i32 s54, s54, s33
	global_load_lds_dwordx4 v[220:221], off
	v_lshl_add_u64 v[222:223], s[28:29], 0, v[136:137]
	s_mov_b32 m0, s54
	s_nop 0
	global_load_lds_dwordx4 v[222:223], off
	v_lshl_add_u64 v[222:223], s[28:29], 0, v[140:141]
	s_add_i32 m0, s54, 0x2000
	s_and_b64 s[28:29], s[50:51], s[4:5]
	s_and_b64 s[28:29], s[28:29], exec
	s_cselect_b32 s28, s18, s10
	s_cselect_b32 s29, s19, s11
	s_add_u32 s28, s28, s53
	s_addc_u32 s29, s29, s52
	global_load_lds_dwordx4 v[222:223], off
	v_lshl_add_u64 v[222:223], s[28:29], 0, v[134:135]
	s_mov_b32 m0, s9
	v_lshl_add_u64 v[224:225], s[28:29], 0, v[138:139]
	global_load_lds_dwordx4 v[222:223], off
	s_mov_b32 m0, s38
	s_nop 0
	global_load_lds_dwordx4 v[224:225], off
	s_waitcnt vmcnt(8)
	s_waitcnt lgkmcnt(0)
	s_barrier
	s_waitcnt lgkmcnt(0)
	v_mfma_f32_16x16x32_bf16 v[54:57], v[152:155], v[184:187], v[54:57]
	v_mfma_f32_16x16x32_bf16 v[78:81], v[160:163], v[184:187], v[78:81]
	v_mfma_f32_16x16x32_bf16 v[62:65], v[152:155], v[192:195], v[62:65]
	v_mfma_f32_16x16x32_bf16 v[82:85], v[160:163], v[192:195], v[82:85]
	v_mfma_f32_16x16x32_bf16 v[70:73], v[152:155], v[202:205], v[70:73]
	v_mfma_f32_16x16x32_bf16 v[98:101], v[160:163], v[202:205], v[98:101]
	v_mfma_f32_16x16x32_bf16 v[90:93], v[152:155], v[210:213], v[90:93]
	v_mfma_f32_16x16x32_bf16 v[94:97], v[160:163], v[210:213], v[94:97]
	v_mfma_f32_16x16x32_bf16 v[54:57], v[156:159], v[188:191], v[54:57]
	v_mfma_f32_16x16x32_bf16 v[78:81], v[164:167], v[188:191], v[78:81]
	v_mfma_f32_16x16x32_bf16 v[62:65], v[156:159], v[196:199], v[62:65]
	v_mfma_f32_16x16x32_bf16 v[82:85], v[164:167], v[196:199], v[82:85]
	v_mfma_f32_16x16x32_bf16 v[70:73], v[156:159], v[206:209], v[70:73]
	v_mfma_f32_16x16x32_bf16 v[98:101], v[164:167], v[206:209], v[98:101]
	v_mfma_f32_16x16x32_bf16 v[90:93], v[156:159], v[214:217], v[90:93]
	v_mfma_f32_16x16x32_bf16 v[94:97], v[164:167], v[214:217], v[94:97]
	v_mfma_f32_16x16x32_bf16 v[114:117], v[168:171], v[184:187], v[114:117]
	v_mfma_f32_16x16x32_bf16 v[130:133], v[176:179], v[184:187], v[130:133]
	v_mfma_f32_16x16x32_bf16 v[110:113], v[168:171], v[192:195], v[110:113]
	v_mfma_f32_16x16x32_bf16 v[126:129], v[176:179], v[192:195], v[126:129]
	v_mfma_f32_16x16x32_bf16 v[106:109], v[168:171], v[202:205], v[106:109]
	v_mfma_f32_16x16x32_bf16 v[122:125], v[176:179], v[202:205], v[122:125]
	v_mfma_f32_16x16x32_bf16 v[102:105], v[168:171], v[210:213], v[102:105]
	v_mfma_f32_16x16x32_bf16 v[118:121], v[176:179], v[210:213], v[118:121]
	v_mfma_f32_16x16x32_bf16 v[114:117], v[172:175], v[188:191], v[114:117]
	v_mfma_f32_16x16x32_bf16 v[130:133], v[180:183], v[188:191], v[130:133]
	v_mfma_f32_16x16x32_bf16 v[110:113], v[172:175], v[196:199], v[110:113]
	v_mfma_f32_16x16x32_bf16 v[126:129], v[180:183], v[196:199], v[126:129]
	v_mfma_f32_16x16x32_bf16 v[106:109], v[172:175], v[206:209], v[106:109]
	v_mfma_f32_16x16x32_bf16 v[122:125], v[180:183], v[206:209], v[122:125]
	v_mfma_f32_16x16x32_bf16 v[102:105], v[172:175], v[214:217], v[102:105]
	v_mfma_f32_16x16x32_bf16 v[118:121], v[180:183], v[214:217], v[118:121]
	s_barrier
; #define PG8_STAGE_A(bufoff, base_, nx_, kb_, h_) do { if (GATHER) { if (nx_) PG8_STAGE_G(bufoff, kb_, goN, h_); else PG8_STAGE_G(bufoff, kb_, goC, h_); } \
;         else PG8_STAGE(bufoff, (base_) + (kb_) + (h_) * hstep, voffA); } while (0)
; #define PG8_STAGE(bufoff, gbase, voff) do { _Pragma("unroll") for (int _i = 0; _i < 2; ++_i) \
;         __builtin_amdgcn_global_load_lds((const unsigned*)((const char*)(gbase) + (voff)[_i]), (LAS unsigned*)(lds + (bufoff) + ldsw + _i * 8192), 16, 0, 0); } while (0)
; #define PG8_LDA(dst, b, h) do { _Pragma("unroll") for (int m = 0; m < 4; ++m) _Pragma("unroll") for (int k = 0; k < 2; ++k) dst[m][k] = *(const LAS bf16x8*)(lds + PG8_SA(b, h) + aoff + m * 2048 + k * 1024); } while (0)
; #define PG8_LDB(dst, b, h) do { _Pragma("unroll") for (int n = 0; n < 2; ++n) _Pragma("unroll") for (int k = 0; k < 2; ++k) dst[n][k] = *(const LAS bf16x8*)(lds + PG8_SB(b, h) + boff + n * 2048 + k * 1024); } while (0)
; #define PG8_MMA(ai, bj, At, Bt) do { __builtin_amdgcn_s_setprio(1); _Pragma("unroll") for (int m = 0; m < 4; ++m) _Pragma("unroll") for (int n = 0; n < 2; ++n) _Pragma("unroll") for (int k = 0; k < 2; ++k) \
;         acc[ai][bj][m][n] = __builtin_amdgcn_mfma_f32_16x16x32_bf16(Bt[n][k], At[m][k], acc[ai][bj][m][n], 0, 0, 0); __builtin_amdgcn_s_setprio(0); } while (0)
; #define PG8_WAIT_V(n) asm volatile("s_waitcnt vmcnt(" #n ")" ::: "memory")
; #define PG8_WAIT_L(n) asm volatile("s_waitcnt lgkmcnt(" #n ")" ::: "memory")
; #define PG8_BAR __builtin_amdgcn_s_barrier()
; #define PG8_SCHED __builtin_amdgcn_sched_barrier(0)
; template <class Epi, class Sched, bool GATHER = false>
; __device__ __forceinline__ void gemm_phase(LAS unsigned char* lds, const Gemm g, const Sched& S, const Epi& E, const int tid) {
;     ...
;             PG8_LDB(B0, 1, 0); PG8_LDB(B1, 1, 1); PG8_SCHED; PG8_LDA(At, 1, 0); PG8_STAGE_A(PG8_SA(0, 1), (last ? nA : cA), last, kb2, 1);
;             PG8_WAIT_V(8); PG8_WAIT_L(0); PG8_BAR; PG8_MMA(0, 0, At, B0); PG8_MMA(0, 1, At, B1); PG8_BAR; PG8_SCHED;
;             PG8_LDA(At, 1, 1); PG8_STAGE(PG8_SB(1, 0), b3, voffB); PG8_STAGE(PG8_SB(1, 1), b3 + hstep, voffB); PG8_STAGE_A(PG8_SA(1, 0), (last ? nA : cA), last, kb3, 0);
;             PG8_WAIT_V(8); PG8_WAIT_L(0); PG8_BAR; PG8_MMA(1, 0, At, B0); PG8_MMA(1, 1, At, B1); PG8_BAR; PG8_SCHED;
;     ...
;         }
	s_add_i32 s50, 0, 0x18000
	v_add_u32_e32 v2, s50, v148
	s_add_i32 s51, 0, 0x1c000
	ds_read_b128 v[152:155], v2
	ds_read_b128 v[156:159], v2 offset:1024
	ds_read_b128 v[160:163], v2 offset:2048
	ds_read_b128 v[164:167], v2 offset:3072
	v_add_u32_e32 v2, s51, v148
	ds_read_b128 v[168:171], v2
	ds_read_b128 v[172:175], v2 offset:1024
	ds_read_b128 v[176:179], v2 offset:2048
	ds_read_b128 v[180:183], v2 offset:3072
	s_add_u32 s28, s28, 0x80000
	s_addc_u32 s29, s29, 0
	s_mov_b32 m0, s39
	v_lshl_add_u64 v[226:227], s[28:29], 0, v[134:135]
	ds_read_b128 v[184:187], v150 offset:32768
	ds_read_b128 v[188:191], v150 offset:33792
	ds_read_b128 v[192:195], v150 offset:34816
	ds_read_b128 v[196:199], v150 offset:35840
	ds_read_b128 v[202:205], v150 offset:36864
	ds_read_b128 v[206:209], v150 offset:37888
	ds_read_b128 v[210:213], v150 offset:38912
	ds_read_b128 v[214:217], v150 offset:39936
	global_load_lds_dwordx4 v[226:227], off
	v_lshl_add_u64 v[226:227], s[28:29], 0, v[138:139]
	s_mov_b32 m0, s40
	s_nop 0
	global_load_lds_dwordx4 v[226:227], off
	s_waitcnt vmcnt(8)
	s_waitcnt lgkmcnt(0)
	s_barrier
	s_waitcnt lgkmcnt(0)
	v_mfma_f32_16x16x32_bf16 v[86:89], v[152:155], v[184:187], v[86:89]
	v_mfma_f32_16x16x32_bf16 v[18:21], v[160:163], v[184:187], v[18:21]
	v_mfma_f32_16x16x32_bf16 v[6:9], v[152:155], v[192:195], v[6:9]
	v_mfma_f32_16x16x32_bf16 v[22:25], v[160:163], v[192:195], v[22:25]
	v_mfma_f32_16x16x32_bf16 v[10:13], v[152:155], v[202:205], v[10:13]
	v_mfma_f32_16x16x32_bf16 v[26:29], v[160:163], v[202:205], v[26:29]
	v_mfma_f32_16x16x32_bf16 v[14:17], v[152:155], v[210:213], v[14:17]
	v_mfma_f32_16x16x32_bf16 v[30:33], v[160:163], v[210:213], v[30:33]
	v_mfma_f32_16x16x32_bf16 v[86:89], v[156:159], v[188:191], v[86:89]
	v_mfma_f32_16x16x32_bf16 v[18:21], v[164:167], v[188:191], v[18:21]
	v_mfma_f32_16x16x32_bf16 v[6:9], v[156:159], v[196:199], v[6:9]
	v_mfma_f32_16x16x32_bf16 v[22:25], v[164:167], v[196:199], v[22:25]
	v_mfma_f32_16x16x32_bf16 v[10:13], v[156:159], v[206:209], v[10:13]
	v_mfma_f32_16x16x32_bf16 v[26:29], v[164:167], v[206:209], v[26:29]
	v_mfma_f32_16x16x32_bf16 v[14:17], v[156:159], v[214:217], v[14:17]
	v_mfma_f32_16x16x32_bf16 v[30:33], v[164:167], v[214:217], v[30:33]
	v_mfma_f32_16x16x32_bf16 v[34:37], v[168:171], v[184:187], v[34:37]
	v_mfma_f32_16x16x32_bf16 v[50:53], v[176:179], v[184:187], v[50:53]
	v_mfma_f32_16x16x32_bf16 v[38:41], v[168:171], v[192:195], v[38:41]
	v_mfma_f32_16x16x32_bf16 v[58:61], v[176:179], v[192:195], v[58:61]
	v_mfma_f32_16x16x32_bf16 v[42:45], v[168:171], v[202:205], v[42:45]
	v_mfma_f32_16x16x32_bf16 v[66:69], v[176:179], v[202:205], v[66:69]
	v_mfma_f32_16x16x32_bf16 v[46:49], v[168:171], v[210:213], v[46:49]
	v_mfma_f32_16x16x32_bf16 v[74:77], v[176:179], v[210:213], v[74:77]
	v_mfma_f32_16x16x32_bf16 v[34:37], v[172:175], v[188:191], v[34:37]
	v_mfma_f32_16x16x32_bf16 v[50:53], v[180:183], v[188:191], v[50:53]
	v_mfma_f32_16x16x32_bf16 v[38:41], v[172:175], v[196:199], v[38:41]
	v_mfma_f32_16x16x32_bf16 v[58:61], v[180:183], v[196:199], v[58:61]
	v_mfma_f32_16x16x32_bf16 v[42:45], v[172:175], v[206:209], v[42:45]
	v_mfma_f32_16x16x32_bf16 v[66:69], v[180:183], v[206:209], v[66:69]
	v_mfma_f32_16x16x32_bf16 v[46:49], v[172:175], v[214:217], v[46:49]
	v_mfma_f32_16x16x32_bf16 v[74:77], v[180:183], v[214:217], v[74:77]
	s_barrier
	s_add_i32 s28, s50, s33
	v_lshl_add_u64 v[218:219], v[218:219], 0, s[0:1]
	s_mov_b32 m0, s28
	ds_read_b128 v[184:187], v150 offset:49152
	ds_read_b128 v[188:191], v150 offset:50176
	ds_read_b128 v[192:195], v150 offset:51200
	ds_read_b128 v[196:199], v150 offset:52224
	ds_read_b128 v[202:205], v150 offset:53248
	ds_read_b128 v[206:209], v150 offset:54272
	ds_read_b128 v[210:213], v150 offset:55296
	ds_read_b128 v[214:217], v150 offset:56320
	global_load_lds_dwordx4 v[218:219], off
	s_add_i32 m0, s28, 0x2000
	s_add_u32 s24, s24, 0x80080
	v_lshl_add_u64 v[218:219], v[220:221], 0, s[0:1]
	s_addc_u32 s25, s25, 0
	s_add_i32 s28, s51, s33
	global_load_lds_dwordx4 v[218:219], off
	v_lshl_add_u64 v[218:219], s[24:25], 0, v[136:137]
	s_mov_b32 m0, s28
	s_nop 0
	global_load_lds_dwordx4 v[218:219], off
	v_lshl_add_u64 v[218:219], s[24:25], 0, v[140:141]
	s_add_i32 m0, s28, 0x2000
	s_nop 0
	global_load_lds_dwordx4 v[218:219], off
	v_lshl_add_u64 v[218:219], v[222:223], 0, s[0:1]
	s_mov_b32 m0, s42
	s_nop 0
	global_load_lds_dwordx4 v[218:219], off
	v_lshl_add_u64 v[218:219], v[224:225], 0, s[0:1]
	s_mov_b32 m0, s43
	s_nop 0
	global_load_lds_dwordx4 v[218:219], off
	s_waitcnt vmcnt(8)
	s_waitcnt lgkmcnt(0)
	s_barrier
	s_waitcnt lgkmcnt(0)
	v_mfma_f32_16x16x32_bf16 v[54:57], v[152:155], v[184:187], v[54:57]
	v_mfma_f32_16x16x32_bf16 v[78:81], v[160:163], v[184:187], v[78:81]
	v_mfma_f32_16x16x32_bf16 v[62:65], v[152:155], v[192:195], v[62:65]
	v_mfma_f32_16x16x32_bf16 v[82:85], v[160:163], v[192:195], v[82:85]
	v_mfma_f32_16x16x32_bf16 v[70:73], v[152:155], v[202:205], v[70:73]
	v_mfma_f32_16x16x32_bf16 v[98:101], v[160:163], v[202:205], v[98:101]
	v_mfma_f32_16x16x32_bf16 v[90:93], v[152:155], v[210:213], v[90:93]
	v_mfma_f32_16x16x32_bf16 v[94:97], v[160:163], v[210:213], v[94:97]
	v_mfma_f32_16x16x32_bf16 v[54:57], v[156:159], v[188:191], v[54:57]
	v_mfma_f32_16x16x32_bf16 v[78:81], v[164:167], v[188:191], v[78:81]
	v_mfma_f32_16x16x32_bf16 v[62:65], v[156:159], v[196:199], v[62:65]
	v_mfma_f32_16x16x32_bf16 v[82:85], v[164:167], v[196:199], v[82:85]
	v_mfma_f32_16x16x32_bf16 v[70:73], v[156:159], v[206:209], v[70:73]
	v_mfma_f32_16x16x32_bf16 v[98:101], v[164:167], v[206:209], v[98:101]
	v_mfma_f32_16x16x32_bf16 v[90:93], v[156:159], v[214:217], v[90:93]
	v_mfma_f32_16x16x32_bf16 v[94:97], v[164:167], v[214:217], v[94:97]
	v_mfma_f32_16x16x32_bf16 v[114:117], v[168:171], v[184:187], v[114:117]
	v_mfma_f32_16x16x32_bf16 v[130:133], v[176:179], v[184:187], v[130:133]
	v_mfma_f32_16x16x32_bf16 v[110:113], v[168:171], v[192:195], v[110:113]
	v_mfma_f32_16x16x32_bf16 v[126:129], v[176:179], v[192:195], v[126:129]
	v_mfma_f32_16x16x32_bf16 v[106:109], v[168:171], v[202:205], v[106:109]
	v_mfma_f32_16x16x32_bf16 v[122:125], v[176:179], v[202:205], v[122:125]
	v_mfma_f32_16x16x32_bf16 v[102:105], v[168:171], v[210:213], v[102:105]
	v_mfma_f32_16x16x32_bf16 v[118:121], v[176:179], v[210:213], v[118:121]
	v_mfma_f32_16x16x32_bf16 v[114:117], v[172:175], v[188:191], v[114:117]
	v_mfma_f32_16x16x32_bf16 v[130:133], v[180:183], v[188:191], v[130:133]
	v_mfma_f32_16x16x32_bf16 v[110:113], v[172:175], v[196:199], v[110:113]
	v_mfma_f32_16x16x32_bf16 v[126:129], v[180:183], v[196:199], v[126:129]
	v_mfma_f32_16x16x32_bf16 v[106:109], v[172:175], v[206:209], v[106:109]
	v_mfma_f32_16x16x32_bf16 v[122:125], v[180:183], v[206:209], v[122:125]
	v_mfma_f32_16x16x32_bf16 v[102:105], v[172:175], v[214:217], v[102:105]
	v_mfma_f32_16x16x32_bf16 v[118:121], v[180:183], v[214:217], v[118:121]
	s_barrier
	s_add_i32 s49, s49, 2
	s_cmp_gt_u32 s49, 29
	s_mov_b64 s[28:29], s[22:23]
	s_cbranch_scc0 .LBB0_1128
; __device__ __forceinline__ unsigned cvt_pk_bf16(float lo, float hi) { const f32x2 v = {lo, hi}; const bf16x2_t b = __builtin_convertvector(v, bf16x2_t); return __builtin_bit_cast(unsigned, b); }
; #define ZERO4() ((f32x4){opaque0(), 0.f, 0.f, 0.f} * 0.f)
; #define PG8_BAR __builtin_amdgcn_s_barrier()
;     __device__ __forceinline__ void operator()(const f32x4 (&acc)[2][2][4][2], const Unit& u, int wr, int wc, int fr, int fq) const {
;         const int row0 = u.pm * BM + wr * 64 + fr, col0 = u.pn * BM + wc * 32 + 8 * fq;
; #pragma unroll
;         for (int ai = 0; ai < 2; ++ai)
; #pragma unroll
;             for (int m = 0; m < 4; ++m) { bf16_t* rowp = O + (size_t)(row0 + ai * HALF + m * 16) * ldc + col0;
; #pragma unroll
;                 for (int bj = 0; bj < 2; ++bj) { const f32x4 v0 = acc[ai][bj][m][0], v1 = acc[ai][bj][m][1];
;                     u32x4 w; w.x = cvt_pk_bf16(v0[0], v0[1]); w.y = cvt_pk_bf16(v0[2], v0[3]); w.z = cvt_pk_bf16(v1[0], v1[1]); w.w = cvt_pk_bf16(v1[2], v1[3]);
;                     *(u32x4*)(rowp + bj * HALF) = w; } }
; template <class Epi, class Sched, bool GATHER = false>
; __device__ __forceinline__ void gemm_phase(LAS unsigned char* lds, const Gemm g, const Sched& S, const Epi& E, const int tid) {
;     ...
;         if (wr == 0) PG8_BAR;
;         E(acc, cur, wr, wc, fr, fq);
;         if (!has_next) break;
; #pragma unroll
;         for (int a = 0; a < 2; ++a)
; #pragma unroll
;             for (int b = 0; b < 2; ++b)
; #pragma unroll
;                 for (int m = 0; m < 4; ++m)
; #pragma unroll
;                     for (int n = 0; n < 2; ++n) acc[a][b][m][n] = ZERO4();
;         cur = nxt; cA = nA; cB = nB; ++ui;
;         if (GATHER) {
; #pragma unroll
;             for (int h_ = 0; h_ < 2; ++h_) { goC[h_][0] = goN[h_][0]; goC[h_][1] = goN[h_][1]; } }
;         if (wr == 1) PG8_BAR;
.Lpeel1_exit:
	s_and_b64 vcc, exec, s[12:13]
	s_cbranch_vccz .LBB0_1131
	s_barrier
.LBB0_1131:
	v_lshl_or_b32 v4, s44, 8, v149
	v_lshl_add_u32 v2, s8, 8, v1
	v_ashrrev_i32_e32 v5, 31, v4
	v_mov_b64_e32 v[146:147], s[6:7]
	s_movk_i32 s8, 0x1080
	v_mad_i64_i32 v[152:153], s[10:11], v2, s8, v[146:147]
	v_lshlrev_b64 v[154:155], 1, v[4:5]
	v_lshl_add_u64 v[4:5], v[152:153], 0, v[154:155]
	v_cvt_pk_bf16_f32 v86, v86, v87
	v_cvt_pk_bf16_f32 v87, v88, v89
	v_cvt_pk_bf16_f32 v88, v18, v19
	v_cvt_pk_bf16_f32 v89, v20, v21
	v_cvt_pk_bf16_f32 v18, v34, v35
	v_cvt_pk_bf16_f32 v19, v36, v37
	v_cvt_pk_bf16_f32 v20, v50, v51
	v_cvt_pk_bf16_f32 v21, v52, v53
	global_store_dwordx4 v[4:5], v[86:89], off
	global_store_dwordx4 v[4:5], v[18:21], off offset:256
	v_or_b32_e32 v4, 16, v2
	v_mad_i64_i32 v[4:5], s[10:11], v4, s8, v[146:147]
	v_lshl_add_u64 v[18:19], v[4:5], 0, v[154:155]
	v_cvt_pk_bf16_f32 v4, v6, v7
	v_cvt_pk_bf16_f32 v5, v8, v9
	v_cvt_pk_bf16_f32 v6, v22, v23
	v_cvt_pk_bf16_f32 v7, v24, v25
	global_store_dwordx4 v[18:19], v[4:7], off
	s_andn2_b64 vcc, exec, s[4:5]
	s_mov_b64 s[4:5], -1
	v_cvt_pk_bf16_f32 v4, v38, v39
	v_cvt_pk_bf16_f32 v5, v40, v41
	v_cvt_pk_bf16_f32 v6, v58, v59
	v_cvt_pk_bf16_f32 v7, v60, v61
	global_store_dwordx4 v[18:19], v[4:7], off offset:256
	s_nop 1
	v_or_b32_e32 v4, 32, v2
	v_mad_i64_i32 v[4:5], s[10:11], v4, s8, v[146:147]
	v_lshl_add_u64 v[8:9], v[4:5], 0, v[154:155]
	v_cvt_pk_bf16_f32 v4, v10, v11
	v_cvt_pk_bf16_f32 v5, v12, v13
	v_cvt_pk_bf16_f32 v6, v26, v27
	v_cvt_pk_bf16_f32 v7, v28, v29
	global_store_dwordx4 v[8:9], v[4:7], off
	s_nop 1
	v_cvt_pk_bf16_f32 v4, v42, v43
	v_cvt_pk_bf16_f32 v5, v44, v45
	v_cvt_pk_bf16_f32 v6, v66, v67
	v_cvt_pk_bf16_f32 v7, v68, v69
	global_store_dwordx4 v[8:9], v[4:7], off offset:256
	s_nop 1
	v_or_b32_e32 v4, 48, v2
	v_mad_i64_i32 v[4:5], s[10:11], v4, s8, v[146:147]
	v_lshl_add_u64 v[8:9], v[4:5], 0, v[154:155]
	v_cvt_pk_bf16_f32 v4, v14, v15
	v_cvt_pk_bf16_f32 v5, v16, v17
	v_cvt_pk_bf16_f32 v6, v30, v31
	v_cvt_pk_bf16_f32 v7, v32, v33
	global_store_dwordx4 v[8:9], v[4:7], off
	s_nop 1
	v_cvt_pk_bf16_f32 v4, v46, v47
	v_cvt_pk_bf16_f32 v5, v48, v49
	v_cvt_pk_bf16_f32 v6, v74, v75
	v_cvt_pk_bf16_f32 v7, v76, v77
	global_store_dwordx4 v[8:9], v[4:7], off offset:256
	s_nop 1
	v_add_u32_e32 v4, 0x80, v2
	v_mad_i64_i32 v[4:5], s[10:11], v4, s8, v[146:147]
	v_lshl_add_u64 v[8:9], v[4:5], 0, v[154:155]
	v_cvt_pk_bf16_f32 v4, v54, v55
	v_cvt_pk_bf16_f32 v5, v56, v57
	v_cvt_pk_bf16_f32 v6, v78, v79
	v_cvt_pk_bf16_f32 v7, v80, v81
	global_store_dwordx4 v[8:9], v[4:7], off
	s_nop 1
	v_cvt_pk_bf16_f32 v4, v114, v115
	v_cvt_pk_bf16_f32 v5, v116, v117
	v_cvt_pk_bf16_f32 v6, v130, v131
	v_cvt_pk_bf16_f32 v7, v132, v133
	global_store_dwordx4 v[8:9], v[4:7], off offset:256
	s_nop 1
	v_add_u32_e32 v4, 0x90, v2
	v_mad_i64_i32 v[4:5], s[10:11], v4, s8, v[146:147]
	v_lshl_add_u64 v[8:9], v[4:5], 0, v[154:155]
	v_cvt_pk_bf16_f32 v4, v62, v63
	v_cvt_pk_bf16_f32 v5, v64, v65
	v_cvt_pk_bf16_f32 v6, v82, v83
	v_cvt_pk_bf16_f32 v7, v84, v85
	global_store_dwordx4 v[8:9], v[4:7], off
	s_nop 1
	v_cvt_pk_bf16_f32 v4, v110, v111
	v_cvt_pk_bf16_f32 v5, v112, v113
	v_cvt_pk_bf16_f32 v6, v126, v127
	v_cvt_pk_bf16_f32 v7, v128, v129
	global_store_dwordx4 v[8:9], v[4:7], off offset:256
	s_nop 1
	v_add_u32_e32 v4, 0xa0, v2
	v_mad_i64_i32 v[4:5], s[10:11], v4, s8, v[146:147]
	v_lshl_add_u64 v[8:9], v[4:5], 0, v[154:155]
	v_cvt_pk_bf16_f32 v4, v70, v71
	v_cvt_pk_bf16_f32 v5, v72, v73
	v_cvt_pk_bf16_f32 v6, v98, v99
	v_cvt_pk_bf16_f32 v7, v100, v101
	global_store_dwordx4 v[8:9], v[4:7], off
	v_add_u32_e32 v2, 0xb0, v2
	s_nop 0
	v_cvt_pk_bf16_f32 v4, v106, v107
	v_cvt_pk_bf16_f32 v5, v108, v109
	v_cvt_pk_bf16_f32 v6, v122, v123
	v_cvt_pk_bf16_f32 v7, v124, v125
	global_store_dwordx4 v[8:9], v[4:7], off offset:256
	s_nop 1
	v_mad_i64_i32 v[4:5], s[10:11], v2, s8, v[146:147]
	v_lshl_add_u64 v[8:9], v[4:5], 0, v[154:155]
	v_cvt_pk_bf16_f32 v4, v90, v91
	v_cvt_pk_bf16_f32 v5, v92, v93
	v_cvt_pk_bf16_f32 v6, v94, v95
	v_cvt_pk_bf16_f32 v7, v96, v97
	global_store_dwordx4 v[8:9], v[4:7], off
	s_nop 1
	v_cvt_pk_bf16_f32 v4, v102, v103
	v_cvt_pk_bf16_f32 v5, v104, v105
	v_cvt_pk_bf16_f32 v6, v118, v119
	v_cvt_pk_bf16_f32 v7, v120, v121
	global_store_dwordx4 v[8:9], v[4:7], off offset:256
	s_cbranch_vccnz .LBB0_1120
	v_mov_b32_e32 v2, v3
	s_andn2_b64 vcc, exec, s[2:3]
	s_cbranch_vccnz .LBB0_1119
	s_barrier
	s_branch .LBB0_1119

; #define ZERO4() ((f32x4){opaque0(), 0.f, 0.f, 0.f} * 0.f)
; template <class Epi, class Sched, bool GATHER = false>
; __device__ __forceinline__ void gemm_phase(LAS unsigned char* lds, const Gemm g, const Sched& S, const Epi& E, const int tid) {
;     ...
;     f32x4 acc[2][2][4][2];
; #pragma unroll
;     for (int a = 0; a < 2; ++a)
; #pragma unroll
;         for (int b = 0; b < 2; ++b)
; #pragma unroll
;             for (int m = 0; m < 4; ++m)
; #pragma unroll
;                 for (int n = 0; n < 2; ++n) acc[a][b][m][n] = ZERO4();
.LBB0_1362:
	v_mov_b32_e32 v4, v3
	v_mov_b32_e32 v5, v3
	v_mul_f32_e32 v2, 0, v2
	s_mov_b64 s[8:9], 0

; #define LAS __attribute__((address_space(3)))
;     __device__ __forceinline__ bool next(int i, Unit& u) const { if (i >= per * reps) return false; return StaticOrder::next(i % per, u); }
; #define PG8_STAGE_A(bufoff, base_, nx_, kb_, h_) do { if (GATHER) { if (nx_) PG8_STAGE_G(bufoff, kb_, goN, h_); else PG8_STAGE_G(bufoff, kb_, goC, h_); } \
;         else PG8_STAGE(bufoff, (base_) + (kb_) + (h_) * hstep, voffA); } while (0)
; #define PG8_STAGE(bufoff, gbase, voff) do { _Pragma("unroll") for (int _i = 0; _i < 2; ++_i) \
;         __builtin_amdgcn_global_load_lds((const unsigned*)((const char*)(gbase) + (voff)[_i]), (LAS unsigned*)(lds + (bufoff) + ldsw + _i * 8192), 16, 0, 0); } while (0)
; #define PG8_WAIT_V(n) asm volatile("s_waitcnt vmcnt(" #n ")" ::: "memory")
; #define PG8_WAIT_L(n) asm volatile("s_waitcnt lgkmcnt(" #n ")" ::: "memory")
; template <class Epi, class Sched, bool GATHER = false>
; __device__ __forceinline__ void gemm_phase(LAS unsigned char* lds, const Gemm g, const Sched& S, const Epi& E, const int tid) {
;     ...
;         const bool has_next = S.next(ui + 1, nxt);
;         const char* nA = has_next ? (const char*)g.A + (size_t)nxt.pm * tstep : cA; const char* nB = has_next ? (const char*)g.Bt + (size_t)nxt.pb * tstep : cB;
;         if (GATHER && has_next && wid < 4) __builtin_amdgcn_global_load_lds((const unsigned*)(g.rowmap + nxt.rb + tid), (LAS unsigned*)(lds + STAGE_BYTES + ((ui + 1) & 1) * 1024 + wid * 256), 4, 0, 0);
;         for (int t = 0; t < nt; t += 2) {
;             const bool last = (t == nt - 2);
;             const char* a1 = cA + (size_t)(t + 1) * kstep;
;             const char* a2 = last ? nA : cA + (size_t)(t + 2) * kstep; const char* b2 = last ? nB : cB + (size_t)(t + 2) * kstep;
;             const char* a3 = a2 + kstep; const char* b3 = b2 + kstep;
;     ...
;             const size_t kb1 = (size_t)(t + 1) * kstep, kb2 = last ? (size_t)0 : (size_t)(t + 2) * kstep, kb3 = kb2 + kstep;
;             PG8_LDB(B0, 0, 0); PG8_LDB(B1, 0, 1); PG8_SCHED; PG8_LDA(At, 0, 0); PG8_STAGE_A(PG8_SA(1, 1), cA, false, kb1, 1);
;             PG8_WAIT_V(8); PG8_WAIT_L(0); PG8_BAR; PG8_MMA(0, 0, At, B0); PG8_MMA(0, 1, At, B1); PG8_BAR; PG8_SCHED;
;             PG8_LDA(At, 0, 1); PG8_STAGE(PG8_SB(0, 0), b2, voffB); PG8_STAGE(PG8_SB(0, 1), b2 + hstep, voffB); PG8_STAGE_A(PG8_SA(0, 0), (last ? nA : cA), last, kb2, 0);
.LBB0_1366:
	s_ashr_i32 s23, s22, 31
	s_lshl_b64 s[24:25], s[22:23], 20
	s_add_u32 s24, s12, s24
	s_addc_u32 s25, s13, s25
	s_ashr_i32 s21, s20, 31
	s_lshl_b64 s[28:29], s[20:21], 20
	s_add_u32 s28, s14, s28
	s_addc_u32 s29, s15, s29
	s_and_b64 s[38:39], s[8:9], exec
	s_cselect_b32 s21, s29, s37
	s_cselect_b32 s23, s28, s36
	s_add_u32 s59, s36, 0x100
	s_addc_u32 s60, s37, 0
	s_add_u32 s36, s34, 0x80080
	s_addc_u32 s37, s35, 0
	v_lshl_add_u64 v[4:5], s[36:37], 0, v[144:145]
	v_lshl_add_u64 v[148:149], s[36:37], 0, v[146:147]
	s_mov_b32 s61, -2
	s_mov_b64 s[40:41], 0
	s_add_u32 s62, s59, s40
	s_addc_u32 s63, s60, s41
	s_add_u32 s36, s40, 0x100
	s_addc_u32 s37, s41, 0
	s_cmp_eq_u32 s61, 28
	s_cselect_b64 s[42:43], -1, 0
	s_and_b64 s[38:39], s[42:43], exec
	s_cselect_b32 s39, s21, s63
	s_cselect_b32 s38, s23, s62
	s_cselect_b32 s62, 0, s36
	s_add_i32 s63, 0, 0x10000
	v_add_u32_e32 v2, s63, v135
	s_add_i32 s64, 0, 0x14000
	ds_read_b128 v[152:155], v2
	ds_read_b128 v[156:159], v2 offset:1024
	ds_read_b128 v[160:163], v2 offset:2048
	ds_read_b128 v[164:167], v2 offset:3072
	v_add_u32_e32 v2, s64, v135
	ds_read_b128 v[168:171], v2
	ds_read_b128 v[172:175], v2 offset:1024
	ds_read_b128 v[176:179], v2 offset:2048
	ds_read_b128 v[180:183], v2 offset:3072
	v_lshl_add_u64 v[218:219], v[4:5], 0, s[40:41]
	s_add_i32 m0, s31, 0xc000
	ds_read_b128 v[184:187], v151
	ds_read_b128 v[188:191], v151 offset:1024
	ds_read_b128 v[192:195], v151 offset:2048
	ds_read_b128 v[196:199], v151 offset:3072
	ds_read_b128 v[202:205], v151 offset:4096
	ds_read_b128 v[206:209], v151 offset:5120
	ds_read_b128 v[210:213], v151 offset:6144
	ds_read_b128 v[214:217], v151 offset:7168
	global_load_lds_dwordx4 v[218:219], off
	v_lshl_add_u64 v[218:219], v[148:149], 0, s[40:41]
	s_add_i32 m0, s31, 0xe000
	s_nop 0
	global_load_lds_dwordx4 v[218:219], off
	s_waitcnt vmcnt(8)
	s_waitcnt lgkmcnt(0)
	s_barrier
	s_waitcnt lgkmcnt(0)
	v_mfma_f32_16x16x32_bf16 v[122:125], v[152:155], v[184:187], 0
	v_mfma_f32_16x16x32_bf16 v[74:77], v[160:163], v[184:187], 0
	v_mfma_f32_16x16x32_bf16 v[58:61], v[152:155], v[192:195], 0
	v_mfma_f32_16x16x32_bf16 v[50:53], v[160:163], v[192:195], 0
	v_mfma_f32_16x16x32_bf16 v[38:41], v[152:155], v[202:205], 0
	v_mfma_f32_16x16x32_bf16 v[34:37], v[160:163], v[202:205], 0
	v_mfma_f32_16x16x32_bf16 v[22:25], v[152:155], v[210:213], 0
	v_mfma_f32_16x16x32_bf16 v[18:21], v[160:163], v[210:213], 0
	v_mfma_f32_16x16x32_bf16 v[122:125], v[156:159], v[188:191], v[122:125]
	v_mfma_f32_16x16x32_bf16 v[74:77], v[164:167], v[188:191], v[74:77]
	v_mfma_f32_16x16x32_bf16 v[58:61], v[156:159], v[196:199], v[58:61]
	v_mfma_f32_16x16x32_bf16 v[50:53], v[164:167], v[196:199], v[50:53]
	v_mfma_f32_16x16x32_bf16 v[38:41], v[156:159], v[206:209], v[38:41]
	v_mfma_f32_16x16x32_bf16 v[34:37], v[164:167], v[206:209], v[34:37]
	v_mfma_f32_16x16x32_bf16 v[22:25], v[156:159], v[214:217], v[22:25]
	v_mfma_f32_16x16x32_bf16 v[18:21], v[164:167], v[214:217], v[18:21]
	v_mfma_f32_16x16x32_bf16 v[106:109], v[168:171], v[184:187], 0
	v_mfma_f32_16x16x32_bf16 v[110:113], v[176:179], v[184:187], 0
	v_mfma_f32_16x16x32_bf16 v[90:93], v[168:171], v[192:195], 0
	v_mfma_f32_16x16x32_bf16 v[94:97], v[176:179], v[192:195], 0
	v_mfma_f32_16x16x32_bf16 v[66:69], v[168:171], v[202:205], 0
	v_mfma_f32_16x16x32_bf16 v[70:73], v[176:179], v[202:205], 0
	v_mfma_f32_16x16x32_bf16 v[42:45], v[168:171], v[210:213], 0
	v_mfma_f32_16x16x32_bf16 v[46:49], v[176:179], v[210:213], 0
	v_mfma_f32_16x16x32_bf16 v[106:109], v[172:175], v[188:191], v[106:109]
	v_mfma_f32_16x16x32_bf16 v[110:113], v[180:183], v[188:191], v[110:113]
	v_mfma_f32_16x16x32_bf16 v[90:93], v[172:175], v[196:199], v[90:93]
	v_mfma_f32_16x16x32_bf16 v[94:97], v[180:183], v[196:199], v[94:97]
	v_mfma_f32_16x16x32_bf16 v[66:69], v[172:175], v[206:209], v[66:69]
	v_mfma_f32_16x16x32_bf16 v[70:73], v[180:183], v[206:209], v[70:73]
	v_mfma_f32_16x16x32_bf16 v[42:45], v[172:175], v[214:217], v[42:45]
	v_mfma_f32_16x16x32_bf16 v[46:49], v[180:183], v[214:217], v[46:49]
	s_barrier
	s_add_i32 s40, s63, s50
	v_lshl_add_u64 v[218:219], s[38:39], 0, v[140:141]
	s_mov_b32 m0, s40
	ds_read_b128 v[184:187], v151 offset:16384
	ds_read_b128 v[188:191], v151 offset:17408
	ds_read_b128 v[192:195], v151 offset:18432
	ds_read_b128 v[196:199], v151 offset:19456
	ds_read_b128 v[202:205], v151 offset:20480
	ds_read_b128 v[206:209], v151 offset:21504
	ds_read_b128 v[210:213], v151 offset:22528
	ds_read_b128 v[214:217], v151 offset:23552
	global_load_lds_dwordx4 v[218:219], off
	s_add_i32 m0, s40, 0x2000
	s_add_u32 s40, s38, 0x80000
	v_lshl_add_u64 v[220:221], s[38:39], 0, v[136:137]
	s_addc_u32 s41, s39, 0
	s_add_i32 s63, s64, s50
	global_load_lds_dwordx4 v[220:221], off
	v_lshl_add_u64 v[222:223], s[40:41], 0, v[140:141]
	s_mov_b32 m0, s63
	s_nop 0
	global_load_lds_dwordx4 v[222:223], off
	v_lshl_add_u64 v[222:223], s[40:41], 0, v[136:137]
	s_add_i32 m0, s63, 0x2000
	s_and_b64 s[40:41], s[8:9], s[42:43]
	s_and_b64 s[40:41], s[40:41], exec
	s_cselect_b32 s40, s24, s34
	s_cselect_b32 s41, s25, s35
	s_add_u32 s40, s40, s62
	s_addc_u32 s41, s41, 0
	global_load_lds_dwordx4 v[222:223], off
	v_lshl_add_u64 v[222:223], s[40:41], 0, v[142:143]
	s_mov_b32 m0, s31
	v_lshl_add_u64 v[224:225], s[40:41], 0, v[138:139]
	global_load_lds_dwordx4 v[222:223], off
	s_mov_b32 m0, s52
	s_nop 0
	global_load_lds_dwordx4 v[224:225], off
	s_waitcnt vmcnt(8)
	s_waitcnt lgkmcnt(0)
	s_barrier
; #define PG8_STAGE_A(bufoff, base_, nx_, kb_, h_) do { if (GATHER) { if (nx_) PG8_STAGE_G(bufoff, kb_, goN, h_); else PG8_STAGE_G(bufoff, kb_, goC, h_); } \
;         else PG8_STAGE(bufoff, (base_) + (kb_) + (h_) * hstep, voffA); } while (0)
; #define PG8_LDA(dst, b, h) do { _Pragma("unroll") for (int m = 0; m < 4; ++m) _Pragma("unroll") for (int k = 0; k < 2; ++k) dst[m][k] = *(const LAS bf16x8*)(lds + PG8_SA(b, h) + aoff + m * 2048 + k * 1024); } while (0)
; #define PG8_LDB(dst, b, h) do { _Pragma("unroll") for (int n = 0; n < 2; ++n) _Pragma("unroll") for (int k = 0; k < 2; ++k) dst[n][k] = *(const LAS bf16x8*)(lds + PG8_SB(b, h) + boff + n * 2048 + k * 1024); } while (0)
; #define PG8_MMA(ai, bj, At, Bt) do { __builtin_amdgcn_s_setprio(1); _Pragma("unroll") for (int m = 0; m < 4; ++m) _Pragma("unroll") for (int n = 0; n < 2; ++n) _Pragma("unroll") for (int k = 0; k < 2; ++k) \
;         acc[ai][bj][m][n] = __builtin_amdgcn_mfma_f32_16x16x32_bf16(Bt[n][k], At[m][k], acc[ai][bj][m][n], 0, 0, 0); __builtin_amdgcn_s_setprio(0); } while (0)
; #define PG8_WAIT_V(n) asm volatile("s_waitcnt vmcnt(" #n ")" ::: "memory")
; #define PG8_WAIT_L(n) asm volatile("s_waitcnt lgkmcnt(" #n ")" ::: "memory")
; #define PG8_BAR __builtin_amdgcn_s_barrier()
; #define PG8_SCHED __builtin_amdgcn_sched_barrier(0)
; template <class Epi, class Sched, bool GATHER = false>
; __device__ __forceinline__ void gemm_phase(LAS unsigned char* lds, const Gemm g, const Sched& S, const Epi& E, const int tid) {
;     ...
;             PG8_WAIT_V(8); PG8_WAIT_L(0); PG8_BAR; PG8_MMA(1, 0, At, B0); PG8_MMA(1, 1, At, B1); PG8_BAR; PG8_SCHED;
;             PG8_LDB(B0, 1, 0); PG8_LDB(B1, 1, 1); PG8_SCHED; PG8_LDA(At, 1, 0); PG8_STAGE_A(PG8_SA(0, 1), (last ? nA : cA), last, kb2, 1);
;             PG8_WAIT_V(8); PG8_WAIT_L(0); PG8_BAR; PG8_MMA(0, 0, At, B0); PG8_MMA(0, 1, At, B1); PG8_BAR; PG8_SCHED;
	s_waitcnt lgkmcnt(0)
	v_mfma_f32_16x16x32_bf16 v[30:33], v[152:155], v[184:187], 0
	v_mfma_f32_16x16x32_bf16 v[26:29], v[160:163], v[184:187], 0
	v_mfma_f32_16x16x32_bf16 v[14:17], v[152:155], v[192:195], 0
	v_mfma_f32_16x16x32_bf16 v[10:13], v[160:163], v[192:195], 0
	v_mfma_f32_16x16x32_bf16 v[6:9], v[152:155], v[202:205], 0
	v_mfma_f32_16x16x32_bf16 v[78:81], v[160:163], v[202:205], 0
	v_mfma_f32_16x16x32_bf16 v[62:65], v[152:155], v[210:213], 0
	v_mfma_f32_16x16x32_bf16 v[54:57], v[160:163], v[210:213], 0
	v_mfma_f32_16x16x32_bf16 v[30:33], v[156:159], v[188:191], v[30:33]
	v_mfma_f32_16x16x32_bf16 v[26:29], v[164:167], v[188:191], v[26:29]
	v_mfma_f32_16x16x32_bf16 v[14:17], v[156:159], v[196:199], v[14:17]
	v_mfma_f32_16x16x32_bf16 v[10:13], v[164:167], v[196:199], v[10:13]
	v_mfma_f32_16x16x32_bf16 v[6:9], v[156:159], v[206:209], v[6:9]
	v_mfma_f32_16x16x32_bf16 v[78:81], v[164:167], v[206:209], v[78:81]
	v_mfma_f32_16x16x32_bf16 v[62:65], v[156:159], v[214:217], v[62:65]
	v_mfma_f32_16x16x32_bf16 v[54:57], v[164:167], v[214:217], v[54:57]
	v_mfma_f32_16x16x32_bf16 v[130:133], v[168:171], v[184:187], 0
	v_mfma_f32_16x16x32_bf16 v[126:129], v[176:179], v[184:187], 0
	v_mfma_f32_16x16x32_bf16 v[118:121], v[168:171], v[192:195], 0
	v_mfma_f32_16x16x32_bf16 v[114:117], v[176:179], v[192:195], 0
	v_mfma_f32_16x16x32_bf16 v[102:105], v[168:171], v[202:205], 0
	v_mfma_f32_16x16x32_bf16 v[98:101], v[176:179], v[202:205], 0
	v_mfma_f32_16x16x32_bf16 v[86:89], v[168:171], v[210:213], 0
	v_mfma_f32_16x16x32_bf16 v[82:85], v[176:179], v[210:213], 0
	v_mfma_f32_16x16x32_bf16 v[130:133], v[172:175], v[188:191], v[130:133]
	v_mfma_f32_16x16x32_bf16 v[126:129], v[180:183], v[188:191], v[126:129]
	v_mfma_f32_16x16x32_bf16 v[118:121], v[172:175], v[196:199], v[118:121]
	v_mfma_f32_16x16x32_bf16 v[114:117], v[180:183], v[196:199], v[114:117]
	v_mfma_f32_16x16x32_bf16 v[102:105], v[172:175], v[206:209], v[102:105]
	v_mfma_f32_16x16x32_bf16 v[98:101], v[180:183], v[206:209], v[98:101]
	v_mfma_f32_16x16x32_bf16 v[86:89], v[172:175], v[214:217], v[86:89]
	v_mfma_f32_16x16x32_bf16 v[82:85], v[180:183], v[214:217], v[82:85]
	s_barrier
	s_add_i32 s42, 0, 0x18000
	v_add_u32_e32 v2, s42, v135
	s_add_i32 s43, 0, 0x1c000
	ds_read_b128 v[152:155], v2
	ds_read_b128 v[156:159], v2 offset:1024
	ds_read_b128 v[160:163], v2 offset:2048
	ds_read_b128 v[164:167], v2 offset:3072
	v_add_u32_e32 v2, s43, v135
	ds_read_b128 v[168:171], v2
	ds_read_b128 v[172:175], v2 offset:1024
	ds_read_b128 v[176:179], v2 offset:2048
	ds_read_b128 v[180:183], v2 offset:3072
	s_add_u32 s40, s40, 0x80000
	s_addc_u32 s41, s41, 0
	s_mov_b32 m0, s53
	v_lshl_add_u64 v[226:227], s[40:41], 0, v[142:143]
	ds_read_b128 v[184:187], v151 offset:32768
	ds_read_b128 v[188:191], v151 offset:33792
	ds_read_b128 v[192:195], v151 offset:34816
	ds_read_b128 v[196:199], v151 offset:35840
	ds_read_b128 v[202:205], v151 offset:36864
	ds_read_b128 v[206:209], v151 offset:37888
	ds_read_b128 v[210:213], v151 offset:38912
	ds_read_b128 v[214:217], v151 offset:39936
	global_load_lds_dwordx4 v[226:227], off
	v_lshl_add_u64 v[226:227], s[40:41], 0, v[138:139]
	s_mov_b32 m0, s54
	s_nop 0
	global_load_lds_dwordx4 v[226:227], off
	s_waitcnt vmcnt(8)
	s_waitcnt lgkmcnt(0)
	s_barrier
	s_waitcnt lgkmcnt(0)
	v_mfma_f32_16x16x32_bf16 v[122:125], v[152:155], v[184:187], v[122:125]
	v_mfma_f32_16x16x32_bf16 v[74:77], v[160:163], v[184:187], v[74:77]
	v_mfma_f32_16x16x32_bf16 v[58:61], v[152:155], v[192:195], v[58:61]
	v_mfma_f32_16x16x32_bf16 v[50:53], v[160:163], v[192:195], v[50:53]
	v_mfma_f32_16x16x32_bf16 v[38:41], v[152:155], v[202:205], v[38:41]
	v_mfma_f32_16x16x32_bf16 v[34:37], v[160:163], v[202:205], v[34:37]
	v_mfma_f32_16x16x32_bf16 v[22:25], v[152:155], v[210:213], v[22:25]
	v_mfma_f32_16x16x32_bf16 v[18:21], v[160:163], v[210:213], v[18:21]
	v_mfma_f32_16x16x32_bf16 v[122:125], v[156:159], v[188:191], v[122:125]
	v_mfma_f32_16x16x32_bf16 v[74:77], v[164:167], v[188:191], v[74:77]
	v_mfma_f32_16x16x32_bf16 v[58:61], v[156:159], v[196:199], v[58:61]
	v_mfma_f32_16x16x32_bf16 v[50:53], v[164:167], v[196:199], v[50:53]
	v_mfma_f32_16x16x32_bf16 v[38:41], v[156:159], v[206:209], v[38:41]
	v_mfma_f32_16x16x32_bf16 v[34:37], v[164:167], v[206:209], v[34:37]
	v_mfma_f32_16x16x32_bf16 v[22:25], v[156:159], v[214:217], v[22:25]
	v_mfma_f32_16x16x32_bf16 v[18:21], v[164:167], v[214:217], v[18:21]
	v_mfma_f32_16x16x32_bf16 v[106:109], v[168:171], v[184:187], v[106:109]
	v_mfma_f32_16x16x32_bf16 v[110:113], v[176:179], v[184:187], v[110:113]
	v_mfma_f32_16x16x32_bf16 v[90:93], v[168:171], v[192:195], v[90:93]
	v_mfma_f32_16x16x32_bf16 v[94:97], v[176:179], v[192:195], v[94:97]
	v_mfma_f32_16x16x32_bf16 v[66:69], v[168:171], v[202:205], v[66:69]
	v_mfma_f32_16x16x32_bf16 v[70:73], v[176:179], v[202:205], v[70:73]
	v_mfma_f32_16x16x32_bf16 v[42:45], v[168:171], v[210:213], v[42:45]
	v_mfma_f32_16x16x32_bf16 v[46:49], v[176:179], v[210:213], v[46:49]
	v_mfma_f32_16x16x32_bf16 v[106:109], v[172:175], v[188:191], v[106:109]
	v_mfma_f32_16x16x32_bf16 v[110:113], v[180:183], v[188:191], v[110:113]
	v_mfma_f32_16x16x32_bf16 v[90:93], v[172:175], v[196:199], v[90:93]
	v_mfma_f32_16x16x32_bf16 v[94:97], v[180:183], v[196:199], v[94:97]
	v_mfma_f32_16x16x32_bf16 v[66:69], v[172:175], v[206:209], v[66:69]
	v_mfma_f32_16x16x32_bf16 v[70:73], v[180:183], v[206:209], v[70:73]
	v_mfma_f32_16x16x32_bf16 v[42:45], v[172:175], v[214:217], v[42:45]
	v_mfma_f32_16x16x32_bf16 v[46:49], v[180:183], v[214:217], v[46:49]
	s_barrier
; #define PG8_STAGE_A(bufoff, base_, nx_, kb_, h_) do { if (GATHER) { if (nx_) PG8_STAGE_G(bufoff, kb_, goN, h_); else PG8_STAGE_G(bufoff, kb_, goC, h_); } \
;         else PG8_STAGE(bufoff, (base_) + (kb_) + (h_) * hstep, voffA); } while (0)
; #define PG8_STAGE(bufoff, gbase, voff) do { _Pragma("unroll") for (int _i = 0; _i < 2; ++_i) \
;         __builtin_amdgcn_global_load_lds((const unsigned*)((const char*)(gbase) + (voff)[_i]), (LAS unsigned*)(lds + (bufoff) + ldsw + _i * 8192), 16, 0, 0); } while (0)
; #define PG8_LDA(dst, b, h) do { _Pragma("unroll") for (int m = 0; m < 4; ++m) _Pragma("unroll") for (int k = 0; k < 2; ++k) dst[m][k] = *(const LAS bf16x8*)(lds + PG8_SA(b, h) + aoff + m * 2048 + k * 1024); } while (0)
; #define PG8_LDB(dst, b, h) do { _Pragma("unroll") for (int n = 0; n < 2; ++n) _Pragma("unroll") for (int k = 0; k < 2; ++k) dst[n][k] = *(const LAS bf16x8*)(lds + PG8_SB(b, h) + boff + n * 2048 + k * 1024); } while (0)
; #define PG8_MMA(ai, bj, At, Bt) do { __builtin_amdgcn_s_setprio(1); _Pragma("unroll") for (int m = 0; m < 4; ++m) _Pragma("unroll") for (int n = 0; n < 2; ++n) _Pragma("unroll") for (int k = 0; k < 2; ++k) \
;         acc[ai][bj][m][n] = __builtin_amdgcn_mfma_f32_16x16x32_bf16(Bt[n][k], At[m][k], acc[ai][bj][m][n], 0, 0, 0); __builtin_amdgcn_s_setprio(0); } while (0)
; #define PG8_WAIT_V(n) asm volatile("s_waitcnt vmcnt(" #n ")" ::: "memory")
; #define PG8_WAIT_L(n) asm volatile("s_waitcnt lgkmcnt(" #n ")" ::: "memory")
; #define PG8_BAR __builtin_amdgcn_s_barrier()
; #define PG8_SCHED __builtin_amdgcn_sched_barrier(0)
; template <class Epi, class Sched, bool GATHER = false>
; __device__ __forceinline__ void gemm_phase(LAS unsigned char* lds, const Gemm g, const Sched& S, const Epi& E, const int tid) {
;     ...
;             PG8_LDB(B0, 0, 0); PG8_LDB(B1, 0, 1); PG8_SCHED; PG8_LDA(At, 0, 0); PG8_STAGE_A(PG8_SA(1, 1), cA, false, kb1, 1);
;             PG8_WAIT_V(8); PG8_WAIT_L(0); PG8_BAR; PG8_MMA(0, 0, At, B0); PG8_MMA(0, 1, At, B1); PG8_BAR; PG8_SCHED;
;     ...
;             PG8_LDA(At, 1, 1); PG8_STAGE(PG8_SB(1, 0), b3, voffB); PG8_STAGE(PG8_SB(1, 1), b3 + hstep, voffB); PG8_STAGE_A(PG8_SA(1, 0), (last ? nA : cA), last, kb3, 0);
;             PG8_WAIT_V(8); PG8_WAIT_L(0); PG8_BAR; PG8_MMA(1, 0, At, B0); PG8_MMA(1, 1, At, B1); PG8_BAR; PG8_SCHED;
;     ...
;         }
	s_add_i32 s40, s42, s50
	v_lshl_add_u64 v[218:219], v[218:219], 0, s[0:1]
	s_mov_b32 m0, s40
	ds_read_b128 v[184:187], v151 offset:49152
	ds_read_b128 v[188:191], v151 offset:50176
	ds_read_b128 v[192:195], v151 offset:51200
	ds_read_b128 v[196:199], v151 offset:52224
	ds_read_b128 v[202:205], v151 offset:53248
	ds_read_b128 v[206:209], v151 offset:54272
	ds_read_b128 v[210:213], v151 offset:55296
	ds_read_b128 v[214:217], v151 offset:56320
	global_load_lds_dwordx4 v[218:219], off
	s_add_i32 m0, s40, 0x2000
	s_add_u32 s38, s38, 0x80080
	v_lshl_add_u64 v[218:219], v[220:221], 0, s[0:1]
	s_addc_u32 s39, s39, 0
	s_add_i32 s40, s43, s50
	global_load_lds_dwordx4 v[218:219], off
	v_lshl_add_u64 v[218:219], s[38:39], 0, v[140:141]
	s_mov_b32 m0, s40
	s_nop 0
	global_load_lds_dwordx4 v[218:219], off
	v_lshl_add_u64 v[218:219], s[38:39], 0, v[136:137]
	s_add_i32 m0, s40, 0x2000
	s_nop 0
	global_load_lds_dwordx4 v[218:219], off
	v_lshl_add_u64 v[218:219], v[222:223], 0, s[0:1]
	s_mov_b32 m0, s33
	s_nop 0
	global_load_lds_dwordx4 v[218:219], off
	v_lshl_add_u64 v[218:219], v[224:225], 0, s[0:1]
	s_mov_b32 m0, s55
	s_nop 0
	global_load_lds_dwordx4 v[218:219], off
	s_waitcnt vmcnt(8)
	s_waitcnt lgkmcnt(0)
	s_barrier
	s_waitcnt lgkmcnt(0)
	v_mfma_f32_16x16x32_bf16 v[30:33], v[152:155], v[184:187], v[30:33]
	v_mfma_f32_16x16x32_bf16 v[26:29], v[160:163], v[184:187], v[26:29]
	v_mfma_f32_16x16x32_bf16 v[14:17], v[152:155], v[192:195], v[14:17]
	v_mfma_f32_16x16x32_bf16 v[10:13], v[160:163], v[192:195], v[10:13]
	v_mfma_f32_16x16x32_bf16 v[6:9], v[152:155], v[202:205], v[6:9]
	v_mfma_f32_16x16x32_bf16 v[78:81], v[160:163], v[202:205], v[78:81]
	v_mfma_f32_16x16x32_bf16 v[62:65], v[152:155], v[210:213], v[62:65]
	v_mfma_f32_16x16x32_bf16 v[54:57], v[160:163], v[210:213], v[54:57]
	v_mfma_f32_16x16x32_bf16 v[30:33], v[156:159], v[188:191], v[30:33]
	v_mfma_f32_16x16x32_bf16 v[26:29], v[164:167], v[188:191], v[26:29]
	v_mfma_f32_16x16x32_bf16 v[14:17], v[156:159], v[196:199], v[14:17]
	v_mfma_f32_16x16x32_bf16 v[10:13], v[164:167], v[196:199], v[10:13]
	v_mfma_f32_16x16x32_bf16 v[6:9], v[156:159], v[206:209], v[6:9]
	v_mfma_f32_16x16x32_bf16 v[78:81], v[164:167], v[206:209], v[78:81]
	v_mfma_f32_16x16x32_bf16 v[62:65], v[156:159], v[214:217], v[62:65]
	v_mfma_f32_16x16x32_bf16 v[54:57], v[164:167], v[214:217], v[54:57]
	v_mfma_f32_16x16x32_bf16 v[130:133], v[168:171], v[184:187], v[130:133]
	v_mfma_f32_16x16x32_bf16 v[126:129], v[176:179], v[184:187], v[126:129]
	v_mfma_f32_16x16x32_bf16 v[118:121], v[168:171], v[192:195], v[118:121]
	v_mfma_f32_16x16x32_bf16 v[114:117], v[176:179], v[192:195], v[114:117]
	v_mfma_f32_16x16x32_bf16 v[102:105], v[168:171], v[202:205], v[102:105]
	v_mfma_f32_16x16x32_bf16 v[98:101], v[176:179], v[202:205], v[98:101]
	v_mfma_f32_16x16x32_bf16 v[86:89], v[168:171], v[210:213], v[86:89]
	v_mfma_f32_16x16x32_bf16 v[82:85], v[176:179], v[210:213], v[82:85]
	v_mfma_f32_16x16x32_bf16 v[130:133], v[172:175], v[188:191], v[130:133]
	v_mfma_f32_16x16x32_bf16 v[126:129], v[180:183], v[188:191], v[126:129]
	v_mfma_f32_16x16x32_bf16 v[118:121], v[172:175], v[196:199], v[118:121]
	v_mfma_f32_16x16x32_bf16 v[114:117], v[180:183], v[196:199], v[114:117]
	v_mfma_f32_16x16x32_bf16 v[102:105], v[172:175], v[206:209], v[102:105]
	v_mfma_f32_16x16x32_bf16 v[98:101], v[180:183], v[206:209], v[98:101]
	v_mfma_f32_16x16x32_bf16 v[86:89], v[172:175], v[214:217], v[86:89]
	v_mfma_f32_16x16x32_bf16 v[82:85], v[180:183], v[214:217], v[82:85]
	s_barrier
	s_add_i32 s61, s61, 2
	s_cmp_gt_u32 s61, 29
	s_mov_b64 s[40:41], s[36:37]
	s_cbranch_scc1 .Lpeel2_exit
.LBB0_1367:
	s_add_u32 s62, s59, s40
	s_addc_u32 s63, s60, s41
	s_add_u32 s36, s40, 0x100
	s_addc_u32 s37, s41, 0
	s_cmp_eq_u32 s61, 28
	s_cselect_b64 s[42:43], -1, 0
	s_and_b64 s[38:39], s[42:43], exec
	s_cselect_b32 s39, s21, s63
	s_cselect_b32 s38, s23, s62
	s_cselect_b32 s62, 0, s36
	s_add_i32 s63, 0, 0x10000
	v_add_u32_e32 v2, s63, v135
	s_add_i32 s64, 0, 0x14000
	ds_read_b128 v[152:155], v2
	ds_read_b128 v[156:159], v2 offset:1024
	ds_read_b128 v[160:163], v2 offset:2048
	ds_read_b128 v[164:167], v2 offset:3072
	v_add_u32_e32 v2, s64, v135
	ds_read_b128 v[168:171], v2
	ds_read_b128 v[172:175], v2 offset:1024
	ds_read_b128 v[176:179], v2 offset:2048
	ds_read_b128 v[180:183], v2 offset:3072
	v_lshl_add_u64 v[218:219], v[4:5], 0, s[40:41]
	s_add_i32 m0, s31, 0xc000
	ds_read_b128 v[184:187], v151
	ds_read_b128 v[188:191], v151 offset:1024
	ds_read_b128 v[192:195], v151 offset:2048
	ds_read_b128 v[196:199], v151 offset:3072
	ds_read_b128 v[202:205], v151 offset:4096
	ds_read_b128 v[206:209], v151 offset:5120
	ds_read_b128 v[210:213], v151 offset:6144
	ds_read_b128 v[214:217], v151 offset:7168
	global_load_lds_dwordx4 v[218:219], off
	v_lshl_add_u64 v[218:219], v[148:149], 0, s[40:41]
	s_add_i32 m0, s31, 0xe000
	s_nop 0
	global_load_lds_dwordx4 v[218:219], off
	s_waitcnt vmcnt(8)
	s_waitcnt lgkmcnt(0)
	s_barrier
; #define PG8_STAGE_A(bufoff, base_, nx_, kb_, h_) do { if (GATHER) { if (nx_) PG8_STAGE_G(bufoff, kb_, goN, h_); else PG8_STAGE_G(bufoff, kb_, goC, h_); } \
;         else PG8_STAGE(bufoff, (base_) + (kb_) + (h_) * hstep, voffA); } while (0)
; #define PG8_STAGE(bufoff, gbase, voff) do { _Pragma("unroll") for (int _i = 0; _i < 2; ++_i) \
;         __builtin_amdgcn_global_load_lds((const unsigned*)((const char*)(gbase) + (voff)[_i]), (LAS unsigned*)(lds + (bufoff) + ldsw + _i * 8192), 16, 0, 0); } while (0)
; #define PG8_LDA(dst, b, h) do { _Pragma("unroll") for (int m = 0; m < 4; ++m) _Pragma("unroll") for (int k = 0; k < 2; ++k) dst[m][k] = *(const LAS bf16x8*)(lds + PG8_SA(b, h) + aoff + m * 2048 + k * 1024); } while (0)
; #define PG8_MMA(ai, bj, At, Bt) do { __builtin_amdgcn_s_setprio(1); _Pragma("unroll") for (int m = 0; m < 4; ++m) _Pragma("unroll") for (int n = 0; n < 2; ++n) _Pragma("unroll") for (int k = 0; k < 2; ++k) \
;         acc[ai][bj][m][n] = __builtin_amdgcn_mfma_f32_16x16x32_bf16(Bt[n][k], At[m][k], acc[ai][bj][m][n], 0, 0, 0); __builtin_amdgcn_s_setprio(0); } while (0)
; #define PG8_WAIT_V(n) asm volatile("s_waitcnt vmcnt(" #n ")" ::: "memory")
; #define PG8_WAIT_L(n) asm volatile("s_waitcnt lgkmcnt(" #n ")" ::: "memory")
; #define PG8_BAR __builtin_amdgcn_s_barrier()
; #define PG8_SCHED __builtin_amdgcn_sched_barrier(0)
; template <class Epi, class Sched, bool GATHER = false>
; __device__ __forceinline__ void gemm_phase(LAS unsigned char* lds, const Gemm g, const Sched& S, const Epi& E, const int tid) {
;     ...
;             PG8_WAIT_V(8); PG8_WAIT_L(0); PG8_BAR; PG8_MMA(0, 0, At, B0); PG8_MMA(0, 1, At, B1); PG8_BAR; PG8_SCHED;
;             PG8_LDA(At, 0, 1); PG8_STAGE(PG8_SB(0, 0), b2, voffB); PG8_STAGE(PG8_SB(0, 1), b2 + hstep, voffB); PG8_STAGE_A(PG8_SA(0, 0), (last ? nA : cA), last, kb2, 0);
;             PG8_WAIT_V(8); PG8_WAIT_L(0); PG8_BAR; PG8_MMA(1, 0, At, B0); PG8_MMA(1, 1, At, B1); PG8_BAR; PG8_SCHED;
	s_waitcnt lgkmcnt(0)
	v_mfma_f32_16x16x32_bf16 v[122:125], v[152:155], v[184:187], v[122:125]
	v_mfma_f32_16x16x32_bf16 v[74:77], v[160:163], v[184:187], v[74:77]
	v_mfma_f32_16x16x32_bf16 v[58:61], v[152:155], v[192:195], v[58:61]
	v_mfma_f32_16x16x32_bf16 v[50:53], v[160:163], v[192:195], v[50:53]
	v_mfma_f32_16x16x32_bf16 v[38:41], v[152:155], v[202:205], v[38:41]
	v_mfma_f32_16x16x32_bf16 v[34:37], v[160:163], v[202:205], v[34:37]
	v_mfma_f32_16x16x32_bf16 v[22:25], v[152:155], v[210:213], v[22:25]
	v_mfma_f32_16x16x32_bf16 v[18:21], v[160:163], v[210:213], v[18:21]
	v_mfma_f32_16x16x32_bf16 v[122:125], v[156:159], v[188:191], v[122:125]
	v_mfma_f32_16x16x32_bf16 v[74:77], v[164:167], v[188:191], v[74:77]
	v_mfma_f32_16x16x32_bf16 v[58:61], v[156:159], v[196:199], v[58:61]
	v_mfma_f32_16x16x32_bf16 v[50:53], v[164:167], v[196:199], v[50:53]
	v_mfma_f32_16x16x32_bf16 v[38:41], v[156:159], v[206:209], v[38:41]
	v_mfma_f32_16x16x32_bf16 v[34:37], v[164:167], v[206:209], v[34:37]
	v_mfma_f32_16x16x32_bf16 v[22:25], v[156:159], v[214:217], v[22:25]
	v_mfma_f32_16x16x32_bf16 v[18:21], v[164:167], v[214:217], v[18:21]
	v_mfma_f32_16x16x32_bf16 v[106:109], v[168:171], v[184:187], v[106:109]
	v_mfma_f32_16x16x32_bf16 v[110:113], v[176:179], v[184:187], v[110:113]
	v_mfma_f32_16x16x32_bf16 v[90:93], v[168:171], v[192:195], v[90:93]
	v_mfma_f32_16x16x32_bf16 v[94:97], v[176:179], v[192:195], v[94:97]
	v_mfma_f32_16x16x32_bf16 v[66:69], v[168:171], v[202:205], v[66:69]
	v_mfma_f32_16x16x32_bf16 v[70:73], v[176:179], v[202:205], v[70:73]
	v_mfma_f32_16x16x32_bf16 v[42:45], v[168:171], v[210:213], v[42:45]
	v_mfma_f32_16x16x32_bf16 v[46:49], v[176:179], v[210:213], v[46:49]
	v_mfma_f32_16x16x32_bf16 v[106:109], v[172:175], v[188:191], v[106:109]
	v_mfma_f32_16x16x32_bf16 v[110:113], v[180:183], v[188:191], v[110:113]
	v_mfma_f32_16x16x32_bf16 v[90:93], v[172:175], v[196:199], v[90:93]
	v_mfma_f32_16x16x32_bf16 v[94:97], v[180:183], v[196:199], v[94:97]
	v_mfma_f32_16x16x32_bf16 v[66:69], v[172:175], v[206:209], v[66:69]
	v_mfma_f32_16x16x32_bf16 v[70:73], v[180:183], v[206:209], v[70:73]
	v_mfma_f32_16x16x32_bf16 v[42:45], v[172:175], v[214:217], v[42:45]
	v_mfma_f32_16x16x32_bf16 v[46:49], v[180:183], v[214:217], v[46:49]
	s_barrier
	s_add_i32 s40, s63, s50
	v_lshl_add_u64 v[218:219], s[38:39], 0, v[140:141]
	s_mov_b32 m0, s40
	ds_read_b128 v[184:187], v151 offset:16384
	ds_read_b128 v[188:191], v151 offset:17408
	ds_read_b128 v[192:195], v151 offset:18432
	ds_read_b128 v[196:199], v151 offset:19456
	ds_read_b128 v[202:205], v151 offset:20480
	ds_read_b128 v[206:209], v151 offset:21504
	ds_read_b128 v[210:213], v151 offset:22528
	ds_read_b128 v[214:217], v151 offset:23552
	global_load_lds_dwordx4 v[218:219], off
	s_add_i32 m0, s40, 0x2000
	s_add_u32 s40, s38, 0x80000
	v_lshl_add_u64 v[220:221], s[38:39], 0, v[136:137]
	s_addc_u32 s41, s39, 0
	s_add_i32 s63, s64, s50
	global_load_lds_dwordx4 v[220:221], off
	v_lshl_add_u64 v[222:223], s[40:41], 0, v[140:141]
	s_mov_b32 m0, s63
	s_nop 0
	global_load_lds_dwordx4 v[222:223], off
	v_lshl_add_u64 v[222:223], s[40:41], 0, v[136:137]
	s_add_i32 m0, s63, 0x2000
	s_and_b64 s[40:41], s[8:9], s[42:43]
	s_and_b64 s[40:41], s[40:41], exec
	s_cselect_b32 s40, s24, s34
	s_cselect_b32 s41, s25, s35
	s_add_u32 s40, s40, s62
	s_addc_u32 s41, s41, 0
	global_load_lds_dwordx4 v[222:223], off
	v_lshl_add_u64 v[222:223], s[40:41], 0, v[142:143]
	s_mov_b32 m0, s31
	v_lshl_add_u64 v[224:225], s[40:41], 0, v[138:139]
	global_load_lds_dwordx4 v[222:223], off
	s_mov_b32 m0, s52
	s_nop 0
	global_load_lds_dwordx4 v[224:225], off
	s_waitcnt vmcnt(8)
	s_waitcnt lgkmcnt(0)
	s_barrier
	s_waitcnt lgkmcnt(0)
	v_mfma_f32_16x16x32_bf16 v[30:33], v[152:155], v[184:187], v[30:33]
	v_mfma_f32_16x16x32_bf16 v[26:29], v[160:163], v[184:187], v[26:29]
	v_mfma_f32_16x16x32_bf16 v[14:17], v[152:155], v[192:195], v[14:17]
	v_mfma_f32_16x16x32_bf16 v[10:13], v[160:163], v[192:195], v[10:13]
	v_mfma_f32_16x16x32_bf16 v[6:9], v[152:155], v[202:205], v[6:9]
	v_mfma_f32_16x16x32_bf16 v[78:81], v[160:163], v[202:205], v[78:81]
	v_mfma_f32_16x16x32_bf16 v[62:65], v[152:155], v[210:213], v[62:65]
	v_mfma_f32_16x16x32_bf16 v[54:57], v[160:163], v[210:213], v[54:57]
	v_mfma_f32_16x16x32_bf16 v[30:33], v[156:159], v[188:191], v[30:33]
	v_mfma_f32_16x16x32_bf16 v[26:29], v[164:167], v[188:191], v[26:29]
	v_mfma_f32_16x16x32_bf16 v[14:17], v[156:159], v[196:199], v[14:17]
	v_mfma_f32_16x16x32_bf16 v[10:13], v[164:167], v[196:199], v[10:13]
	v_mfma_f32_16x16x32_bf16 v[6:9], v[156:159], v[206:209], v[6:9]
	v_mfma_f32_16x16x32_bf16 v[78:81], v[164:167], v[206:209], v[78:81]
	v_mfma_f32_16x16x32_bf16 v[62:65], v[156:159], v[214:217], v[62:65]
	v_mfma_f32_16x16x32_bf16 v[54:57], v[164:167], v[214:217], v[54:57]
	v_mfma_f32_16x16x32_bf16 v[130:133], v[168:171], v[184:187], v[130:133]
	v_mfma_f32_16x16x32_bf16 v[126:129], v[176:179], v[184:187], v[126:129]
	v_mfma_f32_16x16x32_bf16 v[118:121], v[168:171], v[192:195], v[118:121]
	v_mfma_f32_16x16x32_bf16 v[114:117], v[176:179], v[192:195], v[114:117]
	v_mfma_f32_16x16x32_bf16 v[102:105], v[168:171], v[202:205], v[102:105]
	v_mfma_f32_16x16x32_bf16 v[98:101], v[176:179], v[202:205], v[98:101]
	v_mfma_f32_16x16x32_bf16 v[86:89], v[168:171], v[210:213], v[86:89]
	v_mfma_f32_16x16x32_bf16 v[82:85], v[176:179], v[210:213], v[82:85]
	v_mfma_f32_16x16x32_bf16 v[130:133], v[172:175], v[188:191], v[130:133]
	v_mfma_f32_16x16x32_bf16 v[126:129], v[180:183], v[188:191], v[126:129]
	v_mfma_f32_16x16x32_bf16 v[118:121], v[172:175], v[196:199], v[118:121]
	v_mfma_f32_16x16x32_bf16 v[114:117], v[180:183], v[196:199], v[114:117]
	v_mfma_f32_16x16x32_bf16 v[102:105], v[172:175], v[206:209], v[102:105]
	v_mfma_f32_16x16x32_bf16 v[98:101], v[180:183], v[206:209], v[98:101]
	v_mfma_f32_16x16x32_bf16 v[86:89], v[172:175], v[214:217], v[86:89]
	v_mfma_f32_16x16x32_bf16 v[82:85], v[180:183], v[214:217], v[82:85]
	s_barrier
; #define PG8_STAGE_A(bufoff, base_, nx_, kb_, h_) do { if (GATHER) { if (nx_) PG8_STAGE_G(bufoff, kb_, goN, h_); else PG8_STAGE_G(bufoff, kb_, goC, h_); } \
;         else PG8_STAGE(bufoff, (base_) + (kb_) + (h_) * hstep, voffA); } while (0)
; #define PG8_STAGE(bufoff, gbase, voff) do { _Pragma("unroll") for (int _i = 0; _i < 2; ++_i) \
;         __builtin_amdgcn_global_load_lds((const unsigned*)((const char*)(gbase) + (voff)[_i]), (LAS unsigned*)(lds + (bufoff) + ldsw + _i * 8192), 16, 0, 0); } while (0)
; #define PG8_LDA(dst, b, h) do { _Pragma("unroll") for (int m = 0; m < 4; ++m) _Pragma("unroll") for (int k = 0; k < 2; ++k) dst[m][k] = *(const LAS bf16x8*)(lds + PG8_SA(b, h) + aoff + m * 2048 + k * 1024); } while (0)
; #define PG8_LDB(dst, b, h) do { _Pragma("unroll") for (int n = 0; n < 2; ++n) _Pragma("unroll") for (int k = 0; k < 2; ++k) dst[n][k] = *(const LAS bf16x8*)(lds + PG8_SB(b, h) + boff + n * 2048 + k * 1024); } while (0)
; #define PG8_MMA(ai, bj, At, Bt) do { __builtin_amdgcn_s_setprio(1); _Pragma("unroll") for (int m = 0; m < 4; ++m) _Pragma("unroll") for (int n = 0; n < 2; ++n) _Pragma("unroll") for (int k = 0; k < 2; ++k) \
;         acc[ai][bj][m][n] = __builtin_amdgcn_mfma_f32_16x16x32_bf16(Bt[n][k], At[m][k], acc[ai][bj][m][n], 0, 0, 0); __builtin_amdgcn_s_setprio(0); } while (0)
; #define PG8_WAIT_V(n) asm volatile("s_waitcnt vmcnt(" #n ")" ::: "memory")
; #define PG8_WAIT_L(n) asm volatile("s_waitcnt lgkmcnt(" #n ")" ::: "memory")
; #define PG8_BAR __builtin_amdgcn_s_barrier()
; #define PG8_SCHED __builtin_amdgcn_sched_barrier(0)
; template <class Epi, class Sched, bool GATHER = false>
; __device__ __forceinline__ void gemm_phase(LAS unsigned char* lds, const Gemm g, const Sched& S, const Epi& E, const int tid) {
;     ...
;             PG8_LDB(B0, 1, 0); PG8_LDB(B1, 1, 1); PG8_SCHED; PG8_LDA(At, 1, 0); PG8_STAGE_A(PG8_SA(0, 1), (last ? nA : cA), last, kb2, 1);
;             PG8_WAIT_V(8); PG8_WAIT_L(0); PG8_BAR; PG8_MMA(0, 0, At, B0); PG8_MMA(0, 1, At, B1); PG8_BAR; PG8_SCHED;
;             PG8_LDA(At, 1, 1); PG8_STAGE(PG8_SB(1, 0), b3, voffB); PG8_STAGE(PG8_SB(1, 1), b3 + hstep, voffB); PG8_STAGE_A(PG8_SA(1, 0), (last ? nA : cA), last, kb3, 0);
;             PG8_WAIT_V(8); PG8_WAIT_L(0); PG8_BAR; PG8_MMA(1, 0, At, B0); PG8_MMA(1, 1, At, B1); PG8_BAR; PG8_SCHED;
	s_add_i32 s42, 0, 0x18000
	v_add_u32_e32 v2, s42, v135
	s_add_i32 s43, 0, 0x1c000
	ds_read_b128 v[152:155], v2
	ds_read_b128 v[156:159], v2 offset:1024
	ds_read_b128 v[160:163], v2 offset:2048
	ds_read_b128 v[164:167], v2 offset:3072
	v_add_u32_e32 v2, s43, v135
	ds_read_b128 v[168:171], v2
	ds_read_b128 v[172:175], v2 offset:1024
	ds_read_b128 v[176:179], v2 offset:2048
	ds_read_b128 v[180:183], v2 offset:3072
	s_add_u32 s40, s40, 0x80000
	s_addc_u32 s41, s41, 0
	s_mov_b32 m0, s53
	v_lshl_add_u64 v[226:227], s[40:41], 0, v[142:143]
	ds_read_b128 v[184:187], v151 offset:32768
	ds_read_b128 v[188:191], v151 offset:33792
	ds_read_b128 v[192:195], v151 offset:34816
	ds_read_b128 v[196:199], v151 offset:35840
	ds_read_b128 v[202:205], v151 offset:36864
	ds_read_b128 v[206:209], v151 offset:37888
	ds_read_b128 v[210:213], v151 offset:38912
	ds_read_b128 v[214:217], v151 offset:39936
	global_load_lds_dwordx4 v[226:227], off
	v_lshl_add_u64 v[226:227], s[40:41], 0, v[138:139]
	s_mov_b32 m0, s54
	s_nop 0
	global_load_lds_dwordx4 v[226:227], off
	s_waitcnt vmcnt(8)
	s_waitcnt lgkmcnt(0)
	s_barrier
	s_waitcnt lgkmcnt(0)
	v_mfma_f32_16x16x32_bf16 v[122:125], v[152:155], v[184:187], v[122:125]
	v_mfma_f32_16x16x32_bf16 v[74:77], v[160:163], v[184:187], v[74:77]
	v_mfma_f32_16x16x32_bf16 v[58:61], v[152:155], v[192:195], v[58:61]
	v_mfma_f32_16x16x32_bf16 v[50:53], v[160:163], v[192:195], v[50:53]
	v_mfma_f32_16x16x32_bf16 v[38:41], v[152:155], v[202:205], v[38:41]
	v_mfma_f32_16x16x32_bf16 v[34:37], v[160:163], v[202:205], v[34:37]
	v_mfma_f32_16x16x32_bf16 v[22:25], v[152:155], v[210:213], v[22:25]
	v_mfma_f32_16x16x32_bf16 v[18:21], v[160:163], v[210:213], v[18:21]
	v_mfma_f32_16x16x32_bf16 v[122:125], v[156:159], v[188:191], v[122:125]
	v_mfma_f32_16x16x32_bf16 v[74:77], v[164:167], v[188:191], v[74:77]
	v_mfma_f32_16x16x32_bf16 v[58:61], v[156:159], v[196:199], v[58:61]
	v_mfma_f32_16x16x32_bf16 v[50:53], v[164:167], v[196:199], v[50:53]
	v_mfma_f32_16x16x32_bf16 v[38:41], v[156:159], v[206:209], v[38:41]
	v_mfma_f32_16x16x32_bf16 v[34:37], v[164:167], v[206:209], v[34:37]
	v_mfma_f32_16x16x32_bf16 v[22:25], v[156:159], v[214:217], v[22:25]
	v_mfma_f32_16x16x32_bf16 v[18:21], v[164:167], v[214:217], v[18:21]
	v_mfma_f32_16x16x32_bf16 v[106:109], v[168:171], v[184:187], v[106:109]
	v_mfma_f32_16x16x32_bf16 v[110:113], v[176:179], v[184:187], v[110:113]
	v_mfma_f32_16x16x32_bf16 v[90:93], v[168:171], v[192:195], v[90:93]
	v_mfma_f32_16x16x32_bf16 v[94:97], v[176:179], v[192:195], v[94:97]
	v_mfma_f32_16x16x32_bf16 v[66:69], v[168:171], v[202:205], v[66:69]
	v_mfma_f32_16x16x32_bf16 v[70:73], v[176:179], v[202:205], v[70:73]
	v_mfma_f32_16x16x32_bf16 v[42:45], v[168:171], v[210:213], v[42:45]
	v_mfma_f32_16x16x32_bf16 v[46:49], v[176:179], v[210:213], v[46:49]
	v_mfma_f32_16x16x32_bf16 v[106:109], v[172:175], v[188:191], v[106:109]
	v_mfma_f32_16x16x32_bf16 v[110:113], v[180:183], v[188:191], v[110:113]
	v_mfma_f32_16x16x32_bf16 v[90:93], v[172:175], v[196:199], v[90:93]
	v_mfma_f32_16x16x32_bf16 v[94:97], v[180:183], v[196:199], v[94:97]
	v_mfma_f32_16x16x32_bf16 v[66:69], v[172:175], v[206:209], v[66:69]
	v_mfma_f32_16x16x32_bf16 v[70:73], v[180:183], v[206:209], v[70:73]
	v_mfma_f32_16x16x32_bf16 v[42:45], v[172:175], v[214:217], v[42:45]
	v_mfma_f32_16x16x32_bf16 v[46:49], v[180:183], v[214:217], v[46:49]
	s_barrier
	s_add_i32 s40, s42, s50
	v_lshl_add_u64 v[218:219], v[218:219], 0, s[0:1]
	s_mov_b32 m0, s40
	ds_read_b128 v[184:187], v151 offset:49152
	ds_read_b128 v[188:191], v151 offset:50176
	ds_read_b128 v[192:195], v151 offset:51200
	ds_read_b128 v[196:199], v151 offset:52224
	ds_read_b128 v[202:205], v151 offset:53248
	ds_read_b128 v[206:209], v151 offset:54272
	ds_read_b128 v[210:213], v151 offset:55296
	ds_read_b128 v[214:217], v151 offset:56320
	global_load_lds_dwordx4 v[218:219], off
	s_add_i32 m0, s40, 0x2000
	s_add_u32 s38, s38, 0x80080
	v_lshl_add_u64 v[218:219], v[220:221], 0, s[0:1]
	s_addc_u32 s39, s39, 0
	s_add_i32 s40, s43, s50
	global_load_lds_dwordx4 v[218:219], off
	v_lshl_add_u64 v[218:219], s[38:39], 0, v[140:141]
	s_mov_b32 m0, s40
	s_nop 0
	global_load_lds_dwordx4 v[218:219], off
	v_lshl_add_u64 v[218:219], s[38:39], 0, v[136:137]
	s_add_i32 m0, s40, 0x2000
	s_nop 0
	global_load_lds_dwordx4 v[218:219], off
	v_lshl_add_u64 v[218:219], v[222:223], 0, s[0:1]
	s_mov_b32 m0, s33
	s_nop 0
	global_load_lds_dwordx4 v[218:219], off
	v_lshl_add_u64 v[218:219], v[224:225], 0, s[0:1]
	s_mov_b32 m0, s55
	s_nop 0
	global_load_lds_dwordx4 v[218:219], off
	s_waitcnt vmcnt(8)
	s_waitcnt lgkmcnt(0)
	s_barrier
	s_waitcnt lgkmcnt(0)
	v_mfma_f32_16x16x32_bf16 v[30:33], v[152:155], v[184:187], v[30:33]
	v_mfma_f32_16x16x32_bf16 v[26:29], v[160:163], v[184:187], v[26:29]
	v_mfma_f32_16x16x32_bf16 v[14:17], v[152:155], v[192:195], v[14:17]
	v_mfma_f32_16x16x32_bf16 v[10:13], v[160:163], v[192:195], v[10:13]
	v_mfma_f32_16x16x32_bf16 v[6:9], v[152:155], v[202:205], v[6:9]
	v_mfma_f32_16x16x32_bf16 v[78:81], v[160:163], v[202:205], v[78:81]
	v_mfma_f32_16x16x32_bf16 v[62:65], v[152:155], v[210:213], v[62:65]
	v_mfma_f32_16x16x32_bf16 v[54:57], v[160:163], v[210:213], v[54:57]
	v_mfma_f32_16x16x32_bf16 v[30:33], v[156:159], v[188:191], v[30:33]
	v_mfma_f32_16x16x32_bf16 v[26:29], v[164:167], v[188:191], v[26:29]
	v_mfma_f32_16x16x32_bf16 v[14:17], v[156:159], v[196:199], v[14:17]
	v_mfma_f32_16x16x32_bf16 v[10:13], v[164:167], v[196:199], v[10:13]
	v_mfma_f32_16x16x32_bf16 v[6:9], v[156:159], v[206:209], v[6:9]
	v_mfma_f32_16x16x32_bf16 v[78:81], v[164:167], v[206:209], v[78:81]
	v_mfma_f32_16x16x32_bf16 v[62:65], v[156:159], v[214:217], v[62:65]
	v_mfma_f32_16x16x32_bf16 v[54:57], v[164:167], v[214:217], v[54:57]
	v_mfma_f32_16x16x32_bf16 v[130:133], v[168:171], v[184:187], v[130:133]
	v_mfma_f32_16x16x32_bf16 v[126:129], v[176:179], v[184:187], v[126:129]
	v_mfma_f32_16x16x32_bf16 v[118:121], v[168:171], v[192:195], v[118:121]
	v_mfma_f32_16x16x32_bf16 v[114:117], v[176:179], v[192:195], v[114:117]
	v_mfma_f32_16x16x32_bf16 v[102:105], v[168:171], v[202:205], v[102:105]
	v_mfma_f32_16x16x32_bf16 v[98:101], v[176:179], v[202:205], v[98:101]
	v_mfma_f32_16x16x32_bf16 v[86:89], v[168:171], v[210:213], v[86:89]
	v_mfma_f32_16x16x32_bf16 v[82:85], v[176:179], v[210:213], v[82:85]
	v_mfma_f32_16x16x32_bf16 v[130:133], v[172:175], v[188:191], v[130:133]
	v_mfma_f32_16x16x32_bf16 v[126:129], v[180:183], v[188:191], v[126:129]
	v_mfma_f32_16x16x32_bf16 v[118:121], v[172:175], v[196:199], v[118:121]
	v_mfma_f32_16x16x32_bf16 v[114:117], v[180:183], v[196:199], v[114:117]
	v_mfma_f32_16x16x32_bf16 v[102:105], v[172:175], v[206:209], v[102:105]
	v_mfma_f32_16x16x32_bf16 v[98:101], v[180:183], v[206:209], v[98:101]
	v_mfma_f32_16x16x32_bf16 v[86:89], v[172:175], v[214:217], v[86:89]
	v_mfma_f32_16x16x32_bf16 v[82:85], v[180:183], v[214:217], v[82:85]
	s_barrier
	s_add_i32 s61, s61, 2
	s_cmp_gt_u32 s61, 29
	s_mov_b64 s[40:41], s[36:37]
	s_cbranch_scc0 .LBB0_1367
; __device__ __forceinline__ unsigned cvt_pk_bf16(float lo, float hi) { const f32x2 v = {lo, hi}; const bf16x2_t b = __builtin_convertvector(v, bf16x2_t); return __builtin_bit_cast(unsigned, b); }
; __device__ __forceinline__ float fast_silu(float x) { return x * __builtin_amdgcn_rcpf(1.f + __builtin_amdgcn_exp2f(-1.4426950408889634f * x)); }
; #define PG8_BAR __builtin_amdgcn_s_barrier()
;     __device__ __forceinline__ void operator()(const f32x4 (&acc)[2][2][4][2], const Unit& u, int wr, int wc, int fr, int fq) const {
;         const int row0 = u.pm * BM + wr * 64 + fr, col0 = u.pn * HALF + wc * 32 + 8 * fq;
; #pragma unroll
;         for (int ai = 0; ai < 2; ++ai)
; #pragma unroll
;             for (int m = 0; m < 4; ++m) { bf16_t* rowp = O + (size_t)(row0 + ai * HALF + m * 16) * ldc + col0;
;                 float o[8];
; #pragma unroll
;                 for (int n = 0; n < 2; ++n)
; #pragma unroll
;                     for (int i = 0; i < 4; ++i) o[n * 4 + i] = fast_silu(acc[ai][0][m][n][i]) * acc[ai][1][m][n][i];
;                 u32x4 w; w.x = cvt_pk_bf16(o[0], o[1]); w.y = cvt_pk_bf16(o[2], o[3]); w.z = cvt_pk_bf16(o[4], o[5]); w.w = cvt_pk_bf16(o[6], o[7]);
;                 *(u32x4*)rowp = w; }
;     }
; template <class Epi, class Sched, bool GATHER = false>
; __device__ __forceinline__ void gemm_phase(LAS unsigned char* lds, const Gemm g, const Sched& S, const Epi& E, const int tid) {
;     ...
;         if (wr == 0) PG8_BAR;
.Lpeel2_exit:
	s_and_b64 vcc, exec, s[16:17]
	s_cbranch_vccz .LBB0_1370
	s_barrier
.LBB0_1370:
	v_mul_f32_e32 v4, 0xbfb8aa3b, v122
	v_exp_f32_e32 v4, v4
	v_mul_f32_e32 v5, 0xbfb8aa3b, v123
	v_exp_f32_e32 v5, v5
	v_lshl_or_b32 v148, s58, 7, v150
	v_add_f32_e32 v4, 1.0, v4
	v_rcp_f32_e32 v152, v4
	v_add_f32_e32 v4, 1.0, v5
	v_rcp_f32_e32 v153, v4
	v_lshl_add_u32 v2, s30, 8, v1
	v_ashrrev_i32_e32 v149, 31, v148
	v_mov_b64_e32 v[4:5], s[10:11]
	v_pk_mul_f32 v[122:123], v[122:123], v[152:153]
	v_mul_f32_e32 v152, 0xbfb8aa3b, v124
	v_mul_f32_e32 v153, 0xbfb8aa3b, v125
	v_exp_f32_e32 v152, v152
	v_exp_f32_e32 v153, v153
	v_pk_mul_f32 v[106:107], v[122:123], v[106:107]
	s_movk_i32 s21, 0x2c00
	v_add_f32_e32 v122, 1.0, v152
	v_add_f32_e32 v123, 1.0, v153
	v_mul_f32_e32 v152, 0xbfb8aa3b, v74
	v_mul_f32_e32 v153, 0xbfb8aa3b, v75
	v_rcp_f32_e32 v122, v122
	v_rcp_f32_e32 v123, v123
	v_exp_f32_e32 v152, v152
	v_exp_f32_e32 v153, v153
	v_cvt_pk_bf16_f32 v106, v106, v107
	v_pk_mul_f32 v[122:123], v[124:125], v[122:123]
	v_add_f32_e32 v124, 1.0, v152
	v_add_f32_e32 v125, 1.0, v153
	v_mul_f32_e32 v152, 0xbfb8aa3b, v76
	v_mul_f32_e32 v153, 0xbfb8aa3b, v77
	v_exp_f32_e32 v152, v152
	v_exp_f32_e32 v153, v153
	v_rcp_f32_e32 v124, v124
	v_rcp_f32_e32 v125, v125
	v_add_f32_e32 v152, 1.0, v152
	v_add_f32_e32 v153, 1.0, v153
	v_rcp_f32_e32 v152, v152
	v_rcp_f32_e32 v153, v153
	v_pk_mul_f32 v[74:75], v[74:75], v[124:125]
	v_pk_mul_f32 v[108:109], v[122:123], v[108:109]
	v_pk_mul_f32 v[110:111], v[74:75], v[110:111]
	v_pk_mul_f32 v[74:75], v[76:77], v[152:153]
	v_cvt_pk_bf16_f32 v107, v108, v109
	v_pk_mul_f32 v[76:77], v[74:75], v[112:113]
	v_mad_i64_i32 v[154:155], s[34:35], v2, s21, v[4:5]
	v_cvt_pk_bf16_f32 v109, v76, v77
	v_mul_f32_e32 v76, 0xbfb8aa3b, v58
	v_mul_f32_e32 v77, 0xbfb8aa3b, v59
	v_exp_f32_e32 v76, v76
	v_exp_f32_e32 v77, v77
	v_lshlrev_b64 v[74:75], 1, v[148:149]
	v_lshl_add_u64 v[112:113], v[154:155], 0, v[74:75]
	v_add_f32_e32 v76, 1.0, v76
	v_add_f32_e32 v77, 1.0, v77
	v_rcp_f32_e32 v76, v76
	v_rcp_f32_e32 v77, v77
	v_cvt_pk_bf16_f32 v108, v110, v111
	global_store_dwordx4 v[112:113], v[106:109], off
	v_readlane_b32 s60, v254, 5
	v_pk_mul_f32 v[58:59], v[58:59], v[76:77]
	v_mul_f32_e32 v76, 0xbfb8aa3b, v60
	v_mul_f32_e32 v77, 0xbfb8aa3b, v61
	v_exp_f32_e32 v76, v76
	v_exp_f32_e32 v77, v77
	v_pk_mul_f32 v[58:59], v[58:59], v[90:91]
	v_mul_f32_e32 v90, 0xbfb8aa3b, v50
	v_add_f32_e32 v76, 1.0, v76
	v_add_f32_e32 v77, 1.0, v77
	v_mul_f32_e32 v91, 0xbfb8aa3b, v51
	v_rcp_f32_e32 v76, v76
	v_rcp_f32_e32 v77, v77
	v_exp_f32_e32 v90, v90
	v_exp_f32_e32 v91, v91
	v_or_b32_e32 v106, 16, v2
	v_pk_mul_f32 v[60:61], v[60:61], v[76:77]
	v_add_f32_e32 v76, 1.0, v90
	v_add_f32_e32 v77, 1.0, v91
	v_mul_f32_e32 v90, 0xbfb8aa3b, v52
	v_mul_f32_e32 v91, 0xbfb8aa3b, v53
	v_exp_f32_e32 v90, v90
	v_exp_f32_e32 v91, v91
	v_rcp_f32_e32 v76, v76
	v_rcp_f32_e32 v77, v77
	v_add_f32_e32 v90, 1.0, v90
	v_add_f32_e32 v91, 1.0, v91
	v_rcp_f32_e32 v90, v90
	v_rcp_f32_e32 v91, v91
	v_pk_mul_f32 v[50:51], v[50:51], v[76:77]
	v_mad_i64_i32 v[106:107], s[34:35], v106, s21, v[4:5]
	v_pk_mul_f32 v[76:77], v[50:51], v[94:95]
	v_pk_mul_f32 v[50:51], v[52:53], v[90:91]
	v_pk_mul_f32 v[60:61], v[60:61], v[92:93]
	v_pk_mul_f32 v[90:91], v[50:51], v[96:97]
	v_cvt_pk_bf16_f32 v50, v58, v59
	v_mul_f32_e32 v58, 0xbfb8aa3b, v38
	v_mul_f32_e32 v59, 0xbfb8aa3b, v39
	v_exp_f32_e32 v58, v58
	v_exp_f32_e32 v59, v59
	v_lshl_add_u64 v[92:93], v[106:107], 0, v[74:75]
	v_cvt_pk_bf16_f32 v51, v60, v61
	v_cvt_pk_bf16_f32 v52, v76, v77
	v_cvt_pk_bf16_f32 v53, v90, v91
	global_store_dwordx4 v[92:93], v[50:53], off
	s_andn2_b64 vcc, exec, s[8:9]
	s_mov_b64 s[8:9], -1
	v_add_f32_e32 v50, 1.0, v58
	v_add_f32_e32 v51, 1.0, v59
	v_rcp_f32_e32 v50, v50
	v_rcp_f32_e32 v51, v51
	v_mul_f32_e32 v58, 0xbfb8aa3b, v34
	v_mul_f32_e32 v59, 0xbfb8aa3b, v35
	v_exp_f32_e32 v58, v58
	v_pk_mul_f32 v[38:39], v[38:39], v[50:51]
	v_mul_f32_e32 v50, 0xbfb8aa3b, v40
	v_mul_f32_e32 v51, 0xbfb8aa3b, v41
	v_exp_f32_e32 v50, v50
	v_exp_f32_e32 v51, v51
	v_exp_f32_e32 v59, v59
	v_pk_mul_f32 v[38:39], v[38:39], v[66:67]
	v_add_f32_e32 v50, 1.0, v50
	v_add_f32_e32 v51, 1.0, v51
	v_rcp_f32_e32 v50, v50
	v_rcp_f32_e32 v51, v51
	v_or_b32_e32 v52, 32, v2
	v_mad_i64_i32 v[52:53], s[34:35], v52, s21, v[4:5]
	v_pk_mul_f32 v[40:41], v[40:41], v[50:51]
	v_add_f32_e32 v50, 1.0, v58
	v_add_f32_e32 v51, 1.0, v59
	v_mul_f32_e32 v58, 0xbfb8aa3b, v36
	v_mul_f32_e32 v59, 0xbfb8aa3b, v37
	v_exp_f32_e32 v58, v58
	v_exp_f32_e32 v59, v59
	v_rcp_f32_e32 v50, v50
	v_rcp_f32_e32 v51, v51
	v_add_f32_e32 v58, 1.0, v58
	v_add_f32_e32 v59, 1.0, v59
	v_rcp_f32_e32 v58, v58
	v_rcp_f32_e32 v59, v59
	v_pk_mul_f32 v[34:35], v[34:35], v[50:51]
	v_pk_mul_f32 v[40:41], v[40:41], v[68:69]
	v_pk_mul_f32 v[50:51], v[34:35], v[70:71]
	v_pk_mul_f32 v[34:35], v[36:37], v[58:59]
	v_lshl_add_u64 v[52:53], v[52:53], 0, v[74:75]
	v_pk_mul_f32 v[58:59], v[34:35], v[72:73]
	v_cvt_pk_bf16_f32 v34, v38, v39
	v_mul_f32_e32 v38, 0xbfb8aa3b, v22
	v_mul_f32_e32 v39, 0xbfb8aa3b, v23
	v_exp_f32_e32 v38, v38
	v_exp_f32_e32 v39, v39
	v_cvt_pk_bf16_f32 v35, v40, v41
	v_cvt_pk_bf16_f32 v36, v50, v51
	v_cvt_pk_bf16_f32 v37, v58, v59
	global_store_dwordx4 v[52:53], v[34:37], off
	v_readlane_b32 s61, v254, 6
	s_nop 0
	v_add_f32_e32 v34, 1.0, v38
	v_add_f32_e32 v35, 1.0, v39
	v_rcp_f32_e32 v34, v34
	v_rcp_f32_e32 v35, v35
	v_mul_f32_e32 v38, 0xbfb8aa3b, v18
	v_mul_f32_e32 v39, 0xbfb8aa3b, v19
	v_exp_f32_e32 v38, v38
	v_pk_mul_f32 v[22:23], v[22:23], v[34:35]
	v_mul_f32_e32 v34, 0xbfb8aa3b, v24
	v_mul_f32_e32 v35, 0xbfb8aa3b, v25
	v_exp_f32_e32 v34, v34
	v_exp_f32_e32 v35, v35
	v_exp_f32_e32 v39, v39
; __device__ __forceinline__ unsigned cvt_pk_bf16(float lo, float hi) { const f32x2 v = {lo, hi}; const bf16x2_t b = __builtin_convertvector(v, bf16x2_t); return __builtin_bit_cast(unsigned, b); }
; __device__ __forceinline__ float fast_silu(float x) { return x * __builtin_amdgcn_rcpf(1.f + __builtin_amdgcn_exp2f(-1.4426950408889634f * x)); }
;     __device__ __forceinline__ void operator()(const f32x4 (&acc)[2][2][4][2], const Unit& u, int wr, int wc, int fr, int fq) const {
;         const int row0 = u.pm * BM + wr * 64 + fr, col0 = u.pn * HALF + wc * 32 + 8 * fq;
; #pragma unroll
;         for (int ai = 0; ai < 2; ++ai)
; #pragma unroll
;             for (int m = 0; m < 4; ++m) { bf16_t* rowp = O + (size_t)(row0 + ai * HALF + m * 16) * ldc + col0;
;                 float o[8];
; #pragma unroll
;                 for (int n = 0; n < 2; ++n)
; #pragma unroll
;                     for (int i = 0; i < 4; ++i) o[n * 4 + i] = fast_silu(acc[ai][0][m][n][i]) * acc[ai][1][m][n][i];
;                 u32x4 w; w.x = cvt_pk_bf16(o[0], o[1]); w.y = cvt_pk_bf16(o[2], o[3]); w.z = cvt_pk_bf16(o[4], o[5]); w.w = cvt_pk_bf16(o[6], o[7]);
;                 *(u32x4*)rowp = w; }
;     }
	v_pk_mul_f32 v[22:23], v[22:23], v[42:43]
	v_add_f32_e32 v34, 1.0, v34
	v_add_f32_e32 v35, 1.0, v35
	v_rcp_f32_e32 v34, v34
	v_rcp_f32_e32 v35, v35
	v_or_b32_e32 v36, 48, v2
	v_mad_i64_i32 v[36:37], s[34:35], v36, s21, v[4:5]
	v_pk_mul_f32 v[24:25], v[24:25], v[34:35]
	v_add_f32_e32 v34, 1.0, v38
	v_add_f32_e32 v35, 1.0, v39
	v_mul_f32_e32 v38, 0xbfb8aa3b, v20
	v_mul_f32_e32 v39, 0xbfb8aa3b, v21
	v_exp_f32_e32 v38, v38
	v_exp_f32_e32 v39, v39
	v_rcp_f32_e32 v34, v34
	v_rcp_f32_e32 v35, v35
	v_add_f32_e32 v38, 1.0, v38
	v_add_f32_e32 v39, 1.0, v39
	v_rcp_f32_e32 v38, v38
	v_rcp_f32_e32 v39, v39
	v_pk_mul_f32 v[18:19], v[18:19], v[34:35]
	v_pk_mul_f32 v[24:25], v[24:25], v[44:45]
	v_pk_mul_f32 v[34:35], v[18:19], v[46:47]
	v_pk_mul_f32 v[18:19], v[20:21], v[38:39]
	v_lshl_add_u64 v[36:37], v[36:37], 0, v[74:75]
	v_pk_mul_f32 v[38:39], v[18:19], v[48:49]
	v_cvt_pk_bf16_f32 v18, v22, v23
	v_mul_f32_e32 v22, 0xbfb8aa3b, v30
	v_mul_f32_e32 v23, 0xbfb8aa3b, v31
	v_exp_f32_e32 v22, v22
	v_exp_f32_e32 v23, v23
	v_cvt_pk_bf16_f32 v19, v24, v25
	v_cvt_pk_bf16_f32 v20, v34, v35
	v_cvt_pk_bf16_f32 v21, v38, v39
	global_store_dwordx4 v[36:37], v[18:21], off
	v_mul_f32_e32 v24, 0xbfb8aa3b, v26
	v_mul_f32_e32 v25, 0xbfb8aa3b, v27
	v_add_f32_e32 v18, 1.0, v22
	v_add_f32_e32 v19, 1.0, v23
	v_rcp_f32_e32 v18, v18
	v_rcp_f32_e32 v19, v19
	v_mul_f32_e32 v22, 0xbfb8aa3b, v32
	v_mul_f32_e32 v23, 0xbfb8aa3b, v33
	v_exp_f32_e32 v22, v22
	v_exp_f32_e32 v23, v23
	v_pk_mul_f32 v[18:19], v[30:31], v[18:19]
	v_mul_f32_e32 v30, 0xbfb8aa3b, v28
	v_mul_f32_e32 v31, 0xbfb8aa3b, v29
	v_add_f32_e32 v22, 1.0, v22
	v_add_f32_e32 v23, 1.0, v23
	v_exp_f32_e32 v24, v24
	v_exp_f32_e32 v25, v25
	v_exp_f32_e32 v30, v30
	v_exp_f32_e32 v31, v31
	v_rcp_f32_e32 v22, v22
	v_rcp_f32_e32 v23, v23
	v_add_f32_e32 v24, 1.0, v24
	v_add_f32_e32 v25, 1.0, v25
	v_add_f32_e32 v30, 1.0, v30
	v_add_f32_e32 v31, 1.0, v31
	v_pk_mul_f32 v[22:23], v[32:33], v[22:23]
	v_rcp_f32_e32 v24, v24
	v_rcp_f32_e32 v25, v25
	v_rcp_f32_e32 v30, v30
	v_rcp_f32_e32 v31, v31
	v_pk_mul_f32 v[18:19], v[18:19], v[130:131]
	v_pk_mul_f32 v[22:23], v[22:23], v[132:133]
	v_cvt_pk_bf16_f32 v18, v18, v19
	v_cvt_pk_bf16_f32 v19, v22, v23
	v_mul_f32_e32 v22, 0xbfb8aa3b, v14
	v_mul_f32_e32 v23, 0xbfb8aa3b, v15
	v_exp_f32_e32 v22, v22
	v_exp_f32_e32 v23, v23
	v_add_u32_e32 v20, 0x80, v2
	v_pk_mul_f32 v[24:25], v[26:27], v[24:25]
	v_pk_mul_f32 v[26:27], v[28:29], v[30:31]
	v_mad_i64_i32 v[20:21], s[34:35], v20, s21, v[4:5]
	v_pk_mul_f32 v[24:25], v[24:25], v[126:127]
	v_pk_mul_f32 v[26:27], v[26:27], v[128:129]
	v_lshl_add_u64 v[28:29], v[20:21], 0, v[74:75]
	v_cvt_pk_bf16_f32 v20, v24, v25
	v_cvt_pk_bf16_f32 v21, v26, v27
	global_store_dwordx4 v[28:29], v[18:21], off
	s_nop 1
	v_add_f32_e32 v18, 1.0, v22
	v_add_f32_e32 v19, 1.0, v23
	v_rcp_f32_e32 v18, v18
	v_rcp_f32_e32 v19, v19
	v_mul_f32_e32 v22, 0xbfb8aa3b, v10
	v_mul_f32_e32 v23, 0xbfb8aa3b, v11
	v_exp_f32_e32 v22, v22
	v_pk_mul_f32 v[14:15], v[14:15], v[18:19]
	v_mul_f32_e32 v18, 0xbfb8aa3b, v16
	v_mul_f32_e32 v19, 0xbfb8aa3b, v17
	v_exp_f32_e32 v18, v18
	v_exp_f32_e32 v19, v19
	v_exp_f32_e32 v23, v23
	v_pk_mul_f32 v[14:15], v[14:15], v[118:119]
	v_add_f32_e32 v18, 1.0, v18
	v_add_f32_e32 v19, 1.0, v19
	v_rcp_f32_e32 v18, v18
	v_rcp_f32_e32 v19, v19
	v_add_u32_e32 v20, 0x90, v2
	v_mad_i64_i32 v[20:21], s[34:35], v20, s21, v[4:5]
	v_pk_mul_f32 v[16:17], v[16:17], v[18:19]
	v_add_f32_e32 v18, 1.0, v22
	v_add_f32_e32 v19, 1.0, v23
	v_mul_f32_e32 v22, 0xbfb8aa3b, v12
	v_mul_f32_e32 v23, 0xbfb8aa3b, v13
	v_exp_f32_e32 v22, v22
	v_exp_f32_e32 v23, v23
	v_rcp_f32_e32 v18, v18
	v_rcp_f32_e32 v19, v19
	v_add_f32_e32 v22, 1.0, v22
	v_add_f32_e32 v23, 1.0, v23
; __device__ __forceinline__ unsigned cvt_pk_bf16(float lo, float hi) { const f32x2 v = {lo, hi}; const bf16x2_t b = __builtin_convertvector(v, bf16x2_t); return __builtin_bit_cast(unsigned, b); }
; #define ZERO4() ((f32x4){opaque0(), 0.f, 0.f, 0.f} * 0.f)
; __device__ __forceinline__ float fast_silu(float x) { return x * __builtin_amdgcn_rcpf(1.f + __builtin_amdgcn_exp2f(-1.4426950408889634f * x)); }
; #define PG8_BAR __builtin_amdgcn_s_barrier()
;     __device__ __forceinline__ void operator()(const f32x4 (&acc)[2][2][4][2], const Unit& u, int wr, int wc, int fr, int fq) const {
;         const int row0 = u.pm * BM + wr * 64 + fr, col0 = u.pn * HALF + wc * 32 + 8 * fq;
; #pragma unroll
;         for (int ai = 0; ai < 2; ++ai)
; #pragma unroll
;             for (int m = 0; m < 4; ++m) { bf16_t* rowp = O + (size_t)(row0 + ai * HALF + m * 16) * ldc + col0;
;                 float o[8];
; #pragma unroll
;                 for (int n = 0; n < 2; ++n)
; #pragma unroll
;                     for (int i = 0; i < 4; ++i) o[n * 4 + i] = fast_silu(acc[ai][0][m][n][i]) * acc[ai][1][m][n][i];
;                 u32x4 w; w.x = cvt_pk_bf16(o[0], o[1]); w.y = cvt_pk_bf16(o[2], o[3]); w.z = cvt_pk_bf16(o[4], o[5]); w.w = cvt_pk_bf16(o[6], o[7]);
;                 *(u32x4*)rowp = w; }
;     }
; template <class Epi, class Sched, bool GATHER = false>
; __device__ __forceinline__ void gemm_phase(LAS unsigned char* lds, const Gemm g, const Sched& S, const Epi& E, const int tid) {
;     ...
;         if (!has_next) break;
; #pragma unroll
;         for (int a = 0; a < 2; ++a)
; #pragma unroll
;             for (int b = 0; b < 2; ++b)
; #pragma unroll
;                 for (int m = 0; m < 4; ++m)
; #pragma unroll
;                     for (int n = 0; n < 2; ++n) acc[a][b][m][n] = ZERO4();
;         cur = nxt; cA = nA; cB = nB; ++ui;
;         if (GATHER) {
; #pragma unroll
;             for (int h_ = 0; h_ < 2; ++h_) { goC[h_][0] = goN[h_][0]; goC[h_][1] = goN[h_][1]; } }
;         if (wr == 1) PG8_BAR;
	v_rcp_f32_e32 v22, v22
	v_rcp_f32_e32 v23, v23
	v_pk_mul_f32 v[10:11], v[10:11], v[18:19]
	v_pk_mul_f32 v[16:17], v[16:17], v[120:121]
	v_pk_mul_f32 v[18:19], v[10:11], v[114:115]
	v_pk_mul_f32 v[10:11], v[12:13], v[22:23]
	v_lshl_add_u64 v[20:21], v[20:21], 0, v[74:75]
	v_pk_mul_f32 v[22:23], v[10:11], v[116:117]
	v_cvt_pk_bf16_f32 v10, v14, v15
	v_mul_f32_e32 v14, 0xbfb8aa3b, v6
	v_mul_f32_e32 v15, 0xbfb8aa3b, v7
	v_exp_f32_e32 v14, v14
	v_exp_f32_e32 v15, v15
	v_cvt_pk_bf16_f32 v11, v16, v17
	v_cvt_pk_bf16_f32 v12, v18, v19
	v_cvt_pk_bf16_f32 v13, v22, v23
	global_store_dwordx4 v[20:21], v[10:13], off
	s_nop 1
	v_add_f32_e32 v10, 1.0, v14
	v_add_f32_e32 v11, 1.0, v15
	v_rcp_f32_e32 v10, v10
	v_rcp_f32_e32 v11, v11
	v_mul_f32_e32 v14, 0xbfb8aa3b, v78
	v_mul_f32_e32 v15, 0xbfb8aa3b, v79
	v_exp_f32_e32 v14, v14
	v_pk_mul_f32 v[6:7], v[6:7], v[10:11]
	v_mul_f32_e32 v10, 0xbfb8aa3b, v8
	v_mul_f32_e32 v11, 0xbfb8aa3b, v9
	v_exp_f32_e32 v10, v10
	v_exp_f32_e32 v11, v11
	v_exp_f32_e32 v15, v15
	v_add_u32_e32 v12, 0xa0, v2
	v_add_f32_e32 v10, 1.0, v10
	v_add_f32_e32 v11, 1.0, v11
	v_rcp_f32_e32 v10, v10
	v_rcp_f32_e32 v11, v11
	v_mad_i64_i32 v[12:13], s[34:35], v12, s21, v[4:5]
	v_pk_mul_f32 v[6:7], v[6:7], v[102:103]
	v_pk_mul_f32 v[8:9], v[8:9], v[10:11]
	v_add_f32_e32 v10, 1.0, v14
	v_add_f32_e32 v11, 1.0, v15
	v_mul_f32_e32 v14, 0xbfb8aa3b, v80
	v_mul_f32_e32 v15, 0xbfb8aa3b, v81
	v_exp_f32_e32 v14, v14
	v_exp_f32_e32 v15, v15
	v_rcp_f32_e32 v10, v10
	v_rcp_f32_e32 v11, v11
	v_add_f32_e32 v14, 1.0, v14
	v_add_f32_e32 v15, 1.0, v15
	v_rcp_f32_e32 v14, v14
	v_rcp_f32_e32 v15, v15
	v_pk_mul_f32 v[10:11], v[78:79], v[10:11]
	v_pk_mul_f32 v[8:9], v[8:9], v[104:105]
	v_pk_mul_f32 v[10:11], v[10:11], v[98:99]
	v_pk_mul_f32 v[14:15], v[80:81], v[14:15]
	v_add_u32_e32 v2, 0xb0, v2
	v_pk_mul_f32 v[14:15], v[14:15], v[100:101]
	v_lshl_add_u64 v[12:13], v[12:13], 0, v[74:75]
	v_cvt_pk_bf16_f32 v6, v6, v7
	v_cvt_pk_bf16_f32 v7, v8, v9
	v_cvt_pk_bf16_f32 v8, v10, v11
	v_cvt_pk_bf16_f32 v9, v14, v15
	v_mad_i64_i32 v[4:5], s[34:35], v2, s21, v[4:5]
	v_mul_f32_e32 v2, 0xbfb8aa3b, v64
	global_store_dwordx4 v[12:13], v[6:9], off
	v_exp_f32_e32 v2, v2
	v_mul_f32_e32 v10, 0xbfb8aa3b, v62
	v_mul_f32_e32 v8, 0xbfb8aa3b, v65
	v_exp_f32_e32 v9, v8
	v_exp_f32_e32 v10, v10
	v_mul_f32_e32 v11, 0xbfb8aa3b, v63
	v_exp_f32_e32 v11, v11
	v_add_f32_e32 v2, 1.0, v2
	v_rcp_f32_e32 v8, v2
	v_add_f32_e32 v2, 1.0, v9
	v_rcp_f32_e32 v9, v2
	v_mul_f32_e32 v2, 0xbfb8aa3b, v54
	v_add_f32_e32 v6, 1.0, v10
	v_exp_f32_e32 v2, v2
	v_mul_f32_e32 v10, 0xbfb8aa3b, v55
	v_add_f32_e32 v7, 1.0, v11
	v_exp_f32_e32 v11, v10
	v_add_f32_e32 v2, 1.0, v2
	v_rcp_f32_e32 v10, v2
	v_rcp_f32_e32 v6, v6
	v_add_f32_e32 v2, 1.0, v11
	v_mul_f32_e32 v11, 0xbfb8aa3b, v56
	v_exp_f32_e32 v12, v11
	v_mul_f32_e32 v11, 0xbfb8aa3b, v57
	v_exp_f32_e32 v13, v11
	v_rcp_f32_e32 v11, v2
	v_add_f32_e32 v2, 1.0, v12
	v_rcp_f32_e32 v12, v2
	v_add_f32_e32 v2, 1.0, v13
	v_rcp_f32_e32 v7, v7
	v_rcp_f32_e32 v13, v2
	v_pk_mul_f32 v[8:9], v[64:65], v[8:9]
	v_pk_mul_f32 v[10:11], v[54:55], v[10:11]
	v_pk_mul_f32 v[6:7], v[62:63], v[6:7]
	v_pk_mul_f32 v[12:13], v[56:57], v[12:13]
	v_pk_mul_f32 v[6:7], v[6:7], v[86:87]
	v_pk_mul_f32 v[8:9], v[8:9], v[88:89]
	v_pk_mul_f32 v[10:11], v[10:11], v[82:83]
	v_pk_mul_f32 v[12:13], v[12:13], v[84:85]
	v_lshl_add_u64 v[14:15], v[4:5], 0, v[74:75]
	v_cvt_pk_bf16_f32 v4, v6, v7
	v_cvt_pk_bf16_f32 v5, v8, v9
	v_cvt_pk_bf16_f32 v6, v10, v11
	v_cvt_pk_bf16_f32 v7, v12, v13
	global_store_dwordx4 v[14:15], v[4:7], off
	s_cbranch_vccnz .LBB0_1363
	v_mov_b32_e32 v2, v3
	s_andn2_b64 vcc, exec, s[2:3]
	s_cbranch_vccnz .LBB0_1362
	s_barrier
	s_branch .LBB0_1362

; #define PG8_STAGE_A(bufoff, base_, nx_, kb_, h_) do { if (GATHER) { if (nx_) PG8_STAGE_G(bufoff, kb_, goN, h_); else PG8_STAGE_G(bufoff, kb_, goC, h_); } \
;         else PG8_STAGE(bufoff, (base_) + (kb_) + (h_) * hstep, voffA); } while (0)
; #define PG8_STAGE(bufoff, gbase, voff) do { _Pragma("unroll") for (int _i = 0; _i < 2; ++_i) \
;         __builtin_amdgcn_global_load_lds((const unsigned*)((const char*)(gbase) + (voff)[_i]), (LAS unsigned*)(lds + (bufoff) + ldsw + _i * 8192), 16, 0, 0); } while (0)
; #define PG8_LDA(dst, b, h) do { _Pragma("unroll") for (int m = 0; m < 4; ++m) _Pragma("unroll") for (int k = 0; k < 2; ++k) dst[m][k] = *(const LAS bf16x8*)(lds + PG8_SA(b, h) + aoff + m * 2048 + k * 1024); } while (0)
; #define PG8_LDB(dst, b, h) do { _Pragma("unroll") for (int n = 0; n < 2; ++n) _Pragma("unroll") for (int k = 0; k < 2; ++k) dst[n][k] = *(const LAS bf16x8*)(lds + PG8_SB(b, h) + boff + n * 2048 + k * 1024); } while (0)
; #define PG8_WAIT_V(n) asm volatile("s_waitcnt vmcnt(" #n ")" ::: "memory")
; #define PG8_WAIT_L(n) asm volatile("s_waitcnt lgkmcnt(" #n ")" ::: "memory")
; #define PG8_BAR __builtin_amdgcn_s_barrier()
; #define PG8_SCHED __builtin_amdgcn_sched_barrier(0)
; template <class Epi, class Sched, bool GATHER = false>
; __device__ __forceinline__ void gemm_phase(LAS unsigned char* lds, const Gemm g, const Sched& S, const Epi& E, const int tid) {
;     ...
;         for (int t = 0; t < nt; t += 2) {
;             const bool last = (t == nt - 2);
;             const char* a1 = cA + (size_t)(t + 1) * kstep;
;             const char* a2 = last ? nA : cA + (size_t)(t + 2) * kstep; const char* b2 = last ? nB : cB + (size_t)(t + 2) * kstep;
;             const char* a3 = a2 + kstep; const char* b3 = b2 + kstep;
;     ...
;             PG8_LDB(B0, 0, 0); PG8_LDB(B1, 0, 1); PG8_SCHED; PG8_LDA(At, 0, 0); PG8_STAGE_A(PG8_SA(1, 1), cA, false, kb1, 1);
;             PG8_WAIT_V(8); PG8_WAIT_L(0); PG8_BAR; PG8_MMA(0, 0, At, B0); PG8_MMA(0, 1, At, B1); PG8_BAR; PG8_SCHED;
;             PG8_LDA(At, 0, 1); PG8_STAGE(PG8_SB(0, 0), b2, voffB); PG8_STAGE(PG8_SB(0, 1), b2 + hstep, voffB); PG8_STAGE_A(PG8_SA(0, 0), (last ? nA : cA), last, kb2, 0);
;             PG8_WAIT_V(8); PG8_WAIT_L(0); PG8_BAR; PG8_MMA(1, 0, At, B0); PG8_MMA(1, 1, At, B1); PG8_BAR; PG8_SCHED;
.LBB0_1482:
	s_add_u32 s56, s28, 0x100
	s_addc_u32 s57, s29, 0
	s_add_u32 s28, s14, 0x160080
	s_addc_u32 s29, s15, 0
	v_lshl_add_u64 v[4:5], s[28:29], 0, v[142:143]
	v_lshl_add_u64 v[146:147], s[28:29], 0, v[144:145]
	s_mov_b32 s58, -2
	s_mov_b64 s[34:35], 0
	s_add_u32 s28, s34, 0x100
	s_addc_u32 s29, s35, 0
	s_add_u32 s30, s56, s34
	s_addc_u32 s31, s57, s35
	s_add_i32 s59, 0, 0x10000
	s_add_i32 s60, 0, 0x14000
	v_add_u32_e32 v2, s59, v149
	ds_read_b128 v[152:155], v2
	ds_read_b128 v[156:159], v2 offset:1024
	ds_read_b128 v[160:163], v2 offset:2048
	ds_read_b128 v[164:167], v2 offset:3072
	v_add_u32_e32 v2, s60, v149
	ds_read_b128 v[168:171], v2
	ds_read_b128 v[172:175], v2 offset:1024
	ds_read_b128 v[176:179], v2 offset:2048
	ds_read_b128 v[180:183], v2 offset:3072
	s_add_i32 s62, s59, s33
	s_add_i32 m0, s44, 0xc000
	s_add_i32 s61, s44, 0xe000
	s_add_i32 s59, s62, 0x2000
	s_cmpk_eq_i32 s58, 0x54
	s_cselect_b32 s31, s25, s31
	s_cselect_b32 s30, s24, s30
	v_lshl_add_u64 v[218:219], v[4:5], 0, s[34:35]
	ds_read_b128 v[184:187], v151
	ds_read_b128 v[188:191], v151 offset:1024
	ds_read_b128 v[192:195], v151 offset:2048
	ds_read_b128 v[196:199], v151 offset:3072
	ds_read_b128 v[202:205], v151 offset:4096
	ds_read_b128 v[206:209], v151 offset:5120
	ds_read_b128 v[210:213], v151 offset:6144
	ds_read_b128 v[214:217], v151 offset:7168
	global_load_lds_dwordx4 v[218:219], off
	v_lshl_add_u64 v[218:219], v[146:147], 0, s[34:35]
	s_mov_b32 m0, s61
	s_nop 0
	global_load_lds_dwordx4 v[218:219], off
	s_waitcnt vmcnt(8)
	s_waitcnt lgkmcnt(0)
	s_barrier
	s_waitcnt lgkmcnt(0)
	v_mfma_f32_16x16x32_bf16 v[86:89], v[152:155], v[184:187], 0
	v_mfma_f32_16x16x32_bf16 v[18:21], v[160:163], v[184:187], 0
	v_mfma_f32_16x16x32_bf16 v[6:9], v[152:155], v[192:195], 0
	v_mfma_f32_16x16x32_bf16 v[22:25], v[160:163], v[192:195], 0
	v_mfma_f32_16x16x32_bf16 v[10:13], v[152:155], v[202:205], 0
	v_mfma_f32_16x16x32_bf16 v[26:29], v[160:163], v[202:205], 0
	v_mfma_f32_16x16x32_bf16 v[14:17], v[152:155], v[210:213], 0
	v_mfma_f32_16x16x32_bf16 v[30:33], v[160:163], v[210:213], 0
	v_mfma_f32_16x16x32_bf16 v[86:89], v[156:159], v[188:191], v[86:89]
	v_mfma_f32_16x16x32_bf16 v[18:21], v[164:167], v[188:191], v[18:21]
	v_mfma_f32_16x16x32_bf16 v[6:9], v[156:159], v[196:199], v[6:9]
	v_mfma_f32_16x16x32_bf16 v[22:25], v[164:167], v[196:199], v[22:25]
	v_mfma_f32_16x16x32_bf16 v[10:13], v[156:159], v[206:209], v[10:13]
	v_mfma_f32_16x16x32_bf16 v[26:29], v[164:167], v[206:209], v[26:29]
	v_mfma_f32_16x16x32_bf16 v[14:17], v[156:159], v[214:217], v[14:17]
	v_mfma_f32_16x16x32_bf16 v[30:33], v[164:167], v[214:217], v[30:33]
	v_mfma_f32_16x16x32_bf16 v[34:37], v[168:171], v[184:187], 0
	v_mfma_f32_16x16x32_bf16 v[50:53], v[176:179], v[184:187], 0
	v_mfma_f32_16x16x32_bf16 v[38:41], v[168:171], v[192:195], 0
	v_mfma_f32_16x16x32_bf16 v[54:57], v[176:179], v[192:195], 0
	v_mfma_f32_16x16x32_bf16 v[42:45], v[168:171], v[202:205], 0
	v_mfma_f32_16x16x32_bf16 v[62:65], v[176:179], v[202:205], 0
	v_mfma_f32_16x16x32_bf16 v[46:49], v[168:171], v[210:213], 0
	v_mfma_f32_16x16x32_bf16 v[70:73], v[176:179], v[210:213], 0
	v_mfma_f32_16x16x32_bf16 v[34:37], v[172:175], v[188:191], v[34:37]
	v_mfma_f32_16x16x32_bf16 v[50:53], v[180:183], v[188:191], v[50:53]
	v_mfma_f32_16x16x32_bf16 v[38:41], v[172:175], v[196:199], v[38:41]
	v_mfma_f32_16x16x32_bf16 v[54:57], v[180:183], v[196:199], v[54:57]
	v_mfma_f32_16x16x32_bf16 v[42:45], v[172:175], v[206:209], v[42:45]
	v_mfma_f32_16x16x32_bf16 v[62:65], v[180:183], v[206:209], v[62:65]
	v_mfma_f32_16x16x32_bf16 v[46:49], v[172:175], v[214:217], v[46:49]
	v_mfma_f32_16x16x32_bf16 v[70:73], v[180:183], v[214:217], v[70:73]
	s_barrier
	s_mov_b32 m0, s62
	v_lshl_add_u64 v[218:219], s[30:31], 0, v[136:137]
	ds_read_b128 v[184:187], v151 offset:16384
	ds_read_b128 v[188:191], v151 offset:17408
	ds_read_b128 v[192:195], v151 offset:18432
	ds_read_b128 v[196:199], v151 offset:19456
	ds_read_b128 v[202:205], v151 offset:20480
	ds_read_b128 v[206:209], v151 offset:21504
	ds_read_b128 v[210:213], v151 offset:22528
	ds_read_b128 v[214:217], v151 offset:23552
	global_load_lds_dwordx4 v[218:219], off
	s_mov_b32 m0, s59
	s_cselect_b32 s59, 0, s29
	s_cselect_b32 s61, 0, s28
	s_cselect_b32 s62, s11, s15
	s_cselect_b32 s63, s10, s14
	s_add_u32 s34, s30, 0x160000
	v_lshl_add_u64 v[220:221], s[30:31], 0, v[140:141]
	s_addc_u32 s35, s31, 0
	s_add_i32 s60, s60, s33
	global_load_lds_dwordx4 v[220:221], off
	v_lshl_add_u64 v[222:223], s[34:35], 0, v[136:137]
	s_mov_b32 m0, s60
	s_nop 0
	global_load_lds_dwordx4 v[222:223], off
	s_add_i32 m0, s60, 0x2000
	v_lshl_add_u64 v[222:223], s[34:35], 0, v[140:141]
	s_add_u32 s34, s63, s61
	s_addc_u32 s35, s62, s59
	global_load_lds_dwordx4 v[222:223], off
	v_lshl_add_u64 v[222:223], s[34:35], 0, v[134:135]
	s_mov_b32 m0, s44
	v_lshl_add_u64 v[224:225], s[34:35], 0, v[138:139]
	global_load_lds_dwordx4 v[222:223], off
	s_mov_b32 m0, s45
	s_nop 0
	global_load_lds_dwordx4 v[224:225], off
	s_waitcnt vmcnt(8)
	s_waitcnt lgkmcnt(0)
	s_barrier
; #define PG8_STAGE_A(bufoff, base_, nx_, kb_, h_) do { if (GATHER) { if (nx_) PG8_STAGE_G(bufoff, kb_, goN, h_); else PG8_STAGE_G(bufoff, kb_, goC, h_); } \
;         else PG8_STAGE(bufoff, (base_) + (kb_) + (h_) * hstep, voffA); } while (0)
; #define PG8_LDA(dst, b, h) do { _Pragma("unroll") for (int m = 0; m < 4; ++m) _Pragma("unroll") for (int k = 0; k < 2; ++k) dst[m][k] = *(const LAS bf16x8*)(lds + PG8_SA(b, h) + aoff + m * 2048 + k * 1024); } while (0)
; #define PG8_LDB(dst, b, h) do { _Pragma("unroll") for (int n = 0; n < 2; ++n) _Pragma("unroll") for (int k = 0; k < 2; ++k) dst[n][k] = *(const LAS bf16x8*)(lds + PG8_SB(b, h) + boff + n * 2048 + k * 1024); } while (0)
; #define PG8_MMA(ai, bj, At, Bt) do { __builtin_amdgcn_s_setprio(1); _Pragma("unroll") for (int m = 0; m < 4; ++m) _Pragma("unroll") for (int n = 0; n < 2; ++n) _Pragma("unroll") for (int k = 0; k < 2; ++k) \
;         acc[ai][bj][m][n] = __builtin_amdgcn_mfma_f32_16x16x32_bf16(Bt[n][k], At[m][k], acc[ai][bj][m][n], 0, 0, 0); __builtin_amdgcn_s_setprio(0); } while (0)
; #define PG8_WAIT_V(n) asm volatile("s_waitcnt vmcnt(" #n ")" ::: "memory")
; #define PG8_WAIT_L(n) asm volatile("s_waitcnt lgkmcnt(" #n ")" ::: "memory")
; #define PG8_BAR __builtin_amdgcn_s_barrier()
; #define PG8_SCHED __builtin_amdgcn_sched_barrier(0)
; template <class Epi, class Sched, bool GATHER = false>
; __device__ __forceinline__ void gemm_phase(LAS unsigned char* lds, const Gemm g, const Sched& S, const Epi& E, const int tid) {
;     ...
;             PG8_WAIT_V(8); PG8_WAIT_L(0); PG8_BAR; PG8_MMA(1, 0, At, B0); PG8_MMA(1, 1, At, B1); PG8_BAR; PG8_SCHED;
;             PG8_LDB(B0, 1, 0); PG8_LDB(B1, 1, 1); PG8_SCHED; PG8_LDA(At, 1, 0); PG8_STAGE_A(PG8_SA(0, 1), (last ? nA : cA), last, kb2, 1);
;             PG8_WAIT_V(8); PG8_WAIT_L(0); PG8_BAR; PG8_MMA(0, 0, At, B0); PG8_MMA(0, 1, At, B1); PG8_BAR; PG8_SCHED;
	s_waitcnt lgkmcnt(0)
	v_mfma_f32_16x16x32_bf16 v[58:61], v[152:155], v[184:187], 0
	v_mfma_f32_16x16x32_bf16 v[78:81], v[160:163], v[184:187], 0
	v_mfma_f32_16x16x32_bf16 v[66:69], v[152:155], v[192:195], 0
	v_mfma_f32_16x16x32_bf16 v[82:85], v[160:163], v[192:195], 0
	v_mfma_f32_16x16x32_bf16 v[74:77], v[152:155], v[202:205], 0
	v_mfma_f32_16x16x32_bf16 v[98:101], v[160:163], v[202:205], 0
	v_mfma_f32_16x16x32_bf16 v[90:93], v[152:155], v[210:213], 0
	v_mfma_f32_16x16x32_bf16 v[94:97], v[160:163], v[210:213], 0
	v_mfma_f32_16x16x32_bf16 v[58:61], v[156:159], v[188:191], v[58:61]
	v_mfma_f32_16x16x32_bf16 v[78:81], v[164:167], v[188:191], v[78:81]
	v_mfma_f32_16x16x32_bf16 v[66:69], v[156:159], v[196:199], v[66:69]
	v_mfma_f32_16x16x32_bf16 v[82:85], v[164:167], v[196:199], v[82:85]
	v_mfma_f32_16x16x32_bf16 v[74:77], v[156:159], v[206:209], v[74:77]
	v_mfma_f32_16x16x32_bf16 v[98:101], v[164:167], v[206:209], v[98:101]
	v_mfma_f32_16x16x32_bf16 v[90:93], v[156:159], v[214:217], v[90:93]
	v_mfma_f32_16x16x32_bf16 v[94:97], v[164:167], v[214:217], v[94:97]
	v_mfma_f32_16x16x32_bf16 v[114:117], v[168:171], v[184:187], 0
	v_mfma_f32_16x16x32_bf16 v[130:133], v[176:179], v[184:187], 0
	v_mfma_f32_16x16x32_bf16 v[110:113], v[168:171], v[192:195], 0
	v_mfma_f32_16x16x32_bf16 v[126:129], v[176:179], v[192:195], 0
	v_mfma_f32_16x16x32_bf16 v[106:109], v[168:171], v[202:205], 0
	v_mfma_f32_16x16x32_bf16 v[122:125], v[176:179], v[202:205], 0
	v_mfma_f32_16x16x32_bf16 v[102:105], v[168:171], v[210:213], 0
	v_mfma_f32_16x16x32_bf16 v[118:121], v[176:179], v[210:213], 0
	v_mfma_f32_16x16x32_bf16 v[114:117], v[172:175], v[188:191], v[114:117]
	v_mfma_f32_16x16x32_bf16 v[130:133], v[180:183], v[188:191], v[130:133]
	v_mfma_f32_16x16x32_bf16 v[110:113], v[172:175], v[196:199], v[110:113]
	v_mfma_f32_16x16x32_bf16 v[126:129], v[180:183], v[196:199], v[126:129]
	v_mfma_f32_16x16x32_bf16 v[106:109], v[172:175], v[206:209], v[106:109]
	v_mfma_f32_16x16x32_bf16 v[122:125], v[180:183], v[206:209], v[122:125]
	v_mfma_f32_16x16x32_bf16 v[102:105], v[172:175], v[214:217], v[102:105]
	v_mfma_f32_16x16x32_bf16 v[118:121], v[180:183], v[214:217], v[118:121]
	s_barrier
	s_add_i32 s59, 0, 0x18000
	v_add_u32_e32 v2, s59, v149
	s_add_i32 s60, 0, 0x1c000
	ds_read_b128 v[152:155], v2
	ds_read_b128 v[156:159], v2 offset:1024
	ds_read_b128 v[160:163], v2 offset:2048
	ds_read_b128 v[164:167], v2 offset:3072
	v_add_u32_e32 v2, s60, v149
	ds_read_b128 v[168:171], v2
	ds_read_b128 v[172:175], v2 offset:1024
	ds_read_b128 v[176:179], v2 offset:2048
	ds_read_b128 v[180:183], v2 offset:3072
	s_add_u32 s34, s34, 0x160000
	s_addc_u32 s35, s35, 0
	s_mov_b32 m0, s46
	v_lshl_add_u64 v[226:227], s[34:35], 0, v[134:135]
	ds_read_b128 v[184:187], v151 offset:32768
	ds_read_b128 v[188:191], v151 offset:33792
	ds_read_b128 v[192:195], v151 offset:34816
	ds_read_b128 v[196:199], v151 offset:35840
	ds_read_b128 v[202:205], v151 offset:36864
	ds_read_b128 v[206:209], v151 offset:37888
	ds_read_b128 v[210:213], v151 offset:38912
	ds_read_b128 v[214:217], v151 offset:39936
	global_load_lds_dwordx4 v[226:227], off
	v_lshl_add_u64 v[226:227], s[34:35], 0, v[138:139]
	s_mov_b32 m0, s47
	s_nop 0
	global_load_lds_dwordx4 v[226:227], off
	s_waitcnt vmcnt(8)
	s_waitcnt lgkmcnt(0)
	s_barrier
	s_waitcnt lgkmcnt(0)
	v_mfma_f32_16x16x32_bf16 v[86:89], v[152:155], v[184:187], v[86:89]
	v_mfma_f32_16x16x32_bf16 v[18:21], v[160:163], v[184:187], v[18:21]
	v_mfma_f32_16x16x32_bf16 v[6:9], v[152:155], v[192:195], v[6:9]
	v_mfma_f32_16x16x32_bf16 v[22:25], v[160:163], v[192:195], v[22:25]
	v_mfma_f32_16x16x32_bf16 v[10:13], v[152:155], v[202:205], v[10:13]
	v_mfma_f32_16x16x32_bf16 v[26:29], v[160:163], v[202:205], v[26:29]
	v_mfma_f32_16x16x32_bf16 v[14:17], v[152:155], v[210:213], v[14:17]
	v_mfma_f32_16x16x32_bf16 v[30:33], v[160:163], v[210:213], v[30:33]
	v_mfma_f32_16x16x32_bf16 v[86:89], v[156:159], v[188:191], v[86:89]
	v_mfma_f32_16x16x32_bf16 v[18:21], v[164:167], v[188:191], v[18:21]
	v_mfma_f32_16x16x32_bf16 v[6:9], v[156:159], v[196:199], v[6:9]
	v_mfma_f32_16x16x32_bf16 v[22:25], v[164:167], v[196:199], v[22:25]
	v_mfma_f32_16x16x32_bf16 v[10:13], v[156:159], v[206:209], v[10:13]
	v_mfma_f32_16x16x32_bf16 v[26:29], v[164:167], v[206:209], v[26:29]
	v_mfma_f32_16x16x32_bf16 v[14:17], v[156:159], v[214:217], v[14:17]
	v_mfma_f32_16x16x32_bf16 v[30:33], v[164:167], v[214:217], v[30:33]
	v_mfma_f32_16x16x32_bf16 v[34:37], v[168:171], v[184:187], v[34:37]
	v_mfma_f32_16x16x32_bf16 v[50:53], v[176:179], v[184:187], v[50:53]
	v_mfma_f32_16x16x32_bf16 v[38:41], v[168:171], v[192:195], v[38:41]
	v_mfma_f32_16x16x32_bf16 v[54:57], v[176:179], v[192:195], v[54:57]
	v_mfma_f32_16x16x32_bf16 v[42:45], v[168:171], v[202:205], v[42:45]
	v_mfma_f32_16x16x32_bf16 v[62:65], v[176:179], v[202:205], v[62:65]
	v_mfma_f32_16x16x32_bf16 v[46:49], v[168:171], v[210:213], v[46:49]
	v_mfma_f32_16x16x32_bf16 v[70:73], v[176:179], v[210:213], v[70:73]
	v_mfma_f32_16x16x32_bf16 v[34:37], v[172:175], v[188:191], v[34:37]
	v_mfma_f32_16x16x32_bf16 v[50:53], v[180:183], v[188:191], v[50:53]
	v_mfma_f32_16x16x32_bf16 v[38:41], v[172:175], v[196:199], v[38:41]
	v_mfma_f32_16x16x32_bf16 v[54:57], v[180:183], v[196:199], v[54:57]
	v_mfma_f32_16x16x32_bf16 v[42:45], v[172:175], v[206:209], v[42:45]
	v_mfma_f32_16x16x32_bf16 v[62:65], v[180:183], v[206:209], v[62:65]
	v_mfma_f32_16x16x32_bf16 v[46:49], v[172:175], v[214:217], v[46:49]
	v_mfma_f32_16x16x32_bf16 v[70:73], v[180:183], v[214:217], v[70:73]
	s_barrier
; #define PG8_STAGE_A(bufoff, base_, nx_, kb_, h_) do { if (GATHER) { if (nx_) PG8_STAGE_G(bufoff, kb_, goN, h_); else PG8_STAGE_G(bufoff, kb_, goC, h_); } \
;         else PG8_STAGE(bufoff, (base_) + (kb_) + (h_) * hstep, voffA); } while (0)
; #define PG8_STAGE(bufoff, gbase, voff) do { _Pragma("unroll") for (int _i = 0; _i < 2; ++_i) \
;         __builtin_amdgcn_global_load_lds((const unsigned*)((const char*)(gbase) + (voff)[_i]), (LAS unsigned*)(lds + (bufoff) + ldsw + _i * 8192), 16, 0, 0); } while (0)
; #define PG8_LDA(dst, b, h) do { _Pragma("unroll") for (int m = 0; m < 4; ++m) _Pragma("unroll") for (int k = 0; k < 2; ++k) dst[m][k] = *(const LAS bf16x8*)(lds + PG8_SA(b, h) + aoff + m * 2048 + k * 1024); } while (0)
; #define PG8_LDB(dst, b, h) do { _Pragma("unroll") for (int n = 0; n < 2; ++n) _Pragma("unroll") for (int k = 0; k < 2; ++k) dst[n][k] = *(const LAS bf16x8*)(lds + PG8_SB(b, h) + boff + n * 2048 + k * 1024); } while (0)
; #define PG8_WAIT_V(n) asm volatile("s_waitcnt vmcnt(" #n ")" ::: "memory")
; #define PG8_WAIT_L(n) asm volatile("s_waitcnt lgkmcnt(" #n ")" ::: "memory")
; template <class Epi, class Sched, bool GATHER = false>
; __device__ __forceinline__ void gemm_phase(LAS unsigned char* lds, const Gemm g, const Sched& S, const Epi& E, const int tid) {
;     ...
;             PG8_LDB(B0, 0, 0); PG8_LDB(B1, 0, 1); PG8_SCHED; PG8_LDA(At, 0, 0); PG8_STAGE_A(PG8_SA(1, 1), cA, false, kb1, 1);
;             PG8_WAIT_V(8); PG8_WAIT_L(0); PG8_BAR; PG8_MMA(0, 0, At, B0); PG8_MMA(0, 1, At, B1); PG8_BAR; PG8_SCHED;
;             PG8_LDA(At, 0, 1); PG8_STAGE(PG8_SB(0, 0), b2, voffB); PG8_STAGE(PG8_SB(0, 1), b2 + hstep, voffB); PG8_STAGE_A(PG8_SA(0, 0), (last ? nA : cA), last, kb2, 0);
;             PG8_WAIT_V(8); PG8_WAIT_L(0); PG8_BAR; PG8_MMA(1, 0, At, B0); PG8_MMA(1, 1, At, B1); PG8_BAR; PG8_SCHED;
;             PG8_LDB(B0, 1, 0); PG8_LDB(B1, 1, 1); PG8_SCHED; PG8_LDA(At, 1, 0); PG8_STAGE_A(PG8_SA(0, 1), (last ? nA : cA), last, kb2, 1);
;             PG8_WAIT_V(8); PG8_WAIT_L(0); PG8_BAR; PG8_MMA(0, 0, At, B0); PG8_MMA(0, 1, At, B1); PG8_BAR; PG8_SCHED;
;             PG8_LDA(At, 1, 1); PG8_STAGE(PG8_SB(1, 0), b3, voffB); PG8_STAGE(PG8_SB(1, 1), b3 + hstep, voffB); PG8_STAGE_A(PG8_SA(1, 0), (last ? nA : cA), last, kb3, 0);
;             PG8_WAIT_V(8); PG8_WAIT_L(0); PG8_BAR; PG8_MMA(1, 0, At, B0); PG8_MMA(1, 1, At, B1); PG8_BAR; PG8_SCHED;
	s_add_i32 s34, s59, s33
	v_lshl_add_u64 v[218:219], v[218:219], 0, s[0:1]
	s_mov_b32 m0, s34
	ds_read_b128 v[184:187], v151 offset:49152
	ds_read_b128 v[188:191], v151 offset:50176
	ds_read_b128 v[192:195], v151 offset:51200
	ds_read_b128 v[196:199], v151 offset:52224
	ds_read_b128 v[202:205], v151 offset:53248
	ds_read_b128 v[206:209], v151 offset:54272
	ds_read_b128 v[210:213], v151 offset:55296
	ds_read_b128 v[214:217], v151 offset:56320
	global_load_lds_dwordx4 v[218:219], off
	s_add_i32 m0, s34, 0x2000
	s_add_u32 s30, s30, 0x160080
	v_lshl_add_u64 v[218:219], v[220:221], 0, s[0:1]
	s_addc_u32 s31, s31, 0
	s_add_i32 s34, s60, s33
	global_load_lds_dwordx4 v[218:219], off
	v_lshl_add_u64 v[218:219], s[30:31], 0, v[136:137]
	s_mov_b32 m0, s34
	s_nop 0
	global_load_lds_dwordx4 v[218:219], off
	v_lshl_add_u64 v[218:219], s[30:31], 0, v[140:141]
	s_add_i32 m0, s34, 0x2000
	s_nop 0
	global_load_lds_dwordx4 v[218:219], off
	v_lshl_add_u64 v[218:219], v[222:223], 0, s[0:1]
	s_mov_b32 m0, s48
	s_nop 0
	global_load_lds_dwordx4 v[218:219], off
	v_lshl_add_u64 v[218:219], v[224:225], 0, s[0:1]
	s_mov_b32 m0, s49
	s_nop 0
	global_load_lds_dwordx4 v[218:219], off
	s_waitcnt vmcnt(8)
	s_waitcnt lgkmcnt(0)
	s_barrier
	s_waitcnt lgkmcnt(0)
	v_mfma_f32_16x16x32_bf16 v[58:61], v[152:155], v[184:187], v[58:61]
	v_mfma_f32_16x16x32_bf16 v[78:81], v[160:163], v[184:187], v[78:81]
	v_mfma_f32_16x16x32_bf16 v[66:69], v[152:155], v[192:195], v[66:69]
	v_mfma_f32_16x16x32_bf16 v[82:85], v[160:163], v[192:195], v[82:85]
	v_mfma_f32_16x16x32_bf16 v[74:77], v[152:155], v[202:205], v[74:77]
	v_mfma_f32_16x16x32_bf16 v[98:101], v[160:163], v[202:205], v[98:101]
	v_mfma_f32_16x16x32_bf16 v[90:93], v[152:155], v[210:213], v[90:93]
	v_mfma_f32_16x16x32_bf16 v[94:97], v[160:163], v[210:213], v[94:97]
	v_mfma_f32_16x16x32_bf16 v[58:61], v[156:159], v[188:191], v[58:61]
	v_mfma_f32_16x16x32_bf16 v[78:81], v[164:167], v[188:191], v[78:81]
	v_mfma_f32_16x16x32_bf16 v[66:69], v[156:159], v[196:199], v[66:69]
	v_mfma_f32_16x16x32_bf16 v[82:85], v[164:167], v[196:199], v[82:85]
	v_mfma_f32_16x16x32_bf16 v[74:77], v[156:159], v[206:209], v[74:77]
	v_mfma_f32_16x16x32_bf16 v[98:101], v[164:167], v[206:209], v[98:101]
	v_mfma_f32_16x16x32_bf16 v[90:93], v[156:159], v[214:217], v[90:93]
	v_mfma_f32_16x16x32_bf16 v[94:97], v[164:167], v[214:217], v[94:97]
	v_mfma_f32_16x16x32_bf16 v[114:117], v[168:171], v[184:187], v[114:117]
	v_mfma_f32_16x16x32_bf16 v[130:133], v[176:179], v[184:187], v[130:133]
	v_mfma_f32_16x16x32_bf16 v[110:113], v[168:171], v[192:195], v[110:113]
	v_mfma_f32_16x16x32_bf16 v[126:129], v[176:179], v[192:195], v[126:129]
	v_mfma_f32_16x16x32_bf16 v[106:109], v[168:171], v[202:205], v[106:109]
	v_mfma_f32_16x16x32_bf16 v[122:125], v[176:179], v[202:205], v[122:125]
	v_mfma_f32_16x16x32_bf16 v[102:105], v[168:171], v[210:213], v[102:105]
	v_mfma_f32_16x16x32_bf16 v[118:121], v[176:179], v[210:213], v[118:121]
	v_mfma_f32_16x16x32_bf16 v[114:117], v[172:175], v[188:191], v[114:117]
	v_mfma_f32_16x16x32_bf16 v[130:133], v[180:183], v[188:191], v[130:133]
	v_mfma_f32_16x16x32_bf16 v[110:113], v[172:175], v[196:199], v[110:113]
	v_mfma_f32_16x16x32_bf16 v[126:129], v[180:183], v[196:199], v[126:129]
	v_mfma_f32_16x16x32_bf16 v[106:109], v[172:175], v[206:209], v[106:109]
	v_mfma_f32_16x16x32_bf16 v[122:125], v[180:183], v[206:209], v[122:125]
	v_mfma_f32_16x16x32_bf16 v[102:105], v[172:175], v[214:217], v[102:105]
	v_mfma_f32_16x16x32_bf16 v[118:121], v[180:183], v[214:217], v[118:121]
	s_barrier
	s_add_i32 s58, s58, 2
	s_cmpk_gt_u32 s58, 0x55
	s_mov_b64 s[34:35], s[28:29]
	s_cbranch_scc1 .Lpeel3_exit
.LBB0_1483:
	s_add_u32 s28, s34, 0x100
	s_addc_u32 s29, s35, 0
	s_add_u32 s30, s56, s34
	s_addc_u32 s31, s57, s35
	s_add_i32 s59, 0, 0x10000
	s_add_i32 s60, 0, 0x14000
	v_add_u32_e32 v2, s59, v149
	ds_read_b128 v[152:155], v2
	ds_read_b128 v[156:159], v2 offset:1024
	ds_read_b128 v[160:163], v2 offset:2048
	ds_read_b128 v[164:167], v2 offset:3072
	v_add_u32_e32 v2, s60, v149
	ds_read_b128 v[168:171], v2
	ds_read_b128 v[172:175], v2 offset:1024
	ds_read_b128 v[176:179], v2 offset:2048
	ds_read_b128 v[180:183], v2 offset:3072
	s_add_i32 s62, s59, s33
	s_add_i32 m0, s44, 0xc000
	s_add_i32 s61, s44, 0xe000
	s_add_i32 s59, s62, 0x2000
	s_cmpk_eq_i32 s58, 0x54
	s_cselect_b32 s31, s25, s31
	s_cselect_b32 s30, s24, s30
	v_lshl_add_u64 v[218:219], v[4:5], 0, s[34:35]
	ds_read_b128 v[184:187], v151
	ds_read_b128 v[188:191], v151 offset:1024
	ds_read_b128 v[192:195], v151 offset:2048
	ds_read_b128 v[196:199], v151 offset:3072
	ds_read_b128 v[202:205], v151 offset:4096
	ds_read_b128 v[206:209], v151 offset:5120
	ds_read_b128 v[210:213], v151 offset:6144
	ds_read_b128 v[214:217], v151 offset:7168
	global_load_lds_dwordx4 v[218:219], off
	v_lshl_add_u64 v[218:219], v[146:147], 0, s[34:35]
	s_mov_b32 m0, s61
	s_nop 0
	global_load_lds_dwordx4 v[218:219], off
	s_waitcnt vmcnt(8)
	s_waitcnt lgkmcnt(0)
	s_barrier
; #define PG8_STAGE_A(bufoff, base_, nx_, kb_, h_) do { if (GATHER) { if (nx_) PG8_STAGE_G(bufoff, kb_, goN, h_); else PG8_STAGE_G(bufoff, kb_, goC, h_); } \
;         else PG8_STAGE(bufoff, (base_) + (kb_) + (h_) * hstep, voffA); } while (0)
; #define PG8_STAGE(bufoff, gbase, voff) do { _Pragma("unroll") for (int _i = 0; _i < 2; ++_i) \
;         __builtin_amdgcn_global_load_lds((const unsigned*)((const char*)(gbase) + (voff)[_i]), (LAS unsigned*)(lds + (bufoff) + ldsw + _i * 8192), 16, 0, 0); } while (0)
; #define PG8_LDA(dst, b, h) do { _Pragma("unroll") for (int m = 0; m < 4; ++m) _Pragma("unroll") for (int k = 0; k < 2; ++k) dst[m][k] = *(const LAS bf16x8*)(lds + PG8_SA(b, h) + aoff + m * 2048 + k * 1024); } while (0)
; #define PG8_LDB(dst, b, h) do { _Pragma("unroll") for (int n = 0; n < 2; ++n) _Pragma("unroll") for (int k = 0; k < 2; ++k) dst[n][k] = *(const LAS bf16x8*)(lds + PG8_SB(b, h) + boff + n * 2048 + k * 1024); } while (0)
; #define PG8_MMA(ai, bj, At, Bt) do { __builtin_amdgcn_s_setprio(1); _Pragma("unroll") for (int m = 0; m < 4; ++m) _Pragma("unroll") for (int n = 0; n < 2; ++n) _Pragma("unroll") for (int k = 0; k < 2; ++k) \
;         acc[ai][bj][m][n] = __builtin_amdgcn_mfma_f32_16x16x32_bf16(Bt[n][k], At[m][k], acc[ai][bj][m][n], 0, 0, 0); __builtin_amdgcn_s_setprio(0); } while (0)
; #define PG8_WAIT_V(n) asm volatile("s_waitcnt vmcnt(" #n ")" ::: "memory")
; #define PG8_WAIT_L(n) asm volatile("s_waitcnt lgkmcnt(" #n ")" ::: "memory")
; #define PG8_BAR __builtin_amdgcn_s_barrier()
; #define PG8_SCHED __builtin_amdgcn_sched_barrier(0)
; template <class Epi, class Sched, bool GATHER = false>
; __device__ __forceinline__ void gemm_phase(LAS unsigned char* lds, const Gemm g, const Sched& S, const Epi& E, const int tid) {
;     ...
;             PG8_WAIT_V(8); PG8_WAIT_L(0); PG8_BAR; PG8_MMA(0, 0, At, B0); PG8_MMA(0, 1, At, B1); PG8_BAR; PG8_SCHED;
;             PG8_LDA(At, 0, 1); PG8_STAGE(PG8_SB(0, 0), b2, voffB); PG8_STAGE(PG8_SB(0, 1), b2 + hstep, voffB); PG8_STAGE_A(PG8_SA(0, 0), (last ? nA : cA), last, kb2, 0);
;             PG8_WAIT_V(8); PG8_WAIT_L(0); PG8_BAR; PG8_MMA(1, 0, At, B0); PG8_MMA(1, 1, At, B1); PG8_BAR; PG8_SCHED;
;             PG8_LDB(B0, 1, 0); PG8_LDB(B1, 1, 1); PG8_SCHED; PG8_LDA(At, 1, 0); PG8_STAGE_A(PG8_SA(0, 1), (last ? nA : cA), last, kb2, 1);
	s_waitcnt lgkmcnt(0)
	v_mfma_f32_16x16x32_bf16 v[86:89], v[152:155], v[184:187], v[86:89]
	v_mfma_f32_16x16x32_bf16 v[18:21], v[160:163], v[184:187], v[18:21]
	v_mfma_f32_16x16x32_bf16 v[6:9], v[152:155], v[192:195], v[6:9]
	v_mfma_f32_16x16x32_bf16 v[22:25], v[160:163], v[192:195], v[22:25]
	v_mfma_f32_16x16x32_bf16 v[10:13], v[152:155], v[202:205], v[10:13]
	v_mfma_f32_16x16x32_bf16 v[26:29], v[160:163], v[202:205], v[26:29]
	v_mfma_f32_16x16x32_bf16 v[14:17], v[152:155], v[210:213], v[14:17]
	v_mfma_f32_16x16x32_bf16 v[30:33], v[160:163], v[210:213], v[30:33]
	v_mfma_f32_16x16x32_bf16 v[86:89], v[156:159], v[188:191], v[86:89]
	v_mfma_f32_16x16x32_bf16 v[18:21], v[164:167], v[188:191], v[18:21]
	v_mfma_f32_16x16x32_bf16 v[6:9], v[156:159], v[196:199], v[6:9]
	v_mfma_f32_16x16x32_bf16 v[22:25], v[164:167], v[196:199], v[22:25]
	v_mfma_f32_16x16x32_bf16 v[10:13], v[156:159], v[206:209], v[10:13]
	v_mfma_f32_16x16x32_bf16 v[26:29], v[164:167], v[206:209], v[26:29]
	v_mfma_f32_16x16x32_bf16 v[14:17], v[156:159], v[214:217], v[14:17]
	v_mfma_f32_16x16x32_bf16 v[30:33], v[164:167], v[214:217], v[30:33]
	v_mfma_f32_16x16x32_bf16 v[34:37], v[168:171], v[184:187], v[34:37]
	v_mfma_f32_16x16x32_bf16 v[50:53], v[176:179], v[184:187], v[50:53]
	v_mfma_f32_16x16x32_bf16 v[38:41], v[168:171], v[192:195], v[38:41]
	v_mfma_f32_16x16x32_bf16 v[54:57], v[176:179], v[192:195], v[54:57]
	v_mfma_f32_16x16x32_bf16 v[42:45], v[168:171], v[202:205], v[42:45]
	v_mfma_f32_16x16x32_bf16 v[62:65], v[176:179], v[202:205], v[62:65]
	v_mfma_f32_16x16x32_bf16 v[46:49], v[168:171], v[210:213], v[46:49]
	v_mfma_f32_16x16x32_bf16 v[70:73], v[176:179], v[210:213], v[70:73]
	v_mfma_f32_16x16x32_bf16 v[34:37], v[172:175], v[188:191], v[34:37]
	v_mfma_f32_16x16x32_bf16 v[50:53], v[180:183], v[188:191], v[50:53]
	v_mfma_f32_16x16x32_bf16 v[38:41], v[172:175], v[196:199], v[38:41]
	v_mfma_f32_16x16x32_bf16 v[54:57], v[180:183], v[196:199], v[54:57]
	v_mfma_f32_16x16x32_bf16 v[42:45], v[172:175], v[206:209], v[42:45]
	v_mfma_f32_16x16x32_bf16 v[62:65], v[180:183], v[206:209], v[62:65]
	v_mfma_f32_16x16x32_bf16 v[46:49], v[172:175], v[214:217], v[46:49]
	v_mfma_f32_16x16x32_bf16 v[70:73], v[180:183], v[214:217], v[70:73]
	s_barrier
	s_mov_b32 m0, s62
	v_lshl_add_u64 v[218:219], s[30:31], 0, v[136:137]
	ds_read_b128 v[184:187], v151 offset:16384
	ds_read_b128 v[188:191], v151 offset:17408
	ds_read_b128 v[192:195], v151 offset:18432
	ds_read_b128 v[196:199], v151 offset:19456
	ds_read_b128 v[202:205], v151 offset:20480
	ds_read_b128 v[206:209], v151 offset:21504
	ds_read_b128 v[210:213], v151 offset:22528
	ds_read_b128 v[214:217], v151 offset:23552
	global_load_lds_dwordx4 v[218:219], off
	s_mov_b32 m0, s59
	s_cselect_b32 s59, 0, s29
	s_cselect_b32 s61, 0, s28
	s_cselect_b32 s62, s11, s15
	s_cselect_b32 s63, s10, s14
	s_add_u32 s34, s30, 0x160000
	v_lshl_add_u64 v[220:221], s[30:31], 0, v[140:141]
	s_addc_u32 s35, s31, 0
	s_add_i32 s60, s60, s33
	global_load_lds_dwordx4 v[220:221], off
	v_lshl_add_u64 v[222:223], s[34:35], 0, v[136:137]
	s_mov_b32 m0, s60
	s_nop 0
	global_load_lds_dwordx4 v[222:223], off
	s_add_i32 m0, s60, 0x2000
	v_lshl_add_u64 v[222:223], s[34:35], 0, v[140:141]
	s_add_u32 s34, s63, s61
	s_addc_u32 s35, s62, s59
	global_load_lds_dwordx4 v[222:223], off
	v_lshl_add_u64 v[222:223], s[34:35], 0, v[134:135]
	s_mov_b32 m0, s44
	v_lshl_add_u64 v[224:225], s[34:35], 0, v[138:139]
	global_load_lds_dwordx4 v[222:223], off
	s_mov_b32 m0, s45
	s_nop 0
	global_load_lds_dwordx4 v[224:225], off
	s_waitcnt vmcnt(8)
	s_waitcnt lgkmcnt(0)
	s_barrier
	s_waitcnt lgkmcnt(0)
	v_mfma_f32_16x16x32_bf16 v[58:61], v[152:155], v[184:187], v[58:61]
	v_mfma_f32_16x16x32_bf16 v[78:81], v[160:163], v[184:187], v[78:81]
	v_mfma_f32_16x16x32_bf16 v[66:69], v[152:155], v[192:195], v[66:69]
	v_mfma_f32_16x16x32_bf16 v[82:85], v[160:163], v[192:195], v[82:85]
	v_mfma_f32_16x16x32_bf16 v[74:77], v[152:155], v[202:205], v[74:77]
	v_mfma_f32_16x16x32_bf16 v[98:101], v[160:163], v[202:205], v[98:101]
	v_mfma_f32_16x16x32_bf16 v[90:93], v[152:155], v[210:213], v[90:93]
	v_mfma_f32_16x16x32_bf16 v[94:97], v[160:163], v[210:213], v[94:97]
	v_mfma_f32_16x16x32_bf16 v[58:61], v[156:159], v[188:191], v[58:61]
	v_mfma_f32_16x16x32_bf16 v[78:81], v[164:167], v[188:191], v[78:81]
	v_mfma_f32_16x16x32_bf16 v[66:69], v[156:159], v[196:199], v[66:69]
	v_mfma_f32_16x16x32_bf16 v[82:85], v[164:167], v[196:199], v[82:85]
	v_mfma_f32_16x16x32_bf16 v[74:77], v[156:159], v[206:209], v[74:77]
	v_mfma_f32_16x16x32_bf16 v[98:101], v[164:167], v[206:209], v[98:101]
	v_mfma_f32_16x16x32_bf16 v[90:93], v[156:159], v[214:217], v[90:93]
	v_mfma_f32_16x16x32_bf16 v[94:97], v[164:167], v[214:217], v[94:97]
	v_mfma_f32_16x16x32_bf16 v[114:117], v[168:171], v[184:187], v[114:117]
	v_mfma_f32_16x16x32_bf16 v[130:133], v[176:179], v[184:187], v[130:133]
	v_mfma_f32_16x16x32_bf16 v[110:113], v[168:171], v[192:195], v[110:113]
	v_mfma_f32_16x16x32_bf16 v[126:129], v[176:179], v[192:195], v[126:129]
	v_mfma_f32_16x16x32_bf16 v[106:109], v[168:171], v[202:205], v[106:109]
	v_mfma_f32_16x16x32_bf16 v[122:125], v[176:179], v[202:205], v[122:125]
	v_mfma_f32_16x16x32_bf16 v[102:105], v[168:171], v[210:213], v[102:105]
	v_mfma_f32_16x16x32_bf16 v[118:121], v[176:179], v[210:213], v[118:121]
	v_mfma_f32_16x16x32_bf16 v[114:117], v[172:175], v[188:191], v[114:117]
	v_mfma_f32_16x16x32_bf16 v[130:133], v[180:183], v[188:191], v[130:133]
	v_mfma_f32_16x16x32_bf16 v[110:113], v[172:175], v[196:199], v[110:113]
	v_mfma_f32_16x16x32_bf16 v[126:129], v[180:183], v[196:199], v[126:129]
	v_mfma_f32_16x16x32_bf16 v[106:109], v[172:175], v[206:209], v[106:109]
	v_mfma_f32_16x16x32_bf16 v[122:125], v[180:183], v[206:209], v[122:125]
	v_mfma_f32_16x16x32_bf16 v[102:105], v[172:175], v[214:217], v[102:105]
	v_mfma_f32_16x16x32_bf16 v[118:121], v[180:183], v[214:217], v[118:121]
	s_barrier
; #define PG8_STAGE_A(bufoff, base_, nx_, kb_, h_) do { if (GATHER) { if (nx_) PG8_STAGE_G(bufoff, kb_, goN, h_); else PG8_STAGE_G(bufoff, kb_, goC, h_); } \
;         else PG8_STAGE(bufoff, (base_) + (kb_) + (h_) * hstep, voffA); } while (0)
; #define PG8_STAGE(bufoff, gbase, voff) do { _Pragma("unroll") for (int _i = 0; _i < 2; ++_i) \
;         __builtin_amdgcn_global_load_lds((const unsigned*)((const char*)(gbase) + (voff)[_i]), (LAS unsigned*)(lds + (bufoff) + ldsw + _i * 8192), 16, 0, 0); } while (0)
; #define PG8_LDA(dst, b, h) do { _Pragma("unroll") for (int m = 0; m < 4; ++m) _Pragma("unroll") for (int k = 0; k < 2; ++k) dst[m][k] = *(const LAS bf16x8*)(lds + PG8_SA(b, h) + aoff + m * 2048 + k * 1024); } while (0)
; #define PG8_LDB(dst, b, h) do { _Pragma("unroll") for (int n = 0; n < 2; ++n) _Pragma("unroll") for (int k = 0; k < 2; ++k) dst[n][k] = *(const LAS bf16x8*)(lds + PG8_SB(b, h) + boff + n * 2048 + k * 1024); } while (0)
; #define PG8_MMA(ai, bj, At, Bt) do { __builtin_amdgcn_s_setprio(1); _Pragma("unroll") for (int m = 0; m < 4; ++m) _Pragma("unroll") for (int n = 0; n < 2; ++n) _Pragma("unroll") for (int k = 0; k < 2; ++k) \
;         acc[ai][bj][m][n] = __builtin_amdgcn_mfma_f32_16x16x32_bf16(Bt[n][k], At[m][k], acc[ai][bj][m][n], 0, 0, 0); __builtin_amdgcn_s_setprio(0); } while (0)
; #define PG8_WAIT_V(n) asm volatile("s_waitcnt vmcnt(" #n ")" ::: "memory")
; #define PG8_WAIT_L(n) asm volatile("s_waitcnt lgkmcnt(" #n ")" ::: "memory")
; #define PG8_BAR __builtin_amdgcn_s_barrier()
; #define PG8_SCHED __builtin_amdgcn_sched_barrier(0)
; template <class Epi, class Sched, bool GATHER = false>
; __device__ __forceinline__ void gemm_phase(LAS unsigned char* lds, const Gemm g, const Sched& S, const Epi& E, const int tid) {
;     ...
;             PG8_LDB(B0, 1, 0); PG8_LDB(B1, 1, 1); PG8_SCHED; PG8_LDA(At, 1, 0); PG8_STAGE_A(PG8_SA(0, 1), (last ? nA : cA), last, kb2, 1);
;             PG8_WAIT_V(8); PG8_WAIT_L(0); PG8_BAR; PG8_MMA(0, 0, At, B0); PG8_MMA(0, 1, At, B1); PG8_BAR; PG8_SCHED;
;             PG8_LDA(At, 1, 1); PG8_STAGE(PG8_SB(1, 0), b3, voffB); PG8_STAGE(PG8_SB(1, 1), b3 + hstep, voffB); PG8_STAGE_A(PG8_SA(1, 0), (last ? nA : cA), last, kb3, 0);
;             PG8_WAIT_V(8); PG8_WAIT_L(0); PG8_BAR; PG8_MMA(1, 0, At, B0); PG8_MMA(1, 1, At, B1); PG8_BAR; PG8_SCHED;
	s_add_i32 s59, 0, 0x18000
	v_add_u32_e32 v2, s59, v149
	s_add_i32 s60, 0, 0x1c000
	ds_read_b128 v[152:155], v2
	ds_read_b128 v[156:159], v2 offset:1024
	ds_read_b128 v[160:163], v2 offset:2048
	ds_read_b128 v[164:167], v2 offset:3072
	v_add_u32_e32 v2, s60, v149
	ds_read_b128 v[168:171], v2
	ds_read_b128 v[172:175], v2 offset:1024
	ds_read_b128 v[176:179], v2 offset:2048
	ds_read_b128 v[180:183], v2 offset:3072
	s_add_u32 s34, s34, 0x160000
	s_addc_u32 s35, s35, 0
	s_mov_b32 m0, s46
	v_lshl_add_u64 v[226:227], s[34:35], 0, v[134:135]
	ds_read_b128 v[184:187], v151 offset:32768
	ds_read_b128 v[188:191], v151 offset:33792
	ds_read_b128 v[192:195], v151 offset:34816
	ds_read_b128 v[196:199], v151 offset:35840
	ds_read_b128 v[202:205], v151 offset:36864
	ds_read_b128 v[206:209], v151 offset:37888
	ds_read_b128 v[210:213], v151 offset:38912
	ds_read_b128 v[214:217], v151 offset:39936
	global_load_lds_dwordx4 v[226:227], off
	v_lshl_add_u64 v[226:227], s[34:35], 0, v[138:139]
	s_mov_b32 m0, s47
	s_nop 0
	global_load_lds_dwordx4 v[226:227], off
	s_waitcnt vmcnt(8)
	s_waitcnt lgkmcnt(0)
	s_barrier
	s_waitcnt lgkmcnt(0)
	v_mfma_f32_16x16x32_bf16 v[86:89], v[152:155], v[184:187], v[86:89]
	v_mfma_f32_16x16x32_bf16 v[18:21], v[160:163], v[184:187], v[18:21]
	v_mfma_f32_16x16x32_bf16 v[6:9], v[152:155], v[192:195], v[6:9]
	v_mfma_f32_16x16x32_bf16 v[22:25], v[160:163], v[192:195], v[22:25]
	v_mfma_f32_16x16x32_bf16 v[10:13], v[152:155], v[202:205], v[10:13]
	v_mfma_f32_16x16x32_bf16 v[26:29], v[160:163], v[202:205], v[26:29]
	v_mfma_f32_16x16x32_bf16 v[14:17], v[152:155], v[210:213], v[14:17]
	v_mfma_f32_16x16x32_bf16 v[30:33], v[160:163], v[210:213], v[30:33]
	v_mfma_f32_16x16x32_bf16 v[86:89], v[156:159], v[188:191], v[86:89]
	v_mfma_f32_16x16x32_bf16 v[18:21], v[164:167], v[188:191], v[18:21]
	v_mfma_f32_16x16x32_bf16 v[6:9], v[156:159], v[196:199], v[6:9]
	v_mfma_f32_16x16x32_bf16 v[22:25], v[164:167], v[196:199], v[22:25]
	v_mfma_f32_16x16x32_bf16 v[10:13], v[156:159], v[206:209], v[10:13]
	v_mfma_f32_16x16x32_bf16 v[26:29], v[164:167], v[206:209], v[26:29]
	v_mfma_f32_16x16x32_bf16 v[14:17], v[156:159], v[214:217], v[14:17]
	v_mfma_f32_16x16x32_bf16 v[30:33], v[164:167], v[214:217], v[30:33]
	v_mfma_f32_16x16x32_bf16 v[34:37], v[168:171], v[184:187], v[34:37]
	v_mfma_f32_16x16x32_bf16 v[50:53], v[176:179], v[184:187], v[50:53]
	v_mfma_f32_16x16x32_bf16 v[38:41], v[168:171], v[192:195], v[38:41]
	v_mfma_f32_16x16x32_bf16 v[54:57], v[176:179], v[192:195], v[54:57]
	v_mfma_f32_16x16x32_bf16 v[42:45], v[168:171], v[202:205], v[42:45]
	v_mfma_f32_16x16x32_bf16 v[62:65], v[176:179], v[202:205], v[62:65]
	v_mfma_f32_16x16x32_bf16 v[46:49], v[168:171], v[210:213], v[46:49]
	v_mfma_f32_16x16x32_bf16 v[70:73], v[176:179], v[210:213], v[70:73]
	v_mfma_f32_16x16x32_bf16 v[34:37], v[172:175], v[188:191], v[34:37]
	v_mfma_f32_16x16x32_bf16 v[50:53], v[180:183], v[188:191], v[50:53]
	v_mfma_f32_16x16x32_bf16 v[38:41], v[172:175], v[196:199], v[38:41]
	v_mfma_f32_16x16x32_bf16 v[54:57], v[180:183], v[196:199], v[54:57]
	v_mfma_f32_16x16x32_bf16 v[42:45], v[172:175], v[206:209], v[42:45]
	v_mfma_f32_16x16x32_bf16 v[62:65], v[180:183], v[206:209], v[62:65]
	v_mfma_f32_16x16x32_bf16 v[46:49], v[172:175], v[214:217], v[46:49]
	v_mfma_f32_16x16x32_bf16 v[70:73], v[180:183], v[214:217], v[70:73]
	s_barrier
	s_add_i32 s34, s59, s33
	v_lshl_add_u64 v[218:219], v[218:219], 0, s[0:1]
	s_mov_b32 m0, s34
	ds_read_b128 v[184:187], v151 offset:49152
	ds_read_b128 v[188:191], v151 offset:50176
	ds_read_b128 v[192:195], v151 offset:51200
	ds_read_b128 v[196:199], v151 offset:52224
	ds_read_b128 v[202:205], v151 offset:53248
	ds_read_b128 v[206:209], v151 offset:54272
	ds_read_b128 v[210:213], v151 offset:55296
	ds_read_b128 v[214:217], v151 offset:56320
	global_load_lds_dwordx4 v[218:219], off
	s_add_i32 m0, s34, 0x2000
	s_add_u32 s30, s30, 0x160080
	v_lshl_add_u64 v[218:219], v[220:221], 0, s[0:1]
	s_addc_u32 s31, s31, 0
	s_add_i32 s34, s60, s33
	global_load_lds_dwordx4 v[218:219], off
	v_lshl_add_u64 v[218:219], s[30:31], 0, v[136:137]
	s_mov_b32 m0, s34
	s_nop 0
	global_load_lds_dwordx4 v[218:219], off
	v_lshl_add_u64 v[218:219], s[30:31], 0, v[140:141]
	s_add_i32 m0, s34, 0x2000
	s_nop 0
	global_load_lds_dwordx4 v[218:219], off
	v_lshl_add_u64 v[218:219], v[222:223], 0, s[0:1]
	s_mov_b32 m0, s48
	s_nop 0
	global_load_lds_dwordx4 v[218:219], off
	v_lshl_add_u64 v[218:219], v[224:225], 0, s[0:1]
	s_mov_b32 m0, s49
	s_nop 0
	global_load_lds_dwordx4 v[218:219], off
	s_waitcnt vmcnt(8)
	s_waitcnt lgkmcnt(0)
	s_barrier
	s_waitcnt lgkmcnt(0)
	v_mfma_f32_16x16x32_bf16 v[58:61], v[152:155], v[184:187], v[58:61]
	v_mfma_f32_16x16x32_bf16 v[78:81], v[160:163], v[184:187], v[78:81]
	v_mfma_f32_16x16x32_bf16 v[66:69], v[152:155], v[192:195], v[66:69]
	v_mfma_f32_16x16x32_bf16 v[82:85], v[160:163], v[192:195], v[82:85]
	v_mfma_f32_16x16x32_bf16 v[74:77], v[152:155], v[202:205], v[74:77]
	v_mfma_f32_16x16x32_bf16 v[98:101], v[160:163], v[202:205], v[98:101]
	v_mfma_f32_16x16x32_bf16 v[90:93], v[152:155], v[210:213], v[90:93]
	v_mfma_f32_16x16x32_bf16 v[94:97], v[160:163], v[210:213], v[94:97]
	v_mfma_f32_16x16x32_bf16 v[58:61], v[156:159], v[188:191], v[58:61]
	v_mfma_f32_16x16x32_bf16 v[78:81], v[164:167], v[188:191], v[78:81]
	v_mfma_f32_16x16x32_bf16 v[66:69], v[156:159], v[196:199], v[66:69]
	v_mfma_f32_16x16x32_bf16 v[82:85], v[164:167], v[196:199], v[82:85]
	v_mfma_f32_16x16x32_bf16 v[74:77], v[156:159], v[206:209], v[74:77]
	v_mfma_f32_16x16x32_bf16 v[98:101], v[164:167], v[206:209], v[98:101]
	v_mfma_f32_16x16x32_bf16 v[90:93], v[156:159], v[214:217], v[90:93]
	v_mfma_f32_16x16x32_bf16 v[94:97], v[164:167], v[214:217], v[94:97]
	v_mfma_f32_16x16x32_bf16 v[114:117], v[168:171], v[184:187], v[114:117]
	v_mfma_f32_16x16x32_bf16 v[130:133], v[176:179], v[184:187], v[130:133]
	v_mfma_f32_16x16x32_bf16 v[110:113], v[168:171], v[192:195], v[110:113]
	v_mfma_f32_16x16x32_bf16 v[126:129], v[176:179], v[192:195], v[126:129]
	v_mfma_f32_16x16x32_bf16 v[106:109], v[168:171], v[202:205], v[106:109]
	v_mfma_f32_16x16x32_bf16 v[122:125], v[176:179], v[202:205], v[122:125]
	v_mfma_f32_16x16x32_bf16 v[102:105], v[168:171], v[210:213], v[102:105]
	v_mfma_f32_16x16x32_bf16 v[118:121], v[176:179], v[210:213], v[118:121]
	v_mfma_f32_16x16x32_bf16 v[114:117], v[172:175], v[188:191], v[114:117]
	v_mfma_f32_16x16x32_bf16 v[130:133], v[180:183], v[188:191], v[130:133]
	v_mfma_f32_16x16x32_bf16 v[110:113], v[172:175], v[196:199], v[110:113]
	v_mfma_f32_16x16x32_bf16 v[126:129], v[180:183], v[196:199], v[126:129]
	v_mfma_f32_16x16x32_bf16 v[106:109], v[172:175], v[206:209], v[106:109]
	v_mfma_f32_16x16x32_bf16 v[122:125], v[180:183], v[206:209], v[122:125]
	v_mfma_f32_16x16x32_bf16 v[102:105], v[172:175], v[214:217], v[102:105]
	v_mfma_f32_16x16x32_bf16 v[118:121], v[180:183], v[214:217], v[118:121]
	s_barrier
	s_add_i32 s58, s58, 2
	s_cmpk_gt_u32 s58, 0x55
	s_mov_b64 s[34:35], s[28:29]
	s_cbranch_scc0 .LBB0_1483

; __device__ __forceinline__ unsigned cvt_pk_bf16(float lo, float hi) { const f32x2 v = {lo, hi}; const bf16x2_t b = __builtin_convertvector(v, bf16x2_t); return __builtin_bit_cast(unsigned, b); }
; #define ZERO4() ((f32x4){opaque0(), 0.f, 0.f, 0.f} * 0.f)
; #define PG8_BAR __builtin_amdgcn_s_barrier()
;     __device__ __forceinline__ void operator()(const f32x4 (&acc)[2][2][4][2], const Unit& u, int wr, int wc, int fr, int fq) const {
;         const int row0 = u.pm * BM + wr * 64 + fr, col0 = u.pn * BM + wc * 32 + 8 * fq;
; #pragma unroll
;         for (int ai = 0; ai < 2; ++ai)
; #pragma unroll
;             for (int m = 0; m < 4; ++m) { bf16_t* rowp = O + (size_t)(row0 + ai * HALF + m * 16) * ldc + col0;
; #pragma unroll
;                 for (int bj = 0; bj < 2; ++bj) { const f32x4 v0 = acc[ai][bj][m][0], v1 = acc[ai][bj][m][1];
;                     u32x4 w; w.x = cvt_pk_bf16(v0[0], v0[1]); w.y = cvt_pk_bf16(v0[2], v0[3]); w.z = cvt_pk_bf16(v1[0], v1[1]); w.w = cvt_pk_bf16(v1[2], v1[3]);
;                     *(u32x4*)(rowp + bj * HALF) = w; } }
;     }
; template <class Epi, class Sched, bool GATHER = false>
; __device__ __forceinline__ void gemm_phase(LAS unsigned char* lds, const Gemm g, const Sched& S, const Epi& E, const int tid) {
;     ...
;         if (!has_next) break;
; #pragma unroll
;         for (int a = 0; a < 2; ++a)
; #pragma unroll
;             for (int b = 0; b < 2; ++b)
; #pragma unroll
;                 for (int m = 0; m < 4; ++m)
; #pragma unroll
;                     for (int n = 0; n < 2; ++n) acc[a][b][m][n] = ZERO4();
;         cur = nxt; cA = nA; cB = nB; ++ui;
;         if (GATHER) {
; #pragma unroll
;             for (int h_ = 0; h_ < 2; ++h_) { goC[h_][0] = goN[h_][0]; goC[h_][1] = goN[h_][1]; } }
;         if (wr == 1) PG8_BAR;
.LBB0_1486:
	v_lshl_or_b32 v4, s51, 8, v150
	v_lshl_add_u32 v2, s50, 8, v148
	v_ashrrev_i32_e32 v5, 31, v4
	v_mov_b64_e32 v[146:147], s[12:13]
	s_movk_i32 s28, 0x1080
	v_mad_i64_i32 v[152:153], s[14:15], v2, s28, v[146:147]
	v_lshlrev_b64 v[154:155], 1, v[4:5]
	v_lshl_add_u64 v[4:5], v[152:153], 0, v[154:155]
	v_cvt_pk_bf16_f32 v86, v86, v87
	v_cvt_pk_bf16_f32 v87, v88, v89
	v_cvt_pk_bf16_f32 v88, v18, v19
	v_cvt_pk_bf16_f32 v89, v20, v21
	v_cvt_pk_bf16_f32 v18, v34, v35
	v_cvt_pk_bf16_f32 v19, v36, v37
	v_cvt_pk_bf16_f32 v20, v50, v51
	v_cvt_pk_bf16_f32 v21, v52, v53
	global_store_dwordx4 v[4:5], v[86:89], off
	global_store_dwordx4 v[4:5], v[18:21], off offset:256
	v_or_b32_e32 v4, 16, v2
	v_mad_i64_i32 v[4:5], s[14:15], v4, s28, v[146:147]
	v_lshl_add_u64 v[18:19], v[4:5], 0, v[154:155]
	v_cvt_pk_bf16_f32 v4, v6, v7
	v_cvt_pk_bf16_f32 v5, v8, v9
	v_cvt_pk_bf16_f32 v6, v22, v23
	v_cvt_pk_bf16_f32 v7, v24, v25
	global_store_dwordx4 v[18:19], v[4:7], off
	v_readlane_b32 s60, v254, 5
	s_and_b64 vcc, exec, s[8:9]
	v_cvt_pk_bf16_f32 v4, v38, v39
	v_cvt_pk_bf16_f32 v5, v40, v41
	v_cvt_pk_bf16_f32 v6, v54, v55
	v_cvt_pk_bf16_f32 v7, v56, v57
	global_store_dwordx4 v[18:19], v[4:7], off offset:256
	s_mov_b64 s[8:9], -1
	v_readlane_b32 s61, v254, 6
	v_or_b32_e32 v4, 32, v2
	v_mad_i64_i32 v[4:5], s[14:15], v4, s28, v[146:147]
	v_lshl_add_u64 v[8:9], v[4:5], 0, v[154:155]
	v_cvt_pk_bf16_f32 v4, v10, v11
	v_cvt_pk_bf16_f32 v5, v12, v13
	v_cvt_pk_bf16_f32 v6, v26, v27
	v_cvt_pk_bf16_f32 v7, v28, v29
	global_store_dwordx4 v[8:9], v[4:7], off
	s_nop 1
	v_cvt_pk_bf16_f32 v4, v42, v43
	v_cvt_pk_bf16_f32 v5, v44, v45
	v_cvt_pk_bf16_f32 v6, v62, v63
	v_cvt_pk_bf16_f32 v7, v64, v65
	global_store_dwordx4 v[8:9], v[4:7], off offset:256
	s_nop 1
	v_or_b32_e32 v4, 48, v2
	v_mad_i64_i32 v[4:5], s[14:15], v4, s28, v[146:147]
	v_lshl_add_u64 v[8:9], v[4:5], 0, v[154:155]
	v_cvt_pk_bf16_f32 v4, v14, v15
	v_cvt_pk_bf16_f32 v5, v16, v17
	v_cvt_pk_bf16_f32 v6, v30, v31
	v_cvt_pk_bf16_f32 v7, v32, v33
	global_store_dwordx4 v[8:9], v[4:7], off
	s_nop 1
	v_cvt_pk_bf16_f32 v4, v46, v47
	v_cvt_pk_bf16_f32 v5, v48, v49
	v_cvt_pk_bf16_f32 v6, v70, v71
	v_cvt_pk_bf16_f32 v7, v72, v73
	global_store_dwordx4 v[8:9], v[4:7], off offset:256
	s_nop 1
	v_add_u32_e32 v4, 0x80, v2
	v_mad_i64_i32 v[4:5], s[14:15], v4, s28, v[146:147]
	v_lshl_add_u64 v[8:9], v[4:5], 0, v[154:155]
	v_cvt_pk_bf16_f32 v4, v58, v59
	v_cvt_pk_bf16_f32 v5, v60, v61
	v_cvt_pk_bf16_f32 v6, v78, v79
	v_cvt_pk_bf16_f32 v7, v80, v81
	global_store_dwordx4 v[8:9], v[4:7], off
	s_nop 1
	v_cvt_pk_bf16_f32 v4, v114, v115
	v_cvt_pk_bf16_f32 v5, v116, v117
	v_cvt_pk_bf16_f32 v6, v130, v131
	v_cvt_pk_bf16_f32 v7, v132, v133
	global_store_dwordx4 v[8:9], v[4:7], off offset:256
	s_nop 1
	v_add_u32_e32 v4, 0x90, v2
	v_mad_i64_i32 v[4:5], s[14:15], v4, s28, v[146:147]
	v_lshl_add_u64 v[8:9], v[4:5], 0, v[154:155]
	v_cvt_pk_bf16_f32 v4, v66, v67
	v_cvt_pk_bf16_f32 v5, v68, v69
	v_cvt_pk_bf16_f32 v6, v82, v83
	v_cvt_pk_bf16_f32 v7, v84, v85
	global_store_dwordx4 v[8:9], v[4:7], off
	s_nop 1
	v_cvt_pk_bf16_f32 v4, v110, v111
	v_cvt_pk_bf16_f32 v5, v112, v113
	v_cvt_pk_bf16_f32 v6, v126, v127
	v_cvt_pk_bf16_f32 v7, v128, v129
	global_store_dwordx4 v[8:9], v[4:7], off offset:256
	s_nop 1
	v_add_u32_e32 v4, 0xa0, v2
	v_mad_i64_i32 v[4:5], s[14:15], v4, s28, v[146:147]
	v_lshl_add_u64 v[8:9], v[4:5], 0, v[154:155]
	v_cvt_pk_bf16_f32 v4, v74, v75
	v_cvt_pk_bf16_f32 v5, v76, v77
	v_cvt_pk_bf16_f32 v6, v98, v99
	v_cvt_pk_bf16_f32 v7, v100, v101
	global_store_dwordx4 v[8:9], v[4:7], off
	v_add_u32_e32 v2, 0xb0, v2
	s_nop 0
	v_cvt_pk_bf16_f32 v4, v106, v107
	v_cvt_pk_bf16_f32 v5, v108, v109
	v_cvt_pk_bf16_f32 v6, v122, v123
	v_cvt_pk_bf16_f32 v7, v124, v125
	global_store_dwordx4 v[8:9], v[4:7], off offset:256
	s_nop 1
	v_mad_i64_i32 v[4:5], s[14:15], v2, s28, v[146:147]
	v_lshl_add_u64 v[8:9], v[4:5], 0, v[154:155]
	v_cvt_pk_bf16_f32 v4, v90, v91
	v_cvt_pk_bf16_f32 v5, v92, v93
	v_cvt_pk_bf16_f32 v6, v94, v95
	v_cvt_pk_bf16_f32 v7, v96, v97
	global_store_dwordx4 v[8:9], v[4:7], off
	s_nop 1
	v_cvt_pk_bf16_f32 v4, v102, v103
	v_cvt_pk_bf16_f32 v5, v104, v105
	v_cvt_pk_bf16_f32 v6, v118, v119
	v_cvt_pk_bf16_f32 v7, v120, v121
	global_store_dwordx4 v[8:9], v[4:7], off offset:256
	s_cbranch_vccnz .LBB0_1471
	v_mov_b32_e32 v2, v3
	s_andn2_b64 vcc, exec, s[2:3]
	s_cbranch_vccnz .LBB0_1470
	s_barrier
	s_branch .LBB0_1470

; #define LAS __attribute__((address_space(3)))
;     __device__ __forceinline__ bool next(int i, Unit& u) const { if (i >= per * reps) return false; return StaticOrder::next(i % per, u); }
; #define PG8_STAGE_A(bufoff, base_, nx_, kb_, h_) do { if (GATHER) { if (nx_) PG8_STAGE_G(bufoff, kb_, goN, h_); else PG8_STAGE_G(bufoff, kb_, goC, h_); } \
;         else PG8_STAGE(bufoff, (base_) + (kb_) + (h_) * hstep, voffA); } while (0)
; #define PG8_STAGE(bufoff, gbase, voff) do { _Pragma("unroll") for (int _i = 0; _i < 2; ++_i) \
;         __builtin_amdgcn_global_load_lds((const unsigned*)((const char*)(gbase) + (voff)[_i]), (LAS unsigned*)(lds + (bufoff) + ldsw + _i * 8192), 16, 0, 0); } while (0)
; #define PG8_WAIT_V(n) asm volatile("s_waitcnt vmcnt(" #n ")" ::: "memory")
; #define PG8_WAIT_L(n) asm volatile("s_waitcnt lgkmcnt(" #n ")" ::: "memory")
; template <class Epi, class Sched, bool GATHER = false>
; __device__ __forceinline__ void gemm_phase(LAS unsigned char* lds, const Gemm g, const Sched& S, const Epi& E, const int tid) {
;     ...
;         const bool has_next = S.next(ui + 1, nxt);
;         const char* nA = has_next ? (const char*)g.A + (size_t)nxt.pm * tstep : cA; const char* nB = has_next ? (const char*)g.Bt + (size_t)nxt.pb * tstep : cB;
;         if (GATHER && has_next && wid < 4) __builtin_amdgcn_global_load_lds((const unsigned*)(g.rowmap + nxt.rb + tid), (LAS unsigned*)(lds + STAGE_BYTES + ((ui + 1) & 1) * 1024 + wid * 256), 4, 0, 0);
;         for (int t = 0; t < nt; t += 2) {
;             const bool last = (t == nt - 2);
;             const char* a1 = cA + (size_t)(t + 1) * kstep;
;             const char* a2 = last ? nA : cA + (size_t)(t + 2) * kstep; const char* b2 = last ? nB : cB + (size_t)(t + 2) * kstep;
;             const char* a3 = a2 + kstep; const char* b3 = b2 + kstep;
;     ...
;             PG8_LDB(B0, 0, 0); PG8_LDB(B1, 0, 1); PG8_SCHED; PG8_LDA(At, 0, 0); PG8_STAGE_A(PG8_SA(1, 1), cA, false, kb1, 1);
;             PG8_WAIT_V(8); PG8_WAIT_L(0); PG8_BAR; PG8_MMA(0, 0, At, B0); PG8_MMA(0, 1, At, B1); PG8_BAR; PG8_SCHED;
;             PG8_LDA(At, 0, 1); PG8_STAGE(PG8_SB(0, 0), b2, voffB); PG8_STAGE(PG8_SB(0, 1), b2 + hstep, voffB); PG8_STAGE_A(PG8_SA(0, 0), (last ? nA : cA), last, kb2, 0);
;             PG8_WAIT_V(8); PG8_WAIT_L(0); PG8_BAR; PG8_MMA(1, 0, At, B0); PG8_MMA(1, 1, At, B1); PG8_BAR; PG8_SCHED;
.LBB0_1504:
	s_mov_b64 s[30:31], 0x100
	v_lshl_add_u64 v[4:5], v[4:5], 0, s[30:31]
	s_add_u32 s30, s28, 0xb0080
	s_addc_u32 s31, s29, 0
	v_lshl_add_u64 v[148:149], s[30:31], 0, v[142:143]
	v_lshl_add_u64 v[150:151], s[30:31], 0, v[144:145]
	s_mov_b32 s63, -2
	s_mov_b64 s[34:35], 0
	s_mov_b64 s[76:77], 0xb0080
	s_add_u32 s30, s34, 0x100
	s_addc_u32 s31, s35, 0
	s_add_i32 s64, 0, 0x10000
	s_add_i32 s65, 0, 0x14000
	v_add_u32_e32 v2, s64, v153
	ds_read_b128 v[158:161], v2
	ds_read_b128 v[162:165], v2 offset:1024
	ds_read_b128 v[166:169], v2 offset:2048
	ds_read_b128 v[170:173], v2 offset:3072
	v_add_u32_e32 v2, s65, v153
	ds_read_b128 v[174:177], v2
	ds_read_b128 v[178:181], v2 offset:1024
	ds_read_b128 v[182:185], v2 offset:2048
	ds_read_b128 v[186:189], v2 offset:3072
	s_add_i32 s67, s64, s48
	s_add_i32 m0, s51, 0xc000
	s_add_i32 s66, s51, 0xe000
	s_add_i32 s68, s67, 0x2000
	s_cmp_eq_u32 s63, 40
	v_lshl_add_u64 v[190:191], v[4:5], 0, s[34:35]
	s_cselect_b64 vcc, -1, 0
	v_cndmask_b32_e32 v199, v191, v147, vcc
	v_cndmask_b32_e32 v198, v190, v146, vcc
	s_cselect_b32 s64, 0, s30
	v_lshl_add_u64 v[226:227], v[148:149], 0, s[34:35]
	ds_read_b128 v[190:193], v155
	ds_read_b128 v[194:197], v155 offset:1024
	ds_read_b128 v[202:205], v155 offset:2048
	ds_read_b128 v[206:209], v155 offset:3072
	ds_read_b128 v[210:213], v155 offset:4096
	ds_read_b128 v[214:217], v155 offset:5120
	ds_read_b128 v[218:221], v155 offset:6144
	ds_read_b128 v[222:225], v155 offset:7168
	global_load_lds_dwordx4 v[226:227], off
	v_lshl_add_u64 v[226:227], v[150:151], 0, s[34:35]
	s_mov_b32 m0, s66
	s_nop 0
	global_load_lds_dwordx4 v[226:227], off
	s_waitcnt vmcnt(8)
	s_waitcnt lgkmcnt(0)
	s_barrier
	s_waitcnt lgkmcnt(0)
	v_mfma_f32_16x16x32_bf16 v[90:93], v[158:161], v[190:193], 0
	v_mfma_f32_16x16x32_bf16 v[18:21], v[166:169], v[190:193], 0
	v_mfma_f32_16x16x32_bf16 v[6:9], v[158:161], v[202:205], 0
	v_mfma_f32_16x16x32_bf16 v[22:25], v[166:169], v[202:205], 0
	v_mfma_f32_16x16x32_bf16 v[10:13], v[158:161], v[210:213], 0
	v_mfma_f32_16x16x32_bf16 v[26:29], v[166:169], v[210:213], 0
	v_mfma_f32_16x16x32_bf16 v[14:17], v[158:161], v[218:221], 0
	v_mfma_f32_16x16x32_bf16 v[30:33], v[166:169], v[218:221], 0
	v_mfma_f32_16x16x32_bf16 v[90:93], v[162:165], v[194:197], v[90:93]
	v_mfma_f32_16x16x32_bf16 v[18:21], v[170:173], v[194:197], v[18:21]
	v_mfma_f32_16x16x32_bf16 v[6:9], v[162:165], v[206:209], v[6:9]
	v_mfma_f32_16x16x32_bf16 v[22:25], v[170:173], v[206:209], v[22:25]
	v_mfma_f32_16x16x32_bf16 v[10:13], v[162:165], v[214:217], v[10:13]
	v_mfma_f32_16x16x32_bf16 v[26:29], v[170:173], v[214:217], v[26:29]
	v_mfma_f32_16x16x32_bf16 v[14:17], v[162:165], v[222:225], v[14:17]
	v_mfma_f32_16x16x32_bf16 v[30:33], v[170:173], v[222:225], v[30:33]
	v_mfma_f32_16x16x32_bf16 v[34:37], v[174:177], v[190:193], 0
	v_mfma_f32_16x16x32_bf16 v[50:53], v[182:185], v[190:193], 0
	v_mfma_f32_16x16x32_bf16 v[38:41], v[174:177], v[202:205], 0
	v_mfma_f32_16x16x32_bf16 v[54:57], v[182:185], v[202:205], 0
	v_mfma_f32_16x16x32_bf16 v[42:45], v[174:177], v[210:213], 0
	v_mfma_f32_16x16x32_bf16 v[62:65], v[182:185], v[210:213], 0
	v_mfma_f32_16x16x32_bf16 v[46:49], v[174:177], v[218:221], 0
	v_mfma_f32_16x16x32_bf16 v[70:73], v[182:185], v[218:221], 0
	v_mfma_f32_16x16x32_bf16 v[34:37], v[178:181], v[194:197], v[34:37]
	v_mfma_f32_16x16x32_bf16 v[50:53], v[186:189], v[194:197], v[50:53]
	v_mfma_f32_16x16x32_bf16 v[38:41], v[178:181], v[206:209], v[38:41]
	v_mfma_f32_16x16x32_bf16 v[54:57], v[186:189], v[206:209], v[54:57]
	v_mfma_f32_16x16x32_bf16 v[42:45], v[178:181], v[214:217], v[42:45]
	v_mfma_f32_16x16x32_bf16 v[62:65], v[186:189], v[214:217], v[62:65]
	v_mfma_f32_16x16x32_bf16 v[46:49], v[178:181], v[222:225], v[46:49]
	v_mfma_f32_16x16x32_bf16 v[70:73], v[186:189], v[222:225], v[70:73]
	s_barrier
	s_mov_b32 m0, s67
	v_lshl_add_u64 v[226:227], v[198:199], 0, v[138:139]
	ds_read_b128 v[190:193], v155 offset:16384
	ds_read_b128 v[194:197], v155 offset:17408
	ds_read_b128 v[202:205], v155 offset:18432
	ds_read_b128 v[206:209], v155 offset:19456
	ds_read_b128 v[210:213], v155 offset:20480
	ds_read_b128 v[214:217], v155 offset:21504
	ds_read_b128 v[218:221], v155 offset:22528
	ds_read_b128 v[222:225], v155 offset:23552
	global_load_lds_dwordx4 v[226:227], off
	v_lshl_add_u64 v[228:229], v[198:199], 0, v[134:135]
	s_mov_b32 m0, s68
	s_cselect_b32 s35, s11, s29
	s_cselect_b32 s34, s10, s28
	v_lshl_add_u64 v[230:231], v[198:199], 0, s[72:73]
	s_add_i32 s65, s65, s48
	global_load_lds_dwordx4 v[228:229], off
	v_lshl_add_u64 v[232:233], v[230:231], 0, v[138:139]
	s_mov_b32 m0, s65
	v_lshl_add_u64 v[230:231], v[230:231], 0, v[134:135]
	global_load_lds_dwordx4 v[232:233], off
	s_add_i32 m0, s65, 0x2000
	s_add_u32 s34, s34, s64
	s_addc_u32 s35, s35, 0
	global_load_lds_dwordx4 v[230:231], off
	v_lshl_add_u64 v[230:231], s[34:35], 0, v[140:141]
	s_mov_b32 m0, s51
	v_lshl_add_u64 v[232:233], s[34:35], 0, v[136:137]
	global_load_lds_dwordx4 v[230:231], off
	s_mov_b32 m0, s52
	s_nop 0
	global_load_lds_dwordx4 v[232:233], off
	s_waitcnt vmcnt(8)
	s_waitcnt lgkmcnt(0)
	s_barrier
; #define PG8_STAGE_A(bufoff, base_, nx_, kb_, h_) do { if (GATHER) { if (nx_) PG8_STAGE_G(bufoff, kb_, goN, h_); else PG8_STAGE_G(bufoff, kb_, goC, h_); } \
;         else PG8_STAGE(bufoff, (base_) + (kb_) + (h_) * hstep, voffA); } while (0)
; #define PG8_LDA(dst, b, h) do { _Pragma("unroll") for (int m = 0; m < 4; ++m) _Pragma("unroll") for (int k = 0; k < 2; ++k) dst[m][k] = *(const LAS bf16x8*)(lds + PG8_SA(b, h) + aoff + m * 2048 + k * 1024); } while (0)
; #define PG8_LDB(dst, b, h) do { _Pragma("unroll") for (int n = 0; n < 2; ++n) _Pragma("unroll") for (int k = 0; k < 2; ++k) dst[n][k] = *(const LAS bf16x8*)(lds + PG8_SB(b, h) + boff + n * 2048 + k * 1024); } while (0)
; #define PG8_MMA(ai, bj, At, Bt) do { __builtin_amdgcn_s_setprio(1); _Pragma("unroll") for (int m = 0; m < 4; ++m) _Pragma("unroll") for (int n = 0; n < 2; ++n) _Pragma("unroll") for (int k = 0; k < 2; ++k) \
;         acc[ai][bj][m][n] = __builtin_amdgcn_mfma_f32_16x16x32_bf16(Bt[n][k], At[m][k], acc[ai][bj][m][n], 0, 0, 0); __builtin_amdgcn_s_setprio(0); } while (0)
; #define PG8_WAIT_V(n) asm volatile("s_waitcnt vmcnt(" #n ")" ::: "memory")
; #define PG8_WAIT_L(n) asm volatile("s_waitcnt lgkmcnt(" #n ")" ::: "memory")
; #define PG8_BAR __builtin_amdgcn_s_barrier()
; #define PG8_SCHED __builtin_amdgcn_sched_barrier(0)
; template <class Epi, class Sched, bool GATHER = false>
; __device__ __forceinline__ void gemm_phase(LAS unsigned char* lds, const Gemm g, const Sched& S, const Epi& E, const int tid) {
;     ...
;             PG8_WAIT_V(8); PG8_WAIT_L(0); PG8_BAR; PG8_MMA(1, 0, At, B0); PG8_MMA(1, 1, At, B1); PG8_BAR; PG8_SCHED;
;             PG8_LDB(B0, 1, 0); PG8_LDB(B1, 1, 1); PG8_SCHED; PG8_LDA(At, 1, 0); PG8_STAGE_A(PG8_SA(0, 1), (last ? nA : cA), last, kb2, 1);
;             PG8_WAIT_V(8); PG8_WAIT_L(0); PG8_BAR; PG8_MMA(0, 0, At, B0); PG8_MMA(0, 1, At, B1); PG8_BAR; PG8_SCHED;
	s_waitcnt lgkmcnt(0)
	v_mfma_f32_16x16x32_bf16 v[58:61], v[158:161], v[190:193], 0
	v_mfma_f32_16x16x32_bf16 v[78:81], v[166:169], v[190:193], 0
	v_mfma_f32_16x16x32_bf16 v[66:69], v[158:161], v[202:205], 0
	v_mfma_f32_16x16x32_bf16 v[82:85], v[166:169], v[202:205], 0
	v_mfma_f32_16x16x32_bf16 v[74:77], v[158:161], v[210:213], 0
	v_mfma_f32_16x16x32_bf16 v[86:89], v[166:169], v[210:213], 0
	v_mfma_f32_16x16x32_bf16 v[94:97], v[158:161], v[218:221], 0
	v_mfma_f32_16x16x32_bf16 v[98:101], v[166:169], v[218:221], 0
	v_mfma_f32_16x16x32_bf16 v[58:61], v[162:165], v[194:197], v[58:61]
	v_mfma_f32_16x16x32_bf16 v[78:81], v[170:173], v[194:197], v[78:81]
	v_mfma_f32_16x16x32_bf16 v[66:69], v[162:165], v[206:209], v[66:69]
	v_mfma_f32_16x16x32_bf16 v[82:85], v[170:173], v[206:209], v[82:85]
	v_mfma_f32_16x16x32_bf16 v[74:77], v[162:165], v[214:217], v[74:77]
	v_mfma_f32_16x16x32_bf16 v[86:89], v[170:173], v[214:217], v[86:89]
	v_mfma_f32_16x16x32_bf16 v[94:97], v[162:165], v[222:225], v[94:97]
	v_mfma_f32_16x16x32_bf16 v[98:101], v[170:173], v[222:225], v[98:101]
	v_mfma_f32_16x16x32_bf16 v[114:117], v[174:177], v[190:193], 0
	v_mfma_f32_16x16x32_bf16 v[130:133], v[182:185], v[190:193], 0
	v_mfma_f32_16x16x32_bf16 v[110:113], v[174:177], v[202:205], 0
	v_mfma_f32_16x16x32_bf16 v[126:129], v[182:185], v[202:205], 0
	v_mfma_f32_16x16x32_bf16 v[106:109], v[174:177], v[210:213], 0
	v_mfma_f32_16x16x32_bf16 v[122:125], v[182:185], v[210:213], 0
	v_mfma_f32_16x16x32_bf16 v[102:105], v[174:177], v[218:221], 0
	v_mfma_f32_16x16x32_bf16 v[118:121], v[182:185], v[218:221], 0
	v_mfma_f32_16x16x32_bf16 v[114:117], v[178:181], v[194:197], v[114:117]
	v_mfma_f32_16x16x32_bf16 v[130:133], v[186:189], v[194:197], v[130:133]
	v_mfma_f32_16x16x32_bf16 v[110:113], v[178:181], v[206:209], v[110:113]
	v_mfma_f32_16x16x32_bf16 v[126:129], v[186:189], v[206:209], v[126:129]
	v_mfma_f32_16x16x32_bf16 v[106:109], v[178:181], v[214:217], v[106:109]
	v_mfma_f32_16x16x32_bf16 v[122:125], v[186:189], v[214:217], v[122:125]
	v_mfma_f32_16x16x32_bf16 v[102:105], v[178:181], v[222:225], v[102:105]
	v_mfma_f32_16x16x32_bf16 v[118:121], v[186:189], v[222:225], v[118:121]
	s_barrier
	s_add_i32 s64, 0, 0x18000
	v_add_u32_e32 v2, s64, v153
	s_add_i32 s65, 0, 0x1c000
	ds_read_b128 v[158:161], v2
	ds_read_b128 v[162:165], v2 offset:1024
	ds_read_b128 v[166:169], v2 offset:2048
	ds_read_b128 v[170:173], v2 offset:3072
	v_add_u32_e32 v2, s65, v153
	ds_read_b128 v[174:177], v2
	ds_read_b128 v[178:181], v2 offset:1024
	ds_read_b128 v[182:185], v2 offset:2048
	ds_read_b128 v[186:189], v2 offset:3072
	s_add_u32 s34, s34, 0xb0000
	s_addc_u32 s35, s35, 0
	s_mov_b32 m0, s53
	v_lshl_add_u64 v[234:235], s[34:35], 0, v[140:141]
	ds_read_b128 v[190:193], v155 offset:32768
	ds_read_b128 v[194:197], v155 offset:33792
	ds_read_b128 v[202:205], v155 offset:34816
	ds_read_b128 v[206:209], v155 offset:35840
	ds_read_b128 v[210:213], v155 offset:36864
	ds_read_b128 v[214:217], v155 offset:37888
	ds_read_b128 v[218:221], v155 offset:38912
	ds_read_b128 v[222:225], v155 offset:39936
	global_load_lds_dwordx4 v[234:235], off
	v_lshl_add_u64 v[234:235], s[34:35], 0, v[136:137]
	s_mov_b32 m0, s54
	s_nop 0
	global_load_lds_dwordx4 v[234:235], off
	s_waitcnt vmcnt(8)
	s_waitcnt lgkmcnt(0)
	s_barrier
	s_waitcnt lgkmcnt(0)
	v_mfma_f32_16x16x32_bf16 v[90:93], v[158:161], v[190:193], v[90:93]
	v_mfma_f32_16x16x32_bf16 v[18:21], v[166:169], v[190:193], v[18:21]
	v_mfma_f32_16x16x32_bf16 v[6:9], v[158:161], v[202:205], v[6:9]
	v_mfma_f32_16x16x32_bf16 v[22:25], v[166:169], v[202:205], v[22:25]
	v_mfma_f32_16x16x32_bf16 v[10:13], v[158:161], v[210:213], v[10:13]
	v_mfma_f32_16x16x32_bf16 v[26:29], v[166:169], v[210:213], v[26:29]
	v_mfma_f32_16x16x32_bf16 v[14:17], v[158:161], v[218:221], v[14:17]
	v_mfma_f32_16x16x32_bf16 v[30:33], v[166:169], v[218:221], v[30:33]
	v_mfma_f32_16x16x32_bf16 v[90:93], v[162:165], v[194:197], v[90:93]
	v_mfma_f32_16x16x32_bf16 v[18:21], v[170:173], v[194:197], v[18:21]
	v_mfma_f32_16x16x32_bf16 v[6:9], v[162:165], v[206:209], v[6:9]
	v_mfma_f32_16x16x32_bf16 v[22:25], v[170:173], v[206:209], v[22:25]
	v_mfma_f32_16x16x32_bf16 v[10:13], v[162:165], v[214:217], v[10:13]
	v_mfma_f32_16x16x32_bf16 v[26:29], v[170:173], v[214:217], v[26:29]
	v_mfma_f32_16x16x32_bf16 v[14:17], v[162:165], v[222:225], v[14:17]
	v_mfma_f32_16x16x32_bf16 v[30:33], v[170:173], v[222:225], v[30:33]
	v_mfma_f32_16x16x32_bf16 v[34:37], v[174:177], v[190:193], v[34:37]
	v_mfma_f32_16x16x32_bf16 v[50:53], v[182:185], v[190:193], v[50:53]
	v_mfma_f32_16x16x32_bf16 v[38:41], v[174:177], v[202:205], v[38:41]
	v_mfma_f32_16x16x32_bf16 v[54:57], v[182:185], v[202:205], v[54:57]
	v_mfma_f32_16x16x32_bf16 v[42:45], v[174:177], v[210:213], v[42:45]
	v_mfma_f32_16x16x32_bf16 v[62:65], v[182:185], v[210:213], v[62:65]
	v_mfma_f32_16x16x32_bf16 v[46:49], v[174:177], v[218:221], v[46:49]
	v_mfma_f32_16x16x32_bf16 v[70:73], v[182:185], v[218:221], v[70:73]
	v_mfma_f32_16x16x32_bf16 v[34:37], v[178:181], v[194:197], v[34:37]
	v_mfma_f32_16x16x32_bf16 v[50:53], v[186:189], v[194:197], v[50:53]
	v_mfma_f32_16x16x32_bf16 v[38:41], v[178:181], v[206:209], v[38:41]
	v_mfma_f32_16x16x32_bf16 v[54:57], v[186:189], v[206:209], v[54:57]
	v_mfma_f32_16x16x32_bf16 v[42:45], v[178:181], v[214:217], v[42:45]
	v_mfma_f32_16x16x32_bf16 v[62:65], v[186:189], v[214:217], v[62:65]
	v_mfma_f32_16x16x32_bf16 v[46:49], v[178:181], v[222:225], v[46:49]
	v_mfma_f32_16x16x32_bf16 v[70:73], v[186:189], v[222:225], v[70:73]
	s_barrier
; #define PG8_STAGE_A(bufoff, base_, nx_, kb_, h_) do { if (GATHER) { if (nx_) PG8_STAGE_G(bufoff, kb_, goN, h_); else PG8_STAGE_G(bufoff, kb_, goC, h_); } \
;         else PG8_STAGE(bufoff, (base_) + (kb_) + (h_) * hstep, voffA); } while (0)
; #define PG8_STAGE(bufoff, gbase, voff) do { _Pragma("unroll") for (int _i = 0; _i < 2; ++_i) \
;         __builtin_amdgcn_global_load_lds((const unsigned*)((const char*)(gbase) + (voff)[_i]), (LAS unsigned*)(lds + (bufoff) + ldsw + _i * 8192), 16, 0, 0); } while (0)
; #define PG8_LDA(dst, b, h) do { _Pragma("unroll") for (int m = 0; m < 4; ++m) _Pragma("unroll") for (int k = 0; k < 2; ++k) dst[m][k] = *(const LAS bf16x8*)(lds + PG8_SA(b, h) + aoff + m * 2048 + k * 1024); } while (0)
; #define PG8_LDB(dst, b, h) do { _Pragma("unroll") for (int n = 0; n < 2; ++n) _Pragma("unroll") for (int k = 0; k < 2; ++k) dst[n][k] = *(const LAS bf16x8*)(lds + PG8_SB(b, h) + boff + n * 2048 + k * 1024); } while (0)
; #define PG8_WAIT_V(n) asm volatile("s_waitcnt vmcnt(" #n ")" ::: "memory")
; #define PG8_WAIT_L(n) asm volatile("s_waitcnt lgkmcnt(" #n ")" ::: "memory")
; template <class Epi, class Sched, bool GATHER = false>
; __device__ __forceinline__ void gemm_phase(LAS unsigned char* lds, const Gemm g, const Sched& S, const Epi& E, const int tid) {
;     ...
;             PG8_LDB(B0, 0, 0); PG8_LDB(B1, 0, 1); PG8_SCHED; PG8_LDA(At, 0, 0); PG8_STAGE_A(PG8_SA(1, 1), cA, false, kb1, 1);
;             PG8_WAIT_V(8); PG8_WAIT_L(0); PG8_BAR; PG8_MMA(0, 0, At, B0); PG8_MMA(0, 1, At, B1); PG8_BAR; PG8_SCHED;
;             PG8_LDA(At, 0, 1); PG8_STAGE(PG8_SB(0, 0), b2, voffB); PG8_STAGE(PG8_SB(0, 1), b2 + hstep, voffB); PG8_STAGE_A(PG8_SA(0, 0), (last ? nA : cA), last, kb2, 0);
;             PG8_WAIT_V(8); PG8_WAIT_L(0); PG8_BAR; PG8_MMA(1, 0, At, B0); PG8_MMA(1, 1, At, B1); PG8_BAR; PG8_SCHED;
;             PG8_LDB(B0, 1, 0); PG8_LDB(B1, 1, 1); PG8_SCHED; PG8_LDA(At, 1, 0); PG8_STAGE_A(PG8_SA(0, 1), (last ? nA : cA), last, kb2, 1);
;             PG8_WAIT_V(8); PG8_WAIT_L(0); PG8_BAR; PG8_MMA(0, 0, At, B0); PG8_MMA(0, 1, At, B1); PG8_BAR; PG8_SCHED;
;             PG8_LDA(At, 1, 1); PG8_STAGE(PG8_SB(1, 0), b3, voffB); PG8_STAGE(PG8_SB(1, 1), b3 + hstep, voffB); PG8_STAGE_A(PG8_SA(1, 0), (last ? nA : cA), last, kb3, 0);
;             PG8_WAIT_V(8); PG8_WAIT_L(0); PG8_BAR; PG8_MMA(1, 0, At, B0); PG8_MMA(1, 1, At, B1); PG8_BAR; PG8_SCHED;
	s_add_i32 s34, s64, s48
	v_lshl_add_u64 v[226:227], v[226:227], 0, s[0:1]
	s_mov_b32 m0, s34
	ds_read_b128 v[190:193], v155 offset:49152
	ds_read_b128 v[194:197], v155 offset:50176
	ds_read_b128 v[202:205], v155 offset:51200
	ds_read_b128 v[206:209], v155 offset:52224
	ds_read_b128 v[210:213], v155 offset:53248
	ds_read_b128 v[214:217], v155 offset:54272
	ds_read_b128 v[218:221], v155 offset:55296
	ds_read_b128 v[222:225], v155 offset:56320
	global_load_lds_dwordx4 v[226:227], off
	v_lshl_add_u64 v[226:227], v[228:229], 0, s[0:1]
	s_add_i32 m0, s34, 0x2000
	v_lshl_add_u64 v[198:199], v[198:199], 0, s[76:77]
	s_add_i32 s34, s65, s48
	global_load_lds_dwordx4 v[226:227], off
	v_lshl_add_u64 v[226:227], v[198:199], 0, v[138:139]
	s_mov_b32 m0, s34
	v_lshl_add_u64 v[198:199], v[198:199], 0, v[134:135]
	global_load_lds_dwordx4 v[226:227], off
	s_add_i32 m0, s34, 0x2000
	s_nop 0
	global_load_lds_dwordx4 v[198:199], off
	v_lshl_add_u64 v[198:199], v[230:231], 0, s[0:1]
	s_mov_b32 m0, s55
	s_nop 0
	global_load_lds_dwordx4 v[198:199], off
	v_lshl_add_u64 v[198:199], v[232:233], 0, s[0:1]
	s_mov_b32 m0, s56
	s_nop 0
	global_load_lds_dwordx4 v[198:199], off
	s_waitcnt vmcnt(8)
	s_waitcnt lgkmcnt(0)
	s_barrier
	s_waitcnt lgkmcnt(0)
	v_mfma_f32_16x16x32_bf16 v[58:61], v[158:161], v[190:193], v[58:61]
	v_mfma_f32_16x16x32_bf16 v[78:81], v[166:169], v[190:193], v[78:81]
	v_mfma_f32_16x16x32_bf16 v[66:69], v[158:161], v[202:205], v[66:69]
	v_mfma_f32_16x16x32_bf16 v[82:85], v[166:169], v[202:205], v[82:85]
	v_mfma_f32_16x16x32_bf16 v[74:77], v[158:161], v[210:213], v[74:77]
	v_mfma_f32_16x16x32_bf16 v[86:89], v[166:169], v[210:213], v[86:89]
	v_mfma_f32_16x16x32_bf16 v[94:97], v[158:161], v[218:221], v[94:97]
	v_mfma_f32_16x16x32_bf16 v[98:101], v[166:169], v[218:221], v[98:101]
	v_mfma_f32_16x16x32_bf16 v[58:61], v[162:165], v[194:197], v[58:61]
	v_mfma_f32_16x16x32_bf16 v[78:81], v[170:173], v[194:197], v[78:81]
	v_mfma_f32_16x16x32_bf16 v[66:69], v[162:165], v[206:209], v[66:69]
	v_mfma_f32_16x16x32_bf16 v[82:85], v[170:173], v[206:209], v[82:85]
	v_mfma_f32_16x16x32_bf16 v[74:77], v[162:165], v[214:217], v[74:77]
	v_mfma_f32_16x16x32_bf16 v[86:89], v[170:173], v[214:217], v[86:89]
	v_mfma_f32_16x16x32_bf16 v[94:97], v[162:165], v[222:225], v[94:97]
	v_mfma_f32_16x16x32_bf16 v[98:101], v[170:173], v[222:225], v[98:101]
	v_mfma_f32_16x16x32_bf16 v[114:117], v[174:177], v[190:193], v[114:117]
	v_mfma_f32_16x16x32_bf16 v[130:133], v[182:185], v[190:193], v[130:133]
	v_mfma_f32_16x16x32_bf16 v[110:113], v[174:177], v[202:205], v[110:113]
	v_mfma_f32_16x16x32_bf16 v[126:129], v[182:185], v[202:205], v[126:129]
	v_mfma_f32_16x16x32_bf16 v[106:109], v[174:177], v[210:213], v[106:109]
	v_mfma_f32_16x16x32_bf16 v[122:125], v[182:185], v[210:213], v[122:125]
	v_mfma_f32_16x16x32_bf16 v[102:105], v[174:177], v[218:221], v[102:105]
	v_mfma_f32_16x16x32_bf16 v[118:121], v[182:185], v[218:221], v[118:121]
	v_mfma_f32_16x16x32_bf16 v[114:117], v[178:181], v[194:197], v[114:117]
	v_mfma_f32_16x16x32_bf16 v[130:133], v[186:189], v[194:197], v[130:133]
	v_mfma_f32_16x16x32_bf16 v[110:113], v[178:181], v[206:209], v[110:113]
	v_mfma_f32_16x16x32_bf16 v[126:129], v[186:189], v[206:209], v[126:129]
	v_mfma_f32_16x16x32_bf16 v[106:109], v[178:181], v[214:217], v[106:109]
	v_mfma_f32_16x16x32_bf16 v[122:125], v[186:189], v[214:217], v[122:125]
	v_mfma_f32_16x16x32_bf16 v[102:105], v[178:181], v[222:225], v[102:105]
	v_mfma_f32_16x16x32_bf16 v[118:121], v[186:189], v[222:225], v[118:121]
	s_barrier
	s_add_i32 s63, s63, 2
	s_cmp_gt_u32 s63, 41
	s_mov_b64 s[34:35], s[30:31]
	s_cbranch_scc1 .Lpeel4_exit
.LBB0_1505:
	s_add_u32 s30, s34, 0x100
	s_addc_u32 s31, s35, 0
	s_add_i32 s64, 0, 0x10000
	s_add_i32 s65, 0, 0x14000
	v_add_u32_e32 v2, s64, v153
	ds_read_b128 v[158:161], v2
	ds_read_b128 v[162:165], v2 offset:1024
	ds_read_b128 v[166:169], v2 offset:2048
	ds_read_b128 v[170:173], v2 offset:3072
	v_add_u32_e32 v2, s65, v153
	ds_read_b128 v[174:177], v2
	ds_read_b128 v[178:181], v2 offset:1024
	ds_read_b128 v[182:185], v2 offset:2048
	ds_read_b128 v[186:189], v2 offset:3072
	s_add_i32 s67, s64, s48
	s_add_i32 m0, s51, 0xc000
	s_add_i32 s66, s51, 0xe000
	s_add_i32 s68, s67, 0x2000
	s_cmp_eq_u32 s63, 40
	v_lshl_add_u64 v[190:191], v[4:5], 0, s[34:35]
	s_cselect_b64 vcc, -1, 0
	v_cndmask_b32_e32 v199, v191, v147, vcc
	v_cndmask_b32_e32 v198, v190, v146, vcc
	s_cselect_b32 s64, 0, s30
	v_lshl_add_u64 v[226:227], v[148:149], 0, s[34:35]
	ds_read_b128 v[190:193], v155
	ds_read_b128 v[194:197], v155 offset:1024
	ds_read_b128 v[202:205], v155 offset:2048
	ds_read_b128 v[206:209], v155 offset:3072
	ds_read_b128 v[210:213], v155 offset:4096
	ds_read_b128 v[214:217], v155 offset:5120
	ds_read_b128 v[218:221], v155 offset:6144
	ds_read_b128 v[222:225], v155 offset:7168
	global_load_lds_dwordx4 v[226:227], off
	v_lshl_add_u64 v[226:227], v[150:151], 0, s[34:35]
	s_mov_b32 m0, s66
	s_nop 0
	global_load_lds_dwordx4 v[226:227], off
	s_waitcnt vmcnt(8)
	s_waitcnt lgkmcnt(0)
	s_barrier
; #define PG8_STAGE_A(bufoff, base_, nx_, kb_, h_) do { if (GATHER) { if (nx_) PG8_STAGE_G(bufoff, kb_, goN, h_); else PG8_STAGE_G(bufoff, kb_, goC, h_); } \
;         else PG8_STAGE(bufoff, (base_) + (kb_) + (h_) * hstep, voffA); } while (0)
; #define PG8_STAGE(bufoff, gbase, voff) do { _Pragma("unroll") for (int _i = 0; _i < 2; ++_i) \
;         __builtin_amdgcn_global_load_lds((const unsigned*)((const char*)(gbase) + (voff)[_i]), (LAS unsigned*)(lds + (bufoff) + ldsw + _i * 8192), 16, 0, 0); } while (0)
; #define PG8_LDA(dst, b, h) do { _Pragma("unroll") for (int m = 0; m < 4; ++m) _Pragma("unroll") for (int k = 0; k < 2; ++k) dst[m][k] = *(const LAS bf16x8*)(lds + PG8_SA(b, h) + aoff + m * 2048 + k * 1024); } while (0)
; #define PG8_LDB(dst, b, h) do { _Pragma("unroll") for (int n = 0; n < 2; ++n) _Pragma("unroll") for (int k = 0; k < 2; ++k) dst[n][k] = *(const LAS bf16x8*)(lds + PG8_SB(b, h) + boff + n * 2048 + k * 1024); } while (0)
; #define PG8_MMA(ai, bj, At, Bt) do { __builtin_amdgcn_s_setprio(1); _Pragma("unroll") for (int m = 0; m < 4; ++m) _Pragma("unroll") for (int n = 0; n < 2; ++n) _Pragma("unroll") for (int k = 0; k < 2; ++k) \
;         acc[ai][bj][m][n] = __builtin_amdgcn_mfma_f32_16x16x32_bf16(Bt[n][k], At[m][k], acc[ai][bj][m][n], 0, 0, 0); __builtin_amdgcn_s_setprio(0); } while (0)
; #define PG8_WAIT_V(n) asm volatile("s_waitcnt vmcnt(" #n ")" ::: "memory")
; #define PG8_WAIT_L(n) asm volatile("s_waitcnt lgkmcnt(" #n ")" ::: "memory")
; #define PG8_BAR __builtin_amdgcn_s_barrier()
; #define PG8_SCHED __builtin_amdgcn_sched_barrier(0)
; template <class Epi, class Sched, bool GATHER = false>
; __device__ __forceinline__ void gemm_phase(LAS unsigned char* lds, const Gemm g, const Sched& S, const Epi& E, const int tid) {
;     ...
;             PG8_WAIT_V(8); PG8_WAIT_L(0); PG8_BAR; PG8_MMA(0, 0, At, B0); PG8_MMA(0, 1, At, B1); PG8_BAR; PG8_SCHED;
;             PG8_LDA(At, 0, 1); PG8_STAGE(PG8_SB(0, 0), b2, voffB); PG8_STAGE(PG8_SB(0, 1), b2 + hstep, voffB); PG8_STAGE_A(PG8_SA(0, 0), (last ? nA : cA), last, kb2, 0);
;             PG8_WAIT_V(8); PG8_WAIT_L(0); PG8_BAR; PG8_MMA(1, 0, At, B0); PG8_MMA(1, 1, At, B1); PG8_BAR; PG8_SCHED;
;             PG8_LDB(B0, 1, 0); PG8_LDB(B1, 1, 1); PG8_SCHED; PG8_LDA(At, 1, 0); PG8_STAGE_A(PG8_SA(0, 1), (last ? nA : cA), last, kb2, 1);
	s_waitcnt lgkmcnt(0)
	v_mfma_f32_16x16x32_bf16 v[90:93], v[158:161], v[190:193], v[90:93]
	v_mfma_f32_16x16x32_bf16 v[18:21], v[166:169], v[190:193], v[18:21]
	v_mfma_f32_16x16x32_bf16 v[6:9], v[158:161], v[202:205], v[6:9]
	v_mfma_f32_16x16x32_bf16 v[22:25], v[166:169], v[202:205], v[22:25]
	v_mfma_f32_16x16x32_bf16 v[10:13], v[158:161], v[210:213], v[10:13]
	v_mfma_f32_16x16x32_bf16 v[26:29], v[166:169], v[210:213], v[26:29]
	v_mfma_f32_16x16x32_bf16 v[14:17], v[158:161], v[218:221], v[14:17]
	v_mfma_f32_16x16x32_bf16 v[30:33], v[166:169], v[218:221], v[30:33]
	v_mfma_f32_16x16x32_bf16 v[90:93], v[162:165], v[194:197], v[90:93]
	v_mfma_f32_16x16x32_bf16 v[18:21], v[170:173], v[194:197], v[18:21]
	v_mfma_f32_16x16x32_bf16 v[6:9], v[162:165], v[206:209], v[6:9]
	v_mfma_f32_16x16x32_bf16 v[22:25], v[170:173], v[206:209], v[22:25]
	v_mfma_f32_16x16x32_bf16 v[10:13], v[162:165], v[214:217], v[10:13]
	v_mfma_f32_16x16x32_bf16 v[26:29], v[170:173], v[214:217], v[26:29]
	v_mfma_f32_16x16x32_bf16 v[14:17], v[162:165], v[222:225], v[14:17]
	v_mfma_f32_16x16x32_bf16 v[30:33], v[170:173], v[222:225], v[30:33]
	v_mfma_f32_16x16x32_bf16 v[34:37], v[174:177], v[190:193], v[34:37]
	v_mfma_f32_16x16x32_bf16 v[50:53], v[182:185], v[190:193], v[50:53]
	v_mfma_f32_16x16x32_bf16 v[38:41], v[174:177], v[202:205], v[38:41]
	v_mfma_f32_16x16x32_bf16 v[54:57], v[182:185], v[202:205], v[54:57]
	v_mfma_f32_16x16x32_bf16 v[42:45], v[174:177], v[210:213], v[42:45]
	v_mfma_f32_16x16x32_bf16 v[62:65], v[182:185], v[210:213], v[62:65]
	v_mfma_f32_16x16x32_bf16 v[46:49], v[174:177], v[218:221], v[46:49]
	v_mfma_f32_16x16x32_bf16 v[70:73], v[182:185], v[218:221], v[70:73]
	v_mfma_f32_16x16x32_bf16 v[34:37], v[178:181], v[194:197], v[34:37]
	v_mfma_f32_16x16x32_bf16 v[50:53], v[186:189], v[194:197], v[50:53]
	v_mfma_f32_16x16x32_bf16 v[38:41], v[178:181], v[206:209], v[38:41]
	v_mfma_f32_16x16x32_bf16 v[54:57], v[186:189], v[206:209], v[54:57]
	v_mfma_f32_16x16x32_bf16 v[42:45], v[178:181], v[214:217], v[42:45]
	v_mfma_f32_16x16x32_bf16 v[62:65], v[186:189], v[214:217], v[62:65]
	v_mfma_f32_16x16x32_bf16 v[46:49], v[178:181], v[222:225], v[46:49]
	v_mfma_f32_16x16x32_bf16 v[70:73], v[186:189], v[222:225], v[70:73]
	s_barrier
	s_mov_b32 m0, s67
	v_lshl_add_u64 v[226:227], v[198:199], 0, v[138:139]
	ds_read_b128 v[190:193], v155 offset:16384
	ds_read_b128 v[194:197], v155 offset:17408
	ds_read_b128 v[202:205], v155 offset:18432
	ds_read_b128 v[206:209], v155 offset:19456
	ds_read_b128 v[210:213], v155 offset:20480
	ds_read_b128 v[214:217], v155 offset:21504
	ds_read_b128 v[218:221], v155 offset:22528
	ds_read_b128 v[222:225], v155 offset:23552
	global_load_lds_dwordx4 v[226:227], off
	v_lshl_add_u64 v[228:229], v[198:199], 0, v[134:135]
	s_mov_b32 m0, s68
	s_cselect_b32 s35, s11, s29
	s_cselect_b32 s34, s10, s28
	v_lshl_add_u64 v[230:231], v[198:199], 0, s[72:73]
	s_add_i32 s65, s65, s48
	global_load_lds_dwordx4 v[228:229], off
	v_lshl_add_u64 v[232:233], v[230:231], 0, v[138:139]
	s_mov_b32 m0, s65
	v_lshl_add_u64 v[230:231], v[230:231], 0, v[134:135]
	global_load_lds_dwordx4 v[232:233], off
	s_add_i32 m0, s65, 0x2000
	s_add_u32 s34, s34, s64
	s_addc_u32 s35, s35, 0
	global_load_lds_dwordx4 v[230:231], off
	v_lshl_add_u64 v[230:231], s[34:35], 0, v[140:141]
	s_mov_b32 m0, s51
	v_lshl_add_u64 v[232:233], s[34:35], 0, v[136:137]
	global_load_lds_dwordx4 v[230:231], off
	s_mov_b32 m0, s52
	s_nop 0
	global_load_lds_dwordx4 v[232:233], off
	s_waitcnt vmcnt(8)
	s_waitcnt lgkmcnt(0)
	s_barrier
	s_waitcnt lgkmcnt(0)
	v_mfma_f32_16x16x32_bf16 v[58:61], v[158:161], v[190:193], v[58:61]
	v_mfma_f32_16x16x32_bf16 v[78:81], v[166:169], v[190:193], v[78:81]
	v_mfma_f32_16x16x32_bf16 v[66:69], v[158:161], v[202:205], v[66:69]
	v_mfma_f32_16x16x32_bf16 v[82:85], v[166:169], v[202:205], v[82:85]
	v_mfma_f32_16x16x32_bf16 v[74:77], v[158:161], v[210:213], v[74:77]
	v_mfma_f32_16x16x32_bf16 v[86:89], v[166:169], v[210:213], v[86:89]
	v_mfma_f32_16x16x32_bf16 v[94:97], v[158:161], v[218:221], v[94:97]
	v_mfma_f32_16x16x32_bf16 v[98:101], v[166:169], v[218:221], v[98:101]
	v_mfma_f32_16x16x32_bf16 v[58:61], v[162:165], v[194:197], v[58:61]
	v_mfma_f32_16x16x32_bf16 v[78:81], v[170:173], v[194:197], v[78:81]
	v_mfma_f32_16x16x32_bf16 v[66:69], v[162:165], v[206:209], v[66:69]
	v_mfma_f32_16x16x32_bf16 v[82:85], v[170:173], v[206:209], v[82:85]
	v_mfma_f32_16x16x32_bf16 v[74:77], v[162:165], v[214:217], v[74:77]
	v_mfma_f32_16x16x32_bf16 v[86:89], v[170:173], v[214:217], v[86:89]
	v_mfma_f32_16x16x32_bf16 v[94:97], v[162:165], v[222:225], v[94:97]
	v_mfma_f32_16x16x32_bf16 v[98:101], v[170:173], v[222:225], v[98:101]
	v_mfma_f32_16x16x32_bf16 v[114:117], v[174:177], v[190:193], v[114:117]
	v_mfma_f32_16x16x32_bf16 v[130:133], v[182:185], v[190:193], v[130:133]
	v_mfma_f32_16x16x32_bf16 v[110:113], v[174:177], v[202:205], v[110:113]
	v_mfma_f32_16x16x32_bf16 v[126:129], v[182:185], v[202:205], v[126:129]
	v_mfma_f32_16x16x32_bf16 v[106:109], v[174:177], v[210:213], v[106:109]
	v_mfma_f32_16x16x32_bf16 v[122:125], v[182:185], v[210:213], v[122:125]
	v_mfma_f32_16x16x32_bf16 v[102:105], v[174:177], v[218:221], v[102:105]
	v_mfma_f32_16x16x32_bf16 v[118:121], v[182:185], v[218:221], v[118:121]
	v_mfma_f32_16x16x32_bf16 v[114:117], v[178:181], v[194:197], v[114:117]
	v_mfma_f32_16x16x32_bf16 v[130:133], v[186:189], v[194:197], v[130:133]
	v_mfma_f32_16x16x32_bf16 v[110:113], v[178:181], v[206:209], v[110:113]
	v_mfma_f32_16x16x32_bf16 v[126:129], v[186:189], v[206:209], v[126:129]
	v_mfma_f32_16x16x32_bf16 v[106:109], v[178:181], v[214:217], v[106:109]
	v_mfma_f32_16x16x32_bf16 v[122:125], v[186:189], v[214:217], v[122:125]
	v_mfma_f32_16x16x32_bf16 v[102:105], v[178:181], v[222:225], v[102:105]
	v_mfma_f32_16x16x32_bf16 v[118:121], v[186:189], v[222:225], v[118:121]
	s_barrier
; #define PG8_STAGE_A(bufoff, base_, nx_, kb_, h_) do { if (GATHER) { if (nx_) PG8_STAGE_G(bufoff, kb_, goN, h_); else PG8_STAGE_G(bufoff, kb_, goC, h_); } \
;         else PG8_STAGE(bufoff, (base_) + (kb_) + (h_) * hstep, voffA); } while (0)
; #define PG8_STAGE(bufoff, gbase, voff) do { _Pragma("unroll") for (int _i = 0; _i < 2; ++_i) \
;         __builtin_amdgcn_global_load_lds((const unsigned*)((const char*)(gbase) + (voff)[_i]), (LAS unsigned*)(lds + (bufoff) + ldsw + _i * 8192), 16, 0, 0); } while (0)
; #define PG8_LDA(dst, b, h) do { _Pragma("unroll") for (int m = 0; m < 4; ++m) _Pragma("unroll") for (int k = 0; k < 2; ++k) dst[m][k] = *(const LAS bf16x8*)(lds + PG8_SA(b, h) + aoff + m * 2048 + k * 1024); } while (0)
; #define PG8_LDB(dst, b, h) do { _Pragma("unroll") for (int n = 0; n < 2; ++n) _Pragma("unroll") for (int k = 0; k < 2; ++k) dst[n][k] = *(const LAS bf16x8*)(lds + PG8_SB(b, h) + boff + n * 2048 + k * 1024); } while (0)
; #define PG8_MMA(ai, bj, At, Bt) do { __builtin_amdgcn_s_setprio(1); _Pragma("unroll") for (int m = 0; m < 4; ++m) _Pragma("unroll") for (int n = 0; n < 2; ++n) _Pragma("unroll") for (int k = 0; k < 2; ++k) \
;         acc[ai][bj][m][n] = __builtin_amdgcn_mfma_f32_16x16x32_bf16(Bt[n][k], At[m][k], acc[ai][bj][m][n], 0, 0, 0); __builtin_amdgcn_s_setprio(0); } while (0)
; #define PG8_WAIT_V(n) asm volatile("s_waitcnt vmcnt(" #n ")" ::: "memory")
; #define PG8_WAIT_L(n) asm volatile("s_waitcnt lgkmcnt(" #n ")" ::: "memory")
; #define PG8_BAR __builtin_amdgcn_s_barrier()
; #define PG8_SCHED __builtin_amdgcn_sched_barrier(0)
; template <class Epi, class Sched, bool GATHER = false>
; __device__ __forceinline__ void gemm_phase(LAS unsigned char* lds, const Gemm g, const Sched& S, const Epi& E, const int tid) {
;     ...
;             PG8_LDB(B0, 1, 0); PG8_LDB(B1, 1, 1); PG8_SCHED; PG8_LDA(At, 1, 0); PG8_STAGE_A(PG8_SA(0, 1), (last ? nA : cA), last, kb2, 1);
;             PG8_WAIT_V(8); PG8_WAIT_L(0); PG8_BAR; PG8_MMA(0, 0, At, B0); PG8_MMA(0, 1, At, B1); PG8_BAR; PG8_SCHED;
;             PG8_LDA(At, 1, 1); PG8_STAGE(PG8_SB(1, 0), b3, voffB); PG8_STAGE(PG8_SB(1, 1), b3 + hstep, voffB); PG8_STAGE_A(PG8_SA(1, 0), (last ? nA : cA), last, kb3, 0);
;             PG8_WAIT_V(8); PG8_WAIT_L(0); PG8_BAR; PG8_MMA(1, 0, At, B0); PG8_MMA(1, 1, At, B1); PG8_BAR; PG8_SCHED;
	s_add_i32 s64, 0, 0x18000
	v_add_u32_e32 v2, s64, v153
	s_add_i32 s65, 0, 0x1c000
	ds_read_b128 v[158:161], v2
	ds_read_b128 v[162:165], v2 offset:1024
	ds_read_b128 v[166:169], v2 offset:2048
	ds_read_b128 v[170:173], v2 offset:3072
	v_add_u32_e32 v2, s65, v153
	ds_read_b128 v[174:177], v2
	ds_read_b128 v[178:181], v2 offset:1024
	ds_read_b128 v[182:185], v2 offset:2048
	ds_read_b128 v[186:189], v2 offset:3072
	s_add_u32 s34, s34, 0xb0000
	s_addc_u32 s35, s35, 0
	s_mov_b32 m0, s53
	v_lshl_add_u64 v[234:235], s[34:35], 0, v[140:141]
	ds_read_b128 v[190:193], v155 offset:32768
	ds_read_b128 v[194:197], v155 offset:33792
	ds_read_b128 v[202:205], v155 offset:34816
	ds_read_b128 v[206:209], v155 offset:35840
	ds_read_b128 v[210:213], v155 offset:36864
	ds_read_b128 v[214:217], v155 offset:37888
	ds_read_b128 v[218:221], v155 offset:38912
	ds_read_b128 v[222:225], v155 offset:39936
	global_load_lds_dwordx4 v[234:235], off
	v_lshl_add_u64 v[234:235], s[34:35], 0, v[136:137]
	s_mov_b32 m0, s54
	s_nop 0
	global_load_lds_dwordx4 v[234:235], off
	s_waitcnt vmcnt(8)
	s_waitcnt lgkmcnt(0)
	s_barrier
	s_waitcnt lgkmcnt(0)
	v_mfma_f32_16x16x32_bf16 v[90:93], v[158:161], v[190:193], v[90:93]
	v_mfma_f32_16x16x32_bf16 v[18:21], v[166:169], v[190:193], v[18:21]
	v_mfma_f32_16x16x32_bf16 v[6:9], v[158:161], v[202:205], v[6:9]
	v_mfma_f32_16x16x32_bf16 v[22:25], v[166:169], v[202:205], v[22:25]
	v_mfma_f32_16x16x32_bf16 v[10:13], v[158:161], v[210:213], v[10:13]
	v_mfma_f32_16x16x32_bf16 v[26:29], v[166:169], v[210:213], v[26:29]
	v_mfma_f32_16x16x32_bf16 v[14:17], v[158:161], v[218:221], v[14:17]
	v_mfma_f32_16x16x32_bf16 v[30:33], v[166:169], v[218:221], v[30:33]
	v_mfma_f32_16x16x32_bf16 v[90:93], v[162:165], v[194:197], v[90:93]
	v_mfma_f32_16x16x32_bf16 v[18:21], v[170:173], v[194:197], v[18:21]
	v_mfma_f32_16x16x32_bf16 v[6:9], v[162:165], v[206:209], v[6:9]
	v_mfma_f32_16x16x32_bf16 v[22:25], v[170:173], v[206:209], v[22:25]
	v_mfma_f32_16x16x32_bf16 v[10:13], v[162:165], v[214:217], v[10:13]
	v_mfma_f32_16x16x32_bf16 v[26:29], v[170:173], v[214:217], v[26:29]
	v_mfma_f32_16x16x32_bf16 v[14:17], v[162:165], v[222:225], v[14:17]
	v_mfma_f32_16x16x32_bf16 v[30:33], v[170:173], v[222:225], v[30:33]
	v_mfma_f32_16x16x32_bf16 v[34:37], v[174:177], v[190:193], v[34:37]
	v_mfma_f32_16x16x32_bf16 v[50:53], v[182:185], v[190:193], v[50:53]
	v_mfma_f32_16x16x32_bf16 v[38:41], v[174:177], v[202:205], v[38:41]
	v_mfma_f32_16x16x32_bf16 v[54:57], v[182:185], v[202:205], v[54:57]
	v_mfma_f32_16x16x32_bf16 v[42:45], v[174:177], v[210:213], v[42:45]
	v_mfma_f32_16x16x32_bf16 v[62:65], v[182:185], v[210:213], v[62:65]
	v_mfma_f32_16x16x32_bf16 v[46:49], v[174:177], v[218:221], v[46:49]
	v_mfma_f32_16x16x32_bf16 v[70:73], v[182:185], v[218:221], v[70:73]
	v_mfma_f32_16x16x32_bf16 v[34:37], v[178:181], v[194:197], v[34:37]
	v_mfma_f32_16x16x32_bf16 v[50:53], v[186:189], v[194:197], v[50:53]
	v_mfma_f32_16x16x32_bf16 v[38:41], v[178:181], v[206:209], v[38:41]
	v_mfma_f32_16x16x32_bf16 v[54:57], v[186:189], v[206:209], v[54:57]
	v_mfma_f32_16x16x32_bf16 v[42:45], v[178:181], v[214:217], v[42:45]
	v_mfma_f32_16x16x32_bf16 v[62:65], v[186:189], v[214:217], v[62:65]
	v_mfma_f32_16x16x32_bf16 v[46:49], v[178:181], v[222:225], v[46:49]
	v_mfma_f32_16x16x32_bf16 v[70:73], v[186:189], v[222:225], v[70:73]
	s_barrier
	s_add_i32 s34, s64, s48
	v_lshl_add_u64 v[226:227], v[226:227], 0, s[0:1]
	s_mov_b32 m0, s34
	ds_read_b128 v[190:193], v155 offset:49152
	ds_read_b128 v[194:197], v155 offset:50176
	ds_read_b128 v[202:205], v155 offset:51200
	ds_read_b128 v[206:209], v155 offset:52224
	ds_read_b128 v[210:213], v155 offset:53248
	ds_read_b128 v[214:217], v155 offset:54272
	ds_read_b128 v[218:221], v155 offset:55296
	ds_read_b128 v[222:225], v155 offset:56320
	global_load_lds_dwordx4 v[226:227], off
	v_lshl_add_u64 v[226:227], v[228:229], 0, s[0:1]
	s_add_i32 m0, s34, 0x2000
	v_lshl_add_u64 v[198:199], v[198:199], 0, s[76:77]
	s_add_i32 s34, s65, s48
	global_load_lds_dwordx4 v[226:227], off
	v_lshl_add_u64 v[226:227], v[198:199], 0, v[138:139]
	s_mov_b32 m0, s34
	v_lshl_add_u64 v[198:199], v[198:199], 0, v[134:135]
	global_load_lds_dwordx4 v[226:227], off
	s_add_i32 m0, s34, 0x2000
	s_nop 0
	global_load_lds_dwordx4 v[198:199], off
	v_lshl_add_u64 v[198:199], v[230:231], 0, s[0:1]
	s_mov_b32 m0, s55
	s_nop 0
	global_load_lds_dwordx4 v[198:199], off
	v_lshl_add_u64 v[198:199], v[232:233], 0, s[0:1]
	s_mov_b32 m0, s56
	s_nop 0
	global_load_lds_dwordx4 v[198:199], off
	s_waitcnt vmcnt(8)
	s_waitcnt lgkmcnt(0)
	s_barrier
	s_waitcnt lgkmcnt(0)
	v_mfma_f32_16x16x32_bf16 v[58:61], v[158:161], v[190:193], v[58:61]
	v_mfma_f32_16x16x32_bf16 v[78:81], v[166:169], v[190:193], v[78:81]
	v_mfma_f32_16x16x32_bf16 v[66:69], v[158:161], v[202:205], v[66:69]
	v_mfma_f32_16x16x32_bf16 v[82:85], v[166:169], v[202:205], v[82:85]
	v_mfma_f32_16x16x32_bf16 v[74:77], v[158:161], v[210:213], v[74:77]
	v_mfma_f32_16x16x32_bf16 v[86:89], v[166:169], v[210:213], v[86:89]
	v_mfma_f32_16x16x32_bf16 v[94:97], v[158:161], v[218:221], v[94:97]
	v_mfma_f32_16x16x32_bf16 v[98:101], v[166:169], v[218:221], v[98:101]
	v_mfma_f32_16x16x32_bf16 v[58:61], v[162:165], v[194:197], v[58:61]
	v_mfma_f32_16x16x32_bf16 v[78:81], v[170:173], v[194:197], v[78:81]
	v_mfma_f32_16x16x32_bf16 v[66:69], v[162:165], v[206:209], v[66:69]
	v_mfma_f32_16x16x32_bf16 v[82:85], v[170:173], v[206:209], v[82:85]
	v_mfma_f32_16x16x32_bf16 v[74:77], v[162:165], v[214:217], v[74:77]
	v_mfma_f32_16x16x32_bf16 v[86:89], v[170:173], v[214:217], v[86:89]
	v_mfma_f32_16x16x32_bf16 v[94:97], v[162:165], v[222:225], v[94:97]
	v_mfma_f32_16x16x32_bf16 v[98:101], v[170:173], v[222:225], v[98:101]
	v_mfma_f32_16x16x32_bf16 v[114:117], v[174:177], v[190:193], v[114:117]
	v_mfma_f32_16x16x32_bf16 v[130:133], v[182:185], v[190:193], v[130:133]
	v_mfma_f32_16x16x32_bf16 v[110:113], v[174:177], v[202:205], v[110:113]
	v_mfma_f32_16x16x32_bf16 v[126:129], v[182:185], v[202:205], v[126:129]
	v_mfma_f32_16x16x32_bf16 v[106:109], v[174:177], v[210:213], v[106:109]
	v_mfma_f32_16x16x32_bf16 v[122:125], v[182:185], v[210:213], v[122:125]
	v_mfma_f32_16x16x32_bf16 v[102:105], v[174:177], v[218:221], v[102:105]
	v_mfma_f32_16x16x32_bf16 v[118:121], v[182:185], v[218:221], v[118:121]
	v_mfma_f32_16x16x32_bf16 v[114:117], v[178:181], v[194:197], v[114:117]
	v_mfma_f32_16x16x32_bf16 v[130:133], v[186:189], v[194:197], v[130:133]
	v_mfma_f32_16x16x32_bf16 v[110:113], v[178:181], v[206:209], v[110:113]
	v_mfma_f32_16x16x32_bf16 v[126:129], v[186:189], v[206:209], v[126:129]
	v_mfma_f32_16x16x32_bf16 v[106:109], v[178:181], v[214:217], v[106:109]
	v_mfma_f32_16x16x32_bf16 v[122:125], v[186:189], v[214:217], v[122:125]
	v_mfma_f32_16x16x32_bf16 v[102:105], v[178:181], v[222:225], v[102:105]
	v_mfma_f32_16x16x32_bf16 v[118:121], v[186:189], v[222:225], v[118:121]
	s_barrier
	s_add_i32 s63, s63, 2
	s_cmp_gt_u32 s63, 41
	s_mov_b64 s[34:35], s[30:31]
	s_cbranch_scc0 .LBB0_1505

; __device__ __forceinline__ unsigned cvt_pk_bf16(float lo, float hi) { const f32x2 v = {lo, hi}; const bf16x2_t b = __builtin_convertvector(v, bf16x2_t); return __builtin_bit_cast(unsigned, b); }
; #define ZERO4() ((f32x4){opaque0(), 0.f, 0.f, 0.f} * 0.f)
; #define PG8_BAR __builtin_amdgcn_s_barrier()
;     __device__ __forceinline__ void operator()(const f32x4 (&acc)[2][2][4][2], const Unit& u, int wr, int wc, int fr, int fq) const {
;         const int row0 = u.pm * BM + wr * 64 + fr, col0 = u.pn * BM + wc * 32 + 8 * fq;
; #pragma unroll
;         for (int ai = 0; ai < 2; ++ai)
; #pragma unroll
;             for (int m = 0; m < 4; ++m) { bf16_t* rowp = O + (size_t)(row0 + ai * HALF + m * 16) * ldc + col0;
; #pragma unroll
;                 for (int bj = 0; bj < 2; ++bj) { const f32x4 v0 = acc[ai][bj][m][0], v1 = acc[ai][bj][m][1];
;                     u32x4 w; w.x = cvt_pk_bf16(v0[0], v0[1]); w.y = cvt_pk_bf16(v0[2], v0[3]); w.z = cvt_pk_bf16(v1[0], v1[1]); w.w = cvt_pk_bf16(v1[2], v1[3]);
;                     *(u32x4*)(rowp + bj * HALF) = w; } }
;     }
; template <class Epi, class Sched, bool GATHER = false>
; __device__ __forceinline__ void gemm_phase(LAS unsigned char* lds, const Gemm g, const Sched& S, const Epi& E, const int tid) {
;     ...
;         if (!has_next) break;
; #pragma unroll
;         for (int a = 0; a < 2; ++a)
; #pragma unroll
;             for (int b = 0; b < 2; ++b)
; #pragma unroll
;                 for (int m = 0; m < 4; ++m)
; #pragma unroll
;                     for (int n = 0; n < 2; ++n) acc[a][b][m][n] = ZERO4();
;         cur = nxt; cA = nA; cB = nB; ++ui;
;         if (GATHER) {
; #pragma unroll
;             for (int h_ = 0; h_ < 2; ++h_) { goC[h_][0] = goN[h_][0]; goC[h_][1] = goN[h_][1]; } }
;         if (wr == 1) PG8_BAR;
.LBB0_1508:
	v_lshl_or_b32 v4, s59, 8, v154
	v_lshl_add_u32 v2, s60, 8, v152
	v_ashrrev_i32_e32 v5, 31, v4
	v_mov_b64_e32 v[148:149], s[16:17]
	s_movk_i32 s30, 0x1080
	v_mad_i64_i32 v[150:151], s[28:29], v2, s30, v[148:149]
	v_lshlrev_b64 v[158:159], 1, v[4:5]
	v_lshl_add_u64 v[4:5], v[150:151], 0, v[158:159]
	v_cvt_pk_bf16_f32 v90, v90, v91
	v_cvt_pk_bf16_f32 v91, v92, v93
	v_cvt_pk_bf16_f32 v92, v18, v19
	v_cvt_pk_bf16_f32 v93, v20, v21
	v_cvt_pk_bf16_f32 v18, v34, v35
	v_cvt_pk_bf16_f32 v19, v36, v37
	v_cvt_pk_bf16_f32 v20, v50, v51
	v_cvt_pk_bf16_f32 v21, v52, v53
	global_store_dwordx4 v[4:5], v[90:93], off
	global_store_dwordx4 v[4:5], v[18:21], off offset:256
	v_or_b32_e32 v4, 16, v2
	v_mad_i64_i32 v[4:5], s[28:29], v4, s30, v[148:149]
	v_lshl_add_u64 v[18:19], v[4:5], 0, v[158:159]
	v_cvt_pk_bf16_f32 v4, v6, v7
	v_cvt_pk_bf16_f32 v5, v8, v9
	v_cvt_pk_bf16_f32 v6, v22, v23
	v_cvt_pk_bf16_f32 v7, v24, v25
	global_store_dwordx4 v[18:19], v[4:7], off
	s_and_b64 vcc, exec, s[8:9]
	s_mov_b64 s[8:9], -1
	v_cvt_pk_bf16_f32 v4, v38, v39
	v_cvt_pk_bf16_f32 v5, v40, v41
	v_cvt_pk_bf16_f32 v6, v54, v55
	v_cvt_pk_bf16_f32 v7, v56, v57
	global_store_dwordx4 v[18:19], v[4:7], off offset:256
	s_movk_i32 s68, 0x1730
	s_movk_i32 s67, 0x90
	v_or_b32_e32 v4, 32, v2
	v_mad_i64_i32 v[4:5], s[28:29], v4, s30, v[148:149]
	v_lshl_add_u64 v[8:9], v[4:5], 0, v[158:159]
	v_cvt_pk_bf16_f32 v4, v10, v11
	v_cvt_pk_bf16_f32 v5, v12, v13
	v_cvt_pk_bf16_f32 v6, v26, v27
	v_cvt_pk_bf16_f32 v7, v28, v29
	global_store_dwordx4 v[8:9], v[4:7], off
	s_mov_b32 s65, 0x800000
	s_nop 0
	v_cvt_pk_bf16_f32 v4, v42, v43
	v_cvt_pk_bf16_f32 v5, v44, v45
	v_cvt_pk_bf16_f32 v6, v62, v63
	v_cvt_pk_bf16_f32 v7, v64, v65
	global_store_dwordx4 v[8:9], v[4:7], off offset:256
	s_nop 1
	v_or_b32_e32 v4, 48, v2
	v_mad_i64_i32 v[4:5], s[28:29], v4, s30, v[148:149]
	v_lshl_add_u64 v[8:9], v[4:5], 0, v[158:159]
	v_cvt_pk_bf16_f32 v4, v14, v15
	v_cvt_pk_bf16_f32 v5, v16, v17
	v_cvt_pk_bf16_f32 v6, v30, v31
	v_cvt_pk_bf16_f32 v7, v32, v33
	global_store_dwordx4 v[8:9], v[4:7], off
	s_nop 1
	v_cvt_pk_bf16_f32 v4, v46, v47
	v_cvt_pk_bf16_f32 v5, v48, v49
	v_cvt_pk_bf16_f32 v6, v70, v71
	v_cvt_pk_bf16_f32 v7, v72, v73
	global_store_dwordx4 v[8:9], v[4:7], off offset:256
	s_nop 1
	v_add_u32_e32 v4, 0x80, v2
	v_mad_i64_i32 v[4:5], s[28:29], v4, s30, v[148:149]
	v_lshl_add_u64 v[8:9], v[4:5], 0, v[158:159]
	v_cvt_pk_bf16_f32 v4, v58, v59
	v_cvt_pk_bf16_f32 v5, v60, v61
	v_cvt_pk_bf16_f32 v6, v78, v79
	v_cvt_pk_bf16_f32 v7, v80, v81
	global_store_dwordx4 v[8:9], v[4:7], off
	s_nop 1
	v_cvt_pk_bf16_f32 v4, v114, v115
	v_cvt_pk_bf16_f32 v5, v116, v117
	v_cvt_pk_bf16_f32 v6, v130, v131
	v_cvt_pk_bf16_f32 v7, v132, v133
	global_store_dwordx4 v[8:9], v[4:7], off offset:256
	s_nop 1
	v_add_u32_e32 v4, 0x90, v2
	v_mad_i64_i32 v[4:5], s[28:29], v4, s30, v[148:149]
	v_lshl_add_u64 v[8:9], v[4:5], 0, v[158:159]
	v_cvt_pk_bf16_f32 v4, v66, v67
	v_cvt_pk_bf16_f32 v5, v68, v69
	v_cvt_pk_bf16_f32 v6, v82, v83
	v_cvt_pk_bf16_f32 v7, v84, v85
	global_store_dwordx4 v[8:9], v[4:7], off
	s_nop 1
	v_cvt_pk_bf16_f32 v4, v110, v111
	v_cvt_pk_bf16_f32 v5, v112, v113
	v_cvt_pk_bf16_f32 v6, v126, v127
	v_cvt_pk_bf16_f32 v7, v128, v129
	global_store_dwordx4 v[8:9], v[4:7], off offset:256
	s_nop 1
	v_add_u32_e32 v4, 0xa0, v2
	v_mad_i64_i32 v[4:5], s[28:29], v4, s30, v[148:149]
	v_lshl_add_u64 v[8:9], v[4:5], 0, v[158:159]
	v_cvt_pk_bf16_f32 v4, v74, v75
	v_cvt_pk_bf16_f32 v5, v76, v77
	v_cvt_pk_bf16_f32 v6, v86, v87
	v_cvt_pk_bf16_f32 v7, v88, v89
	global_store_dwordx4 v[8:9], v[4:7], off
	v_add_u32_e32 v2, 0xb0, v2
	s_nop 0
	v_cvt_pk_bf16_f32 v4, v106, v107
	v_cvt_pk_bf16_f32 v5, v108, v109
	v_cvt_pk_bf16_f32 v6, v122, v123
	v_cvt_pk_bf16_f32 v7, v124, v125
	global_store_dwordx4 v[8:9], v[4:7], off offset:256
	s_nop 1
	v_mad_i64_i32 v[4:5], s[28:29], v2, s30, v[148:149]
	v_lshl_add_u64 v[8:9], v[4:5], 0, v[158:159]
	v_cvt_pk_bf16_f32 v4, v94, v95
	v_cvt_pk_bf16_f32 v5, v96, v97
	v_cvt_pk_bf16_f32 v6, v98, v99
	v_cvt_pk_bf16_f32 v7, v100, v101
	global_store_dwordx4 v[8:9], v[4:7], off
	s_nop 1
	v_cvt_pk_bf16_f32 v4, v102, v103
	v_cvt_pk_bf16_f32 v5, v104, v105
	v_cvt_pk_bf16_f32 v6, v118, v119
	v_cvt_pk_bf16_f32 v7, v120, v121
	global_store_dwordx4 v[8:9], v[4:7], off offset:256
	s_cbranch_vccnz .LBB0_1497
	v_mov_b32_e32 v2, v3
	s_andn2_b64 vcc, exec, s[14:15]
	s_cbranch_vccnz .LBB0_1496
	s_barrier
	s_branch .LBB0_1496
